# v68 + closing barrier of each compute segment issued before its last MFMA
# baseline (speedup 1.0000x reference)
.LBB0_286:
	s_lshl_b32 s10, s51, 19
	s_add_u32 s10, s20, s10
	s_addc_u32 s11, s21, 0
	s_and_b64 s[16:17], s[4:5], exec
	s_cselect_b32 s54, s11, s31
	s_cselect_b32 s55, s10, s30
	s_lshl_b32 s14, s50, 19
	s_add_u32 s16, s15, s14
	s_addc_u32 s17, s26, 0
	s_and_b64 s[36:37], s[4:5], exec
	s_cselect_b32 s56, s17, s23
	s_cselect_b32 s57, s16, s22
	s_add_i32 s60, 0, 0x10000
	v_add_u32_e32 v198, s60, v196
	s_add_i32 s62, 0, 0x14000
	v_add_u32_e32 v199, s62, v196
	ds_read_b128 v[160:163], v198
	ds_read_b128 v[152:155], v198 offset:1024
	ds_read_b128 v[156:159], v198 offset:2048
	ds_read_b128 v[148:151], v198 offset:3072
	ds_read_b128 v[144:147], v199
	ds_read_b128 v[136:139], v199 offset:1024
	ds_read_b128 v[140:143], v199 offset:2048
	ds_read_b128 v[132:135], v199 offset:3072
	s_add_u32 s36, s30, 0x40080
	s_addc_u32 s37, s31, 0
	s_add_i32 s58, s41, 0xc000
	v_lshl_add_u64 v[174:175], s[36:37], 0, v[168:169]
	s_mov_b32 m0, s58
	s_add_i32 s59, s41, 0xe000
	ds_read_b128 v[178:181], v197
	ds_read_b128 v[182:185], v197 offset:1024
	ds_read_b128 v[190:193], v197 offset:2048
	ds_read_b128 v[200:203], v197 offset:3072
	ds_read_b128 v[204:207], v197 offset:4096
	ds_read_b128 v[208:211], v197 offset:5120
	ds_read_b128 v[212:215], v197 offset:6144
	ds_read_b128 v[216:219], v197 offset:7168
	global_load_lds_dwordx4 v[174:175], off
	v_lshl_add_u64 v[174:175], s[36:37], 0, v[166:167]
	s_mov_b32 m0, s59
	s_nop 0
	global_load_lds_dwordx4 v[174:175], off
	s_waitcnt vmcnt(8)
	s_waitcnt lgkmcnt(0)
	s_barrier
	v_mfma_f32_16x16x32_bf16 v[128:131], v[160:163], v[178:181], 0
	s_setprio 1
	v_mfma_f32_16x16x32_bf16 v[124:127], v[156:159], v[178:181], 0
	v_mfma_f32_16x16x32_bf16 v[116:119], v[156:159], v[190:193], 0
	v_mfma_f32_16x16x32_bf16 v[120:123], v[160:163], v[190:193], 0
	v_mfma_f32_16x16x32_bf16 v[112:115], v[160:163], v[204:207], 0
	v_mfma_f32_16x16x32_bf16 v[108:111], v[156:159], v[204:207], 0
	v_mfma_f32_16x16x32_bf16 v[100:103], v[156:159], v[212:215], 0
	v_mfma_f32_16x16x32_bf16 v[104:107], v[160:163], v[212:215], 0
	s_nop 0
	v_mfma_f32_16x16x32_bf16 v[128:131], v[152:155], v[182:185], v[128:131]
	v_mfma_f32_16x16x32_bf16 v[124:127], v[148:151], v[182:185], v[124:127]
	v_mfma_f32_16x16x32_bf16 v[116:119], v[148:151], v[200:203], v[116:119]
	v_mfma_f32_16x16x32_bf16 v[120:123], v[152:155], v[200:203], v[120:123]
	v_mfma_f32_16x16x32_bf16 v[112:115], v[152:155], v[208:211], v[112:115]
	v_mfma_f32_16x16x32_bf16 v[108:111], v[148:151], v[208:211], v[108:111]
	v_mfma_f32_16x16x32_bf16 v[100:103], v[148:151], v[216:219], v[100:103]
	v_mfma_f32_16x16x32_bf16 v[104:107], v[152:155], v[216:219], v[104:107]
	s_setprio 0
	s_setprio 1
	v_mfma_f32_16x16x32_bf16 v[96:99], v[144:147], v[178:181], 0
	v_mfma_f32_16x16x32_bf16 v[92:95], v[140:143], v[178:181], 0
	v_mfma_f32_16x16x32_bf16 v[84:87], v[140:143], v[190:193], 0
	v_mfma_f32_16x16x32_bf16 v[88:91], v[144:147], v[190:193], 0
	v_mfma_f32_16x16x32_bf16 v[80:83], v[144:147], v[204:207], 0
	v_mfma_f32_16x16x32_bf16 v[76:79], v[140:143], v[204:207], 0
	v_mfma_f32_16x16x32_bf16 v[68:71], v[140:143], v[212:215], 0
	v_mfma_f32_16x16x32_bf16 v[72:75], v[144:147], v[212:215], 0
	s_nop 0
	v_mfma_f32_16x16x32_bf16 v[96:99], v[136:139], v[182:185], v[96:99]
	v_mfma_f32_16x16x32_bf16 v[92:95], v[132:135], v[182:185], v[92:95]
	v_mfma_f32_16x16x32_bf16 v[84:87], v[132:135], v[200:203], v[84:87]
	v_mfma_f32_16x16x32_bf16 v[88:91], v[136:139], v[200:203], v[88:91]
	v_mfma_f32_16x16x32_bf16 v[80:83], v[136:139], v[208:211], v[80:83]
	v_mfma_f32_16x16x32_bf16 v[76:79], v[132:135], v[208:211], v[76:79]
	v_mfma_f32_16x16x32_bf16 v[68:71], v[132:135], v[216:219], v[68:71]
	s_barrier
	v_mfma_f32_16x16x32_bf16 v[72:75], v[136:139], v[216:219], v[72:75]
	s_setprio 0
	v_lshl_add_u64 v[174:175], s[22:23], 0, v[34:35]
	s_add_i32 s60, s60, s40
	v_lshl_add_u64 v[190:191], v[174:175], 0, s[28:29]
	s_mov_b32 m0, s60
	s_add_i32 s61, s60, 0x2000
	ds_read_b128 v[178:181], v197 offset:16384
	ds_read_b128 v[182:185], v197 offset:17408
	ds_read_b128 v[200:203], v197 offset:18432
	ds_read_b128 v[204:207], v197 offset:19456
	ds_read_b128 v[208:211], v197 offset:20480
	ds_read_b128 v[212:215], v197 offset:21504
	ds_read_b128 v[216:219], v197 offset:22528
	ds_read_b128 v[222:225], v197 offset:23552
	global_load_lds_dwordx4 v[190:191], off
	v_lshl_add_u64 v[190:191], s[22:23], 0, v[164:165]
	s_add_u32 s36, s22, 0x40100
	v_lshl_add_u64 v[192:193], v[190:191], 0, s[28:29]
	s_mov_b32 m0, s61
	s_addc_u32 s37, s23, 0
	s_add_i32 s62, s62, s40
	global_load_lds_dwordx4 v[192:193], off
	v_lshl_add_u64 v[192:193], s[36:37], 0, v[34:35]
	s_mov_b32 m0, s62
	s_add_i32 s63, s62, 0x2000
	global_load_lds_dwordx4 v[192:193], off
	v_lshl_add_u64 v[192:193], s[36:37], 0, v[164:165]
	s_mov_b32 m0, s63
	s_nop 0
	global_load_lds_dwordx4 v[192:193], off
	v_lshl_add_u64 v[192:193], s[30:31], 0, v[168:169]
	v_lshl_add_u64 v[194:195], v[192:193], 0, s[28:29]
	s_mov_b32 m0, s41
	s_nop 0
	global_load_lds_dwordx4 v[194:195], off
	v_lshl_add_u64 v[194:195], s[30:31], 0, v[166:167]
	v_lshl_add_u64 v[226:227], v[194:195], 0, s[28:29]
	s_mov_b32 m0, s42
	s_nop 0
	global_load_lds_dwordx4 v[226:227], off
	s_waitcnt vmcnt(8)
	s_waitcnt lgkmcnt(0)
	s_barrier
	v_mfma_f32_16x16x32_bf16 v[64:67], v[160:163], v[178:181], 0
	s_setprio 1
	v_mfma_f32_16x16x32_bf16 v[60:63], v[156:159], v[178:181], 0
	v_mfma_f32_16x16x32_bf16 v[52:55], v[156:159], v[200:203], 0
	v_mfma_f32_16x16x32_bf16 v[56:59], v[160:163], v[200:203], 0
	v_mfma_f32_16x16x32_bf16 v[48:51], v[160:163], v[208:211], 0
	v_mfma_f32_16x16x32_bf16 v[44:47], v[156:159], v[208:211], 0
	v_mfma_f32_16x16x32_bf16 v[36:39], v[156:159], v[216:219], 0
	v_mfma_f32_16x16x32_bf16 v[40:43], v[160:163], v[216:219], 0
	s_nop 0
	v_mfma_f32_16x16x32_bf16 v[64:67], v[152:155], v[182:185], v[64:67]
	v_mfma_f32_16x16x32_bf16 v[60:63], v[148:151], v[182:185], v[60:63]
	v_mfma_f32_16x16x32_bf16 v[52:55], v[148:151], v[204:207], v[52:55]
	v_mfma_f32_16x16x32_bf16 v[56:59], v[152:155], v[204:207], v[56:59]
	v_mfma_f32_16x16x32_bf16 v[48:51], v[152:155], v[212:215], v[48:51]
	v_mfma_f32_16x16x32_bf16 v[44:47], v[148:151], v[212:215], v[44:47]
	v_mfma_f32_16x16x32_bf16 v[36:39], v[148:151], v[222:225], v[36:39]
	v_mfma_f32_16x16x32_bf16 v[40:43], v[152:155], v[222:225], v[40:43]
	s_setprio 0
	s_setprio 1
	v_mfma_f32_16x16x32_bf16 v[30:33], v[144:147], v[178:181], 0
	v_mfma_f32_16x16x32_bf16 v[26:29], v[140:143], v[178:181], 0
	v_mfma_f32_16x16x32_bf16 v[18:21], v[140:143], v[200:203], 0
	v_mfma_f32_16x16x32_bf16 v[22:25], v[144:147], v[200:203], 0
	v_mfma_f32_16x16x32_bf16 v[14:17], v[144:147], v[208:211], 0
	v_mfma_f32_16x16x32_bf16 v[10:13], v[140:143], v[208:211], 0
	v_mfma_f32_16x16x32_bf16 v[2:5], v[140:143], v[216:219], 0
	v_mfma_f32_16x16x32_bf16 v[6:9], v[144:147], v[216:219], 0
	s_nop 0
	v_mfma_f32_16x16x32_bf16 v[30:33], v[136:139], v[182:185], v[30:33]
	v_mfma_f32_16x16x32_bf16 v[26:29], v[132:135], v[182:185], v[26:29]
	v_mfma_f32_16x16x32_bf16 v[18:21], v[132:135], v[204:207], v[18:21]
	v_mfma_f32_16x16x32_bf16 v[22:25], v[136:139], v[204:207], v[22:25]
	v_mfma_f32_16x16x32_bf16 v[14:17], v[136:139], v[212:215], v[14:17]
	v_mfma_f32_16x16x32_bf16 v[10:13], v[132:135], v[212:215], v[10:13]
	v_mfma_f32_16x16x32_bf16 v[2:5], v[132:135], v[222:225], v[2:5]
	s_barrier
	v_mfma_f32_16x16x32_bf16 v[6:9], v[136:139], v[222:225], v[6:9]
	s_setprio 0
	s_add_i32 s64, 0, 0x18000
	s_add_i32 s66, 0, 0x1c000
	v_add_u32_e32 v132, s64, v196
	v_add_u32_e32 v133, s66, v196
	ds_read_b128 v[134:137], v132
	ds_read_b128 v[138:141], v132 offset:1024
	ds_read_b128 v[142:145], v132 offset:2048
	ds_read_b128 v[146:149], v132 offset:3072
	ds_read_b128 v[150:153], v133
	ds_read_b128 v[154:157], v133 offset:1024
	ds_read_b128 v[158:161], v133 offset:2048
	ds_read_b128 v[178:181], v133 offset:3072
	s_add_u32 s36, s30, 0x40100
	s_addc_u32 s37, s31, 0
	s_mov_b32 m0, s43
	v_lshl_add_u64 v[162:163], s[36:37], 0, v[168:169]
	ds_read_b128 v[182:185], v197 offset:32768
	ds_read_b128 v[200:203], v197 offset:33792
	ds_read_b128 v[204:207], v197 offset:34816
	ds_read_b128 v[208:211], v197 offset:35840
	ds_read_b128 v[212:215], v197 offset:36864
	ds_read_b128 v[216:219], v197 offset:37888
	ds_read_b128 v[222:225], v197 offset:38912
	ds_read_b128 v[226:229], v197 offset:39936
	global_load_lds_dwordx4 v[162:163], off
	v_lshl_add_u64 v[162:163], s[36:37], 0, v[166:167]
	s_mov_b32 m0, s44
	s_nop 0
	global_load_lds_dwordx4 v[162:163], off
	s_waitcnt vmcnt(8)
	s_waitcnt lgkmcnt(0)
	s_barrier
	v_mfma_f32_16x16x32_bf16 v[128:131], v[134:137], v[182:185], v[128:131]
	s_setprio 1
	v_mfma_f32_16x16x32_bf16 v[124:127], v[142:145], v[182:185], v[124:127]
	v_mfma_f32_16x16x32_bf16 v[116:119], v[142:145], v[204:207], v[116:119]
	v_mfma_f32_16x16x32_bf16 v[120:123], v[134:137], v[204:207], v[120:123]
	v_mfma_f32_16x16x32_bf16 v[112:115], v[134:137], v[212:215], v[112:115]
	v_mfma_f32_16x16x32_bf16 v[108:111], v[142:145], v[212:215], v[108:111]
	v_mfma_f32_16x16x32_bf16 v[100:103], v[142:145], v[222:225], v[100:103]
	v_mfma_f32_16x16x32_bf16 v[104:107], v[134:137], v[222:225], v[104:107]
	v_mfma_f32_16x16x32_bf16 v[128:131], v[138:141], v[200:203], v[128:131]
	v_mfma_f32_16x16x32_bf16 v[124:127], v[146:149], v[200:203], v[124:127]
	v_mfma_f32_16x16x32_bf16 v[116:119], v[146:149], v[208:211], v[116:119]
	v_mfma_f32_16x16x32_bf16 v[120:123], v[138:141], v[208:211], v[120:123]
	v_mfma_f32_16x16x32_bf16 v[112:115], v[138:141], v[216:219], v[112:115]
	v_mfma_f32_16x16x32_bf16 v[108:111], v[146:149], v[216:219], v[108:111]
	v_mfma_f32_16x16x32_bf16 v[100:103], v[146:149], v[226:229], v[100:103]
	v_mfma_f32_16x16x32_bf16 v[104:107], v[138:141], v[226:229], v[104:107]
	s_setprio 0
	s_setprio 1
	v_mfma_f32_16x16x32_bf16 v[96:99], v[150:153], v[182:185], v[96:99]
	v_mfma_f32_16x16x32_bf16 v[92:95], v[158:161], v[182:185], v[92:95]
	v_mfma_f32_16x16x32_bf16 v[84:87], v[158:161], v[204:207], v[84:87]
	v_mfma_f32_16x16x32_bf16 v[88:91], v[150:153], v[204:207], v[88:91]
	v_mfma_f32_16x16x32_bf16 v[80:83], v[150:153], v[212:215], v[80:83]
	v_mfma_f32_16x16x32_bf16 v[76:79], v[158:161], v[212:215], v[76:79]
	v_mfma_f32_16x16x32_bf16 v[68:71], v[158:161], v[222:225], v[68:71]
	v_mfma_f32_16x16x32_bf16 v[72:75], v[150:153], v[222:225], v[72:75]
	v_mfma_f32_16x16x32_bf16 v[96:99], v[154:157], v[200:203], v[96:99]
	v_mfma_f32_16x16x32_bf16 v[92:95], v[178:181], v[200:203], v[92:95]
	v_mfma_f32_16x16x32_bf16 v[84:87], v[178:181], v[208:211], v[84:87]
	v_mfma_f32_16x16x32_bf16 v[88:91], v[154:157], v[208:211], v[88:91]
	v_mfma_f32_16x16x32_bf16 v[80:83], v[154:157], v[216:219], v[80:83]
	v_mfma_f32_16x16x32_bf16 v[76:79], v[178:181], v[216:219], v[76:79]
	v_mfma_f32_16x16x32_bf16 v[68:71], v[178:181], v[226:229], v[68:71]
	s_barrier
	v_mfma_f32_16x16x32_bf16 v[72:75], v[154:157], v[226:229], v[72:75]
	s_setprio 0
	s_add_i32 s64, s64, s40
	s_mov_b64 s[24:25], 0x180
	s_add_i32 s65, s64, 0x2000
	v_lshl_add_u64 v[162:163], v[174:175], 0, s[24:25]
	s_mov_b32 m0, s64
	s_add_u32 s36, s22, 0x40180
	ds_read_b128 v[182:185], v197 offset:49152
	ds_read_b128 v[200:203], v197 offset:50176
	ds_read_b128 v[204:207], v197 offset:51200
	ds_read_b128 v[208:211], v197 offset:52224
	ds_read_b128 v[212:215], v197 offset:53248
	ds_read_b128 v[216:219], v197 offset:54272
	ds_read_b128 v[222:225], v197 offset:55296
	ds_read_b128 v[226:229], v197 offset:56320
	global_load_lds_dwordx4 v[162:163], off
	v_lshl_add_u64 v[162:163], v[190:191], 0, s[24:25]
	s_mov_b32 m0, s65
	s_addc_u32 s37, s23, 0
	s_add_i32 s66, s66, s40
	global_load_lds_dwordx4 v[162:163], off
	v_lshl_add_u64 v[162:163], s[36:37], 0, v[34:35]
	s_mov_b32 m0, s66
	s_add_i32 s67, s66, 0x2000
	global_load_lds_dwordx4 v[162:163], off
	v_lshl_add_u64 v[162:163], s[36:37], 0, v[164:165]
	s_mov_b32 m0, s67
	s_nop 0
	global_load_lds_dwordx4 v[162:163], off
	v_lshl_add_u64 v[162:163], v[192:193], 0, s[24:25]
	s_mov_b32 m0, s47
	s_nop 0
	global_load_lds_dwordx4 v[162:163], off
	v_lshl_add_u64 v[162:163], v[194:195], 0, s[24:25]
	s_mov_b32 m0, s48
	s_nop 0
	global_load_lds_dwordx4 v[162:163], off
	s_waitcnt vmcnt(8)
	s_waitcnt lgkmcnt(0)
	s_barrier
	v_mfma_f32_16x16x32_bf16 v[64:67], v[134:137], v[182:185], v[64:67]
	s_setprio 1
	v_mfma_f32_16x16x32_bf16 v[60:63], v[142:145], v[182:185], v[60:63]
	v_mfma_f32_16x16x32_bf16 v[52:55], v[142:145], v[204:207], v[52:55]
	v_mfma_f32_16x16x32_bf16 v[56:59], v[134:137], v[204:207], v[56:59]
	v_mfma_f32_16x16x32_bf16 v[48:51], v[134:137], v[212:215], v[48:51]
	v_mfma_f32_16x16x32_bf16 v[44:47], v[142:145], v[212:215], v[44:47]
	v_mfma_f32_16x16x32_bf16 v[36:39], v[142:145], v[222:225], v[36:39]
	v_mfma_f32_16x16x32_bf16 v[40:43], v[134:137], v[222:225], v[40:43]
	v_mfma_f32_16x16x32_bf16 v[64:67], v[138:141], v[200:203], v[64:67]
	v_mfma_f32_16x16x32_bf16 v[60:63], v[146:149], v[200:203], v[60:63]
	v_mfma_f32_16x16x32_bf16 v[52:55], v[146:149], v[208:211], v[52:55]
	v_mfma_f32_16x16x32_bf16 v[56:59], v[138:141], v[208:211], v[56:59]
	v_mfma_f32_16x16x32_bf16 v[48:51], v[138:141], v[216:219], v[48:51]
	v_mfma_f32_16x16x32_bf16 v[44:47], v[146:149], v[216:219], v[44:47]
	v_mfma_f32_16x16x32_bf16 v[36:39], v[146:149], v[226:229], v[36:39]
	v_mfma_f32_16x16x32_bf16 v[40:43], v[138:141], v[226:229], v[40:43]
	s_setprio 0
	s_setprio 1
	v_mfma_f32_16x16x32_bf16 v[30:33], v[150:153], v[182:185], v[30:33]
	v_mfma_f32_16x16x32_bf16 v[26:29], v[158:161], v[182:185], v[26:29]
	v_mfma_f32_16x16x32_bf16 v[18:21], v[158:161], v[204:207], v[18:21]
	v_mfma_f32_16x16x32_bf16 v[22:25], v[150:153], v[204:207], v[22:25]
	v_mfma_f32_16x16x32_bf16 v[14:17], v[150:153], v[212:215], v[14:17]
	v_mfma_f32_16x16x32_bf16 v[10:13], v[158:161], v[212:215], v[10:13]
	v_mfma_f32_16x16x32_bf16 v[2:5], v[158:161], v[222:225], v[2:5]
	v_mfma_f32_16x16x32_bf16 v[6:9], v[150:153], v[222:225], v[6:9]
	v_mfma_f32_16x16x32_bf16 v[30:33], v[154:157], v[200:203], v[30:33]
	v_mfma_f32_16x16x32_bf16 v[26:29], v[178:181], v[200:203], v[26:29]
	v_mfma_f32_16x16x32_bf16 v[18:21], v[178:181], v[208:211], v[18:21]
	v_mfma_f32_16x16x32_bf16 v[22:25], v[154:157], v[208:211], v[22:25]
	v_mfma_f32_16x16x32_bf16 v[14:17], v[154:157], v[216:219], v[14:17]
	v_mfma_f32_16x16x32_bf16 v[10:13], v[178:181], v[216:219], v[10:13]
	v_mfma_f32_16x16x32_bf16 v[2:5], v[178:181], v[226:229], v[2:5]
	s_barrier
	v_mfma_f32_16x16x32_bf16 v[6:9], v[154:157], v[226:229], v[6:9]
	s_setprio 0
	s_add_u32 s30, s30, 0x40180
	s_addc_u32 s31, s31, 0
	s_add_u32 s68, s22, 0x200
	s_addc_u32 s69, s23, 0
	s_mov_b32 s70, 0
.LBB0_287:
	ds_read_b128 v[134:137], v198
	ds_read_b128 v[138:141], v198 offset:1024
	ds_read_b128 v[142:145], v198 offset:2048
	ds_read_b128 v[146:149], v198 offset:3072
	ds_read_b128 v[150:153], v199
	ds_read_b128 v[154:157], v199 offset:1024
	ds_read_b128 v[158:161], v199 offset:2048
	ds_read_b128 v[178:181], v199 offset:3072
	s_add_u32 s14, s30, 0xfffc0080
	s_addc_u32 s22, s31, -1
	s_cmp_eq_u32 s70, 12
	s_cselect_b32 s37, s54, s22
	s_cselect_b32 s36, s55, s14
	s_cselect_b32 s23, s56, s69
	s_cselect_b32 s22, s57, s68
	s_mov_b32 m0, s58
	v_lshl_add_u64 v[162:163], s[30:31], 0, v[170:171]
	ds_read_b128 v[182:185], v197
	ds_read_b128 v[190:193], v197 offset:1024
	ds_read_b128 v[200:203], v197 offset:2048
	ds_read_b128 v[204:207], v197 offset:3072
	ds_read_b128 v[208:211], v197 offset:4096
	ds_read_b128 v[212:215], v197 offset:5120
	ds_read_b128 v[216:219], v197 offset:6144
	ds_read_b128 v[222:225], v197 offset:7168
	global_load_lds_dwordx4 v[162:163], off
	v_lshl_add_u64 v[162:163], s[30:31], 0, v[172:173]
	s_mov_b32 m0, s59
	s_nop 0
	global_load_lds_dwordx4 v[162:163], off
	s_waitcnt vmcnt(8)
	s_waitcnt lgkmcnt(0)
	s_barrier
	v_mfma_f32_16x16x32_bf16 v[128:131], v[134:137], v[182:185], v[128:131]
	s_setprio 1
	v_mfma_f32_16x16x32_bf16 v[124:127], v[142:145], v[182:185], v[124:127]
	v_mfma_f32_16x16x32_bf16 v[116:119], v[142:145], v[200:203], v[116:119]
	v_mfma_f32_16x16x32_bf16 v[120:123], v[134:137], v[200:203], v[120:123]
	v_mfma_f32_16x16x32_bf16 v[112:115], v[134:137], v[208:211], v[112:115]
	v_mfma_f32_16x16x32_bf16 v[108:111], v[142:145], v[208:211], v[108:111]
	v_mfma_f32_16x16x32_bf16 v[100:103], v[142:145], v[216:219], v[100:103]
	v_mfma_f32_16x16x32_bf16 v[104:107], v[134:137], v[216:219], v[104:107]
	v_mfma_f32_16x16x32_bf16 v[128:131], v[138:141], v[190:193], v[128:131]
	v_mfma_f32_16x16x32_bf16 v[124:127], v[146:149], v[190:193], v[124:127]
	v_mfma_f32_16x16x32_bf16 v[116:119], v[146:149], v[204:207], v[116:119]
	v_mfma_f32_16x16x32_bf16 v[120:123], v[138:141], v[204:207], v[120:123]
	v_mfma_f32_16x16x32_bf16 v[112:115], v[138:141], v[212:215], v[112:115]
	v_mfma_f32_16x16x32_bf16 v[108:111], v[146:149], v[212:215], v[108:111]
	v_mfma_f32_16x16x32_bf16 v[100:103], v[146:149], v[222:225], v[100:103]
	v_mfma_f32_16x16x32_bf16 v[104:107], v[138:141], v[222:225], v[104:107]
	s_setprio 0
	s_setprio 1
	v_mfma_f32_16x16x32_bf16 v[96:99], v[150:153], v[182:185], v[96:99]
	v_mfma_f32_16x16x32_bf16 v[92:95], v[158:161], v[182:185], v[92:95]
	v_mfma_f32_16x16x32_bf16 v[84:87], v[158:161], v[200:203], v[84:87]
	v_mfma_f32_16x16x32_bf16 v[88:91], v[150:153], v[200:203], v[88:91]
	v_mfma_f32_16x16x32_bf16 v[80:83], v[150:153], v[208:211], v[80:83]
	v_mfma_f32_16x16x32_bf16 v[76:79], v[158:161], v[208:211], v[76:79]
	v_mfma_f32_16x16x32_bf16 v[68:71], v[158:161], v[216:219], v[68:71]
	v_mfma_f32_16x16x32_bf16 v[72:75], v[150:153], v[216:219], v[72:75]
	v_mfma_f32_16x16x32_bf16 v[96:99], v[154:157], v[190:193], v[96:99]
	v_mfma_f32_16x16x32_bf16 v[92:95], v[178:181], v[190:193], v[92:95]
	v_mfma_f32_16x16x32_bf16 v[84:87], v[178:181], v[204:207], v[84:87]
	v_mfma_f32_16x16x32_bf16 v[88:91], v[154:157], v[204:207], v[88:91]
	v_mfma_f32_16x16x32_bf16 v[80:83], v[154:157], v[212:215], v[80:83]
	v_mfma_f32_16x16x32_bf16 v[76:79], v[178:181], v[212:215], v[76:79]
	v_mfma_f32_16x16x32_bf16 v[68:71], v[178:181], v[222:225], v[68:71]
	s_barrier
	v_mfma_f32_16x16x32_bf16 v[72:75], v[154:157], v[222:225], v[72:75]
	s_setprio 0
	s_mov_b32 m0, s60
	v_lshl_add_u64 v[162:163], s[22:23], 0, v[34:35]
	s_add_u32 s72, s22, 0x40000
	ds_read_b128 v[182:185], v197 offset:16384
	ds_read_b128 v[190:193], v197 offset:17408
	ds_read_b128 v[200:203], v197 offset:18432
	ds_read_b128 v[204:207], v197 offset:19456
	ds_read_b128 v[208:211], v197 offset:20480
	ds_read_b128 v[212:215], v197 offset:21504
	ds_read_b128 v[216:219], v197 offset:22528
	ds_read_b128 v[222:225], v197 offset:23552
	global_load_lds_dwordx4 v[162:163], off
	v_lshl_add_u64 v[174:175], s[22:23], 0, v[164:165]
	s_mov_b32 m0, s61
	s_addc_u32 s73, s23, 0
	global_load_lds_dwordx4 v[174:175], off
	v_lshl_add_u64 v[194:195], s[72:73], 0, v[34:35]
	s_mov_b32 m0, s62
	v_lshl_add_u64 v[226:227], s[36:37], 0, v[166:167]
	global_load_lds_dwordx4 v[194:195], off
	v_lshl_add_u64 v[194:195], s[72:73], 0, v[164:165]
	s_mov_b32 m0, s63
	s_nop 0
	global_load_lds_dwordx4 v[194:195], off
	v_lshl_add_u64 v[194:195], s[36:37], 0, v[168:169]
	s_mov_b32 m0, s41
	s_nop 0
	global_load_lds_dwordx4 v[194:195], off
	s_mov_b32 m0, s42
	s_nop 0
	global_load_lds_dwordx4 v[226:227], off
	s_waitcnt vmcnt(8)
	s_waitcnt lgkmcnt(0)
	s_barrier
	v_mfma_f32_16x16x32_bf16 v[64:67], v[134:137], v[182:185], v[64:67]
	s_setprio 1
	v_mfma_f32_16x16x32_bf16 v[60:63], v[142:145], v[182:185], v[60:63]
	v_mfma_f32_16x16x32_bf16 v[52:55], v[142:145], v[200:203], v[52:55]
	v_mfma_f32_16x16x32_bf16 v[56:59], v[134:137], v[200:203], v[56:59]
	v_mfma_f32_16x16x32_bf16 v[48:51], v[134:137], v[208:211], v[48:51]
	v_mfma_f32_16x16x32_bf16 v[44:47], v[142:145], v[208:211], v[44:47]
	v_mfma_f32_16x16x32_bf16 v[36:39], v[142:145], v[216:219], v[36:39]
	v_mfma_f32_16x16x32_bf16 v[40:43], v[134:137], v[216:219], v[40:43]
	v_mfma_f32_16x16x32_bf16 v[64:67], v[138:141], v[190:193], v[64:67]
	v_mfma_f32_16x16x32_bf16 v[60:63], v[146:149], v[190:193], v[60:63]
	v_mfma_f32_16x16x32_bf16 v[52:55], v[146:149], v[204:207], v[52:55]
	v_mfma_f32_16x16x32_bf16 v[56:59], v[138:141], v[204:207], v[56:59]
	v_mfma_f32_16x16x32_bf16 v[48:51], v[138:141], v[212:215], v[48:51]
	v_mfma_f32_16x16x32_bf16 v[44:47], v[146:149], v[212:215], v[44:47]
	v_mfma_f32_16x16x32_bf16 v[36:39], v[146:149], v[222:225], v[36:39]
	v_mfma_f32_16x16x32_bf16 v[40:43], v[138:141], v[222:225], v[40:43]
	s_setprio 0
	s_setprio 1
	v_mfma_f32_16x16x32_bf16 v[30:33], v[150:153], v[182:185], v[30:33]
	v_mfma_f32_16x16x32_bf16 v[26:29], v[158:161], v[182:185], v[26:29]
	v_mfma_f32_16x16x32_bf16 v[18:21], v[158:161], v[200:203], v[18:21]
	v_mfma_f32_16x16x32_bf16 v[22:25], v[150:153], v[200:203], v[22:25]
	v_mfma_f32_16x16x32_bf16 v[14:17], v[150:153], v[208:211], v[14:17]
	v_mfma_f32_16x16x32_bf16 v[10:13], v[158:161], v[208:211], v[10:13]
	v_mfma_f32_16x16x32_bf16 v[2:5], v[158:161], v[216:219], v[2:5]
	v_mfma_f32_16x16x32_bf16 v[6:9], v[150:153], v[216:219], v[6:9]
	v_mfma_f32_16x16x32_bf16 v[30:33], v[154:157], v[190:193], v[30:33]
	v_mfma_f32_16x16x32_bf16 v[26:29], v[178:181], v[190:193], v[26:29]
	v_mfma_f32_16x16x32_bf16 v[18:21], v[178:181], v[204:207], v[18:21]
	v_mfma_f32_16x16x32_bf16 v[22:25], v[154:157], v[204:207], v[22:25]
	v_mfma_f32_16x16x32_bf16 v[14:17], v[154:157], v[212:215], v[14:17]
	v_mfma_f32_16x16x32_bf16 v[10:13], v[178:181], v[212:215], v[10:13]
	v_mfma_f32_16x16x32_bf16 v[2:5], v[178:181], v[222:225], v[2:5]
	s_barrier
	v_mfma_f32_16x16x32_bf16 v[6:9], v[154:157], v[222:225], v[6:9]
	s_setprio 0
	ds_read_b128 v[134:137], v132
	ds_read_b128 v[138:141], v132 offset:1024
	ds_read_b128 v[142:145], v132 offset:2048
	ds_read_b128 v[146:149], v132 offset:3072
	ds_read_b128 v[150:153], v133
	ds_read_b128 v[154:157], v133 offset:1024
	ds_read_b128 v[158:161], v133 offset:2048
	ds_read_b128 v[178:181], v133 offset:3072
	s_add_u32 s36, s36, 0x40000
	s_addc_u32 s37, s37, 0
	s_mov_b32 m0, s43
	v_lshl_add_u64 v[228:229], s[36:37], 0, v[168:169]
	ds_read_b128 v[182:185], v197 offset:32768
	ds_read_b128 v[190:193], v197 offset:33792
	ds_read_b128 v[200:203], v197 offset:34816
	ds_read_b128 v[204:207], v197 offset:35840
	ds_read_b128 v[208:211], v197 offset:36864
	ds_read_b128 v[212:215], v197 offset:37888
	ds_read_b128 v[216:219], v197 offset:38912
	ds_read_b128 v[222:225], v197 offset:39936
	global_load_lds_dwordx4 v[228:229], off
	v_lshl_add_u64 v[228:229], s[36:37], 0, v[166:167]
	s_mov_b32 m0, s44
	s_nop 0
	global_load_lds_dwordx4 v[228:229], off
	s_waitcnt vmcnt(8)
	s_waitcnt lgkmcnt(0)
	s_barrier
	v_mfma_f32_16x16x32_bf16 v[128:131], v[134:137], v[182:185], v[128:131]
	s_setprio 1
	v_mfma_f32_16x16x32_bf16 v[124:127], v[142:145], v[182:185], v[124:127]
	v_mfma_f32_16x16x32_bf16 v[116:119], v[142:145], v[200:203], v[116:119]
	v_mfma_f32_16x16x32_bf16 v[120:123], v[134:137], v[200:203], v[120:123]
	v_mfma_f32_16x16x32_bf16 v[112:115], v[134:137], v[208:211], v[112:115]
	v_mfma_f32_16x16x32_bf16 v[108:111], v[142:145], v[208:211], v[108:111]
	v_mfma_f32_16x16x32_bf16 v[100:103], v[142:145], v[216:219], v[100:103]
	v_mfma_f32_16x16x32_bf16 v[104:107], v[134:137], v[216:219], v[104:107]
	v_mfma_f32_16x16x32_bf16 v[128:131], v[138:141], v[190:193], v[128:131]
	v_mfma_f32_16x16x32_bf16 v[124:127], v[146:149], v[190:193], v[124:127]
	v_mfma_f32_16x16x32_bf16 v[116:119], v[146:149], v[204:207], v[116:119]
	v_mfma_f32_16x16x32_bf16 v[120:123], v[138:141], v[204:207], v[120:123]
	v_mfma_f32_16x16x32_bf16 v[112:115], v[138:141], v[212:215], v[112:115]
	v_mfma_f32_16x16x32_bf16 v[108:111], v[146:149], v[212:215], v[108:111]
	v_mfma_f32_16x16x32_bf16 v[100:103], v[146:149], v[222:225], v[100:103]
	v_mfma_f32_16x16x32_bf16 v[104:107], v[138:141], v[222:225], v[104:107]
	s_setprio 0
	s_setprio 1
	v_mfma_f32_16x16x32_bf16 v[96:99], v[150:153], v[182:185], v[96:99]
	v_mfma_f32_16x16x32_bf16 v[92:95], v[158:161], v[182:185], v[92:95]
	v_mfma_f32_16x16x32_bf16 v[84:87], v[158:161], v[200:203], v[84:87]
	v_mfma_f32_16x16x32_bf16 v[88:91], v[150:153], v[200:203], v[88:91]
	v_mfma_f32_16x16x32_bf16 v[80:83], v[150:153], v[208:211], v[80:83]
	v_mfma_f32_16x16x32_bf16 v[76:79], v[158:161], v[208:211], v[76:79]
	v_mfma_f32_16x16x32_bf16 v[68:71], v[158:161], v[216:219], v[68:71]
	v_mfma_f32_16x16x32_bf16 v[72:75], v[150:153], v[216:219], v[72:75]
	v_mfma_f32_16x16x32_bf16 v[96:99], v[154:157], v[190:193], v[96:99]
	v_mfma_f32_16x16x32_bf16 v[92:95], v[178:181], v[190:193], v[92:95]
	v_mfma_f32_16x16x32_bf16 v[84:87], v[178:181], v[204:207], v[84:87]
	v_mfma_f32_16x16x32_bf16 v[88:91], v[154:157], v[204:207], v[88:91]
	v_mfma_f32_16x16x32_bf16 v[80:83], v[154:157], v[212:215], v[80:83]
	v_mfma_f32_16x16x32_bf16 v[76:79], v[178:181], v[212:215], v[76:79]
	v_mfma_f32_16x16x32_bf16 v[68:71], v[178:181], v[222:225], v[68:71]
	s_barrier
	v_mfma_f32_16x16x32_bf16 v[72:75], v[154:157], v[222:225], v[72:75]
	s_setprio 0
	s_mov_b32 m0, s64
	v_lshl_add_u64 v[162:163], v[162:163], 0, s[18:19]
	s_add_u32 s22, s22, 0x40080
	ds_read_b128 v[182:185], v197 offset:49152
	ds_read_b128 v[190:193], v197 offset:50176
	ds_read_b128 v[200:203], v197 offset:51200
	ds_read_b128 v[204:207], v197 offset:52224
	ds_read_b128 v[208:211], v197 offset:53248
	ds_read_b128 v[212:215], v197 offset:54272
	ds_read_b128 v[216:219], v197 offset:55296
	ds_read_b128 v[222:225], v197 offset:56320
	global_load_lds_dwordx4 v[162:163], off
	v_lshl_add_u64 v[162:163], v[174:175], 0, s[18:19]
	s_mov_b32 m0, s65
	s_addc_u32 s23, s23, 0
	global_load_lds_dwordx4 v[162:163], off
	v_lshl_add_u64 v[162:163], s[22:23], 0, v[34:35]
	s_mov_b32 m0, s66
	s_nop 0
	global_load_lds_dwordx4 v[162:163], off
	v_lshl_add_u64 v[162:163], s[22:23], 0, v[164:165]
	s_mov_b32 m0, s67
	s_nop 0
	global_load_lds_dwordx4 v[162:163], off
	v_lshl_add_u64 v[162:163], v[194:195], 0, s[18:19]
	s_mov_b32 m0, s47
	s_nop 0
	global_load_lds_dwordx4 v[162:163], off
	v_lshl_add_u64 v[162:163], v[226:227], 0, s[18:19]
	s_mov_b32 m0, s48
	s_nop 0
	global_load_lds_dwordx4 v[162:163], off
	s_waitcnt vmcnt(8)
	s_waitcnt lgkmcnt(0)
	s_barrier
	v_mfma_f32_16x16x32_bf16 v[64:67], v[134:137], v[182:185], v[64:67]
	s_setprio 1
	v_mfma_f32_16x16x32_bf16 v[60:63], v[142:145], v[182:185], v[60:63]
	v_mfma_f32_16x16x32_bf16 v[52:55], v[142:145], v[200:203], v[52:55]
	v_mfma_f32_16x16x32_bf16 v[56:59], v[134:137], v[200:203], v[56:59]
	v_mfma_f32_16x16x32_bf16 v[48:51], v[134:137], v[208:211], v[48:51]
	v_mfma_f32_16x16x32_bf16 v[44:47], v[142:145], v[208:211], v[44:47]
	v_mfma_f32_16x16x32_bf16 v[36:39], v[142:145], v[216:219], v[36:39]
	v_mfma_f32_16x16x32_bf16 v[40:43], v[134:137], v[216:219], v[40:43]
	v_mfma_f32_16x16x32_bf16 v[64:67], v[138:141], v[190:193], v[64:67]
	v_mfma_f32_16x16x32_bf16 v[60:63], v[146:149], v[190:193], v[60:63]
	v_mfma_f32_16x16x32_bf16 v[52:55], v[146:149], v[204:207], v[52:55]
	v_mfma_f32_16x16x32_bf16 v[56:59], v[138:141], v[204:207], v[56:59]
	v_mfma_f32_16x16x32_bf16 v[48:51], v[138:141], v[212:215], v[48:51]
	v_mfma_f32_16x16x32_bf16 v[44:47], v[146:149], v[212:215], v[44:47]
	v_mfma_f32_16x16x32_bf16 v[36:39], v[146:149], v[222:225], v[36:39]
	v_mfma_f32_16x16x32_bf16 v[40:43], v[138:141], v[222:225], v[40:43]
	s_setprio 0
	s_setprio 1
	v_mfma_f32_16x16x32_bf16 v[30:33], v[150:153], v[182:185], v[30:33]
	v_mfma_f32_16x16x32_bf16 v[26:29], v[158:161], v[182:185], v[26:29]
	v_mfma_f32_16x16x32_bf16 v[18:21], v[158:161], v[200:203], v[18:21]
	v_mfma_f32_16x16x32_bf16 v[22:25], v[150:153], v[200:203], v[22:25]
	v_mfma_f32_16x16x32_bf16 v[14:17], v[150:153], v[208:211], v[14:17]
	v_mfma_f32_16x16x32_bf16 v[10:13], v[158:161], v[208:211], v[10:13]
	v_mfma_f32_16x16x32_bf16 v[2:5], v[158:161], v[216:219], v[2:5]
	v_mfma_f32_16x16x32_bf16 v[6:9], v[150:153], v[216:219], v[6:9]
	v_mfma_f32_16x16x32_bf16 v[30:33], v[154:157], v[190:193], v[30:33]
	v_mfma_f32_16x16x32_bf16 v[26:29], v[178:181], v[190:193], v[26:29]
	v_mfma_f32_16x16x32_bf16 v[18:21], v[178:181], v[204:207], v[18:21]
	v_mfma_f32_16x16x32_bf16 v[22:25], v[154:157], v[204:207], v[22:25]
	v_mfma_f32_16x16x32_bf16 v[14:17], v[154:157], v[212:215], v[14:17]
	v_mfma_f32_16x16x32_bf16 v[10:13], v[178:181], v[212:215], v[10:13]
	v_mfma_f32_16x16x32_bf16 v[2:5], v[178:181], v[222:225], v[2:5]
	s_barrier
	v_mfma_f32_16x16x32_bf16 v[6:9], v[154:157], v[222:225], v[6:9]
	s_setprio 0
	s_add_i32 s70, s70, 2
	s_add_u32 s30, s30, 0x100
	s_addc_u32 s31, s31, 0
	s_add_u32 s68, s68, 0x100
	s_addc_u32 s69, s69, 0
	s_cmp_gt_u32 s70, 13
	s_cbranch_scc0 .LBB0_287
	s_and_b64 vcc, exec, s[8:9]
	s_cbranch_vccz .LBB0_290
	s_barrier

.LBB0_540:
	s_lshl_b32 s14, s55, 19
	v_readlane_b32 s16, v253, 53
	v_readlane_b32 s17, v253, 54
	s_add_u32 s16, s16, s14
	s_addc_u32 s17, s17, 0
	s_and_b64 s[22:23], s[4:5], exec
	s_cselect_b32 s58, s17, s37
	s_cselect_b32 s59, s16, s36
	s_lshl_b32 s14, s54, 19
	s_add_u32 s22, s15, s14
	s_addc_u32 s23, s26, 0
	s_and_b64 s[40:41], s[4:5], exec
	s_cselect_b32 s60, s23, s31
	s_cselect_b32 s61, s22, s30
	s_add_i32 s64, 0, 0x10000
	v_add_u32_e32 v172, s64, v222
	s_add_i32 s66, 0, 0x14000
	v_add_u32_e32 v173, s66, v222
	ds_read_b128 v[160:163], v172
	ds_read_b128 v[152:155], v172 offset:1024
	ds_read_b128 v[156:159], v172 offset:2048
	ds_read_b128 v[148:151], v172 offset:3072
	ds_read_b128 v[144:147], v173
	ds_read_b128 v[136:139], v173 offset:1024
	ds_read_b128 v[140:143], v173 offset:2048
	ds_read_b128 v[132:135], v173 offset:3072
	s_add_u32 s40, s36, 0x40080
	s_addc_u32 s41, s37, 0
	s_add_i32 s62, s43, 0xc000
	v_lshl_add_u64 v[174:175], s[40:41], 0, v[194:195]
	s_mov_b32 m0, s62
	s_add_i32 s63, s43, 0xe000
	ds_read_b128 v[164:167], v223
	ds_read_b128 v[168:171], v223 offset:1024
	ds_read_b128 v[178:181], v223 offset:2048
	ds_read_b128 v[182:185], v223 offset:3072
	ds_read_b128 v[200:203], v223 offset:4096
	ds_read_b128 v[204:207], v223 offset:5120
	ds_read_b128 v[208:211], v223 offset:6144
	ds_read_b128 v[212:215], v223 offset:7168
	global_load_lds_dwordx4 v[174:175], off
	v_lshl_add_u64 v[174:175], s[40:41], 0, v[192:193]
	s_mov_b32 m0, s63
	s_nop 0
	global_load_lds_dwordx4 v[174:175], off
	s_waitcnt vmcnt(8)
	s_waitcnt lgkmcnt(0)
	s_barrier
	v_mfma_f32_16x16x32_bf16 v[128:131], v[160:163], v[164:167], 0
	s_setprio 1
	v_mfma_f32_16x16x32_bf16 v[124:127], v[156:159], v[164:167], 0
	v_mfma_f32_16x16x32_bf16 v[116:119], v[156:159], v[178:181], 0
	v_mfma_f32_16x16x32_bf16 v[120:123], v[160:163], v[178:181], 0
	v_mfma_f32_16x16x32_bf16 v[112:115], v[160:163], v[200:203], 0
	v_mfma_f32_16x16x32_bf16 v[108:111], v[156:159], v[200:203], 0
	v_mfma_f32_16x16x32_bf16 v[100:103], v[156:159], v[208:211], 0
	v_mfma_f32_16x16x32_bf16 v[104:107], v[160:163], v[208:211], 0
	s_nop 0
	v_mfma_f32_16x16x32_bf16 v[128:131], v[152:155], v[168:171], v[128:131]
	v_mfma_f32_16x16x32_bf16 v[124:127], v[148:151], v[168:171], v[124:127]
	v_mfma_f32_16x16x32_bf16 v[116:119], v[148:151], v[182:185], v[116:119]
	v_mfma_f32_16x16x32_bf16 v[120:123], v[152:155], v[182:185], v[120:123]
	v_mfma_f32_16x16x32_bf16 v[112:115], v[152:155], v[204:207], v[112:115]
	v_mfma_f32_16x16x32_bf16 v[108:111], v[148:151], v[204:207], v[108:111]
	v_mfma_f32_16x16x32_bf16 v[100:103], v[148:151], v[212:215], v[100:103]
	v_mfma_f32_16x16x32_bf16 v[104:107], v[152:155], v[212:215], v[104:107]
	s_setprio 0
	s_setprio 1
	v_mfma_f32_16x16x32_bf16 v[96:99], v[144:147], v[164:167], 0
	v_mfma_f32_16x16x32_bf16 v[92:95], v[140:143], v[164:167], 0
	v_mfma_f32_16x16x32_bf16 v[84:87], v[140:143], v[178:181], 0
	v_mfma_f32_16x16x32_bf16 v[88:91], v[144:147], v[178:181], 0
	v_mfma_f32_16x16x32_bf16 v[80:83], v[144:147], v[200:203], 0
	v_mfma_f32_16x16x32_bf16 v[76:79], v[140:143], v[200:203], 0
	v_mfma_f32_16x16x32_bf16 v[68:71], v[140:143], v[208:211], 0
	v_mfma_f32_16x16x32_bf16 v[72:75], v[144:147], v[208:211], 0
	s_nop 0
	v_mfma_f32_16x16x32_bf16 v[96:99], v[136:139], v[168:171], v[96:99]
	v_mfma_f32_16x16x32_bf16 v[92:95], v[132:135], v[168:171], v[92:95]
	v_mfma_f32_16x16x32_bf16 v[84:87], v[132:135], v[182:185], v[84:87]
	v_mfma_f32_16x16x32_bf16 v[88:91], v[136:139], v[182:185], v[88:91]
	v_mfma_f32_16x16x32_bf16 v[80:83], v[136:139], v[204:207], v[80:83]
	v_mfma_f32_16x16x32_bf16 v[76:79], v[132:135], v[204:207], v[76:79]
	v_mfma_f32_16x16x32_bf16 v[68:71], v[132:135], v[212:215], v[68:71]
	s_barrier
	v_mfma_f32_16x16x32_bf16 v[72:75], v[136:139], v[212:215], v[72:75]
	s_setprio 0
	v_lshl_add_u64 v[164:165], s[30:31], 0, v[34:35]
	s_add_i32 s64, s64, s42
	v_lshl_add_u64 v[166:167], v[164:165], 0, s[28:29]
	s_mov_b32 m0, s64
	s_add_i32 s65, s64, 0x2000
	ds_read_b128 v[178:181], v223 offset:16384
	ds_read_b128 v[182:185], v223 offset:17408
	ds_read_b128 v[200:203], v223 offset:18432
	ds_read_b128 v[204:207], v223 offset:19456
	ds_read_b128 v[208:211], v223 offset:20480
	ds_read_b128 v[212:215], v223 offset:21504
	ds_read_b128 v[216:219], v223 offset:22528
	ds_read_b128 v[224:227], v223 offset:23552
	global_load_lds_dwordx4 v[166:167], off
	v_lshl_add_u64 v[166:167], s[30:31], 0, v[190:191]
	s_add_u32 s40, s30, 0x40100
	v_lshl_add_u64 v[168:169], v[166:167], 0, s[28:29]
	s_mov_b32 m0, s65
	s_addc_u32 s41, s31, 0
	s_add_i32 s66, s66, s42
	global_load_lds_dwordx4 v[168:169], off
	v_lshl_add_u64 v[168:169], s[40:41], 0, v[34:35]
	s_mov_b32 m0, s66
	s_add_i32 s67, s66, 0x2000
	global_load_lds_dwordx4 v[168:169], off
	v_lshl_add_u64 v[168:169], s[40:41], 0, v[190:191]
	s_mov_b32 m0, s67
	s_nop 0
	global_load_lds_dwordx4 v[168:169], off
	v_lshl_add_u64 v[168:169], s[36:37], 0, v[194:195]
	v_lshl_add_u64 v[170:171], v[168:169], 0, s[28:29]
	s_mov_b32 m0, s43
	s_nop 0
	global_load_lds_dwordx4 v[170:171], off
	v_lshl_add_u64 v[170:171], s[36:37], 0, v[192:193]
	v_lshl_add_u64 v[174:175], v[170:171], 0, s[28:29]
	s_mov_b32 m0, s44
	s_nop 0
	global_load_lds_dwordx4 v[174:175], off
	s_waitcnt vmcnt(8)
	s_waitcnt lgkmcnt(0)
	s_barrier
	v_mfma_f32_16x16x32_bf16 v[64:67], v[160:163], v[178:181], 0
	s_setprio 1
	v_mfma_f32_16x16x32_bf16 v[60:63], v[156:159], v[178:181], 0
	v_mfma_f32_16x16x32_bf16 v[52:55], v[156:159], v[200:203], 0
	v_mfma_f32_16x16x32_bf16 v[56:59], v[160:163], v[200:203], 0
	v_mfma_f32_16x16x32_bf16 v[48:51], v[160:163], v[208:211], 0
	v_mfma_f32_16x16x32_bf16 v[44:47], v[156:159], v[208:211], 0
	v_mfma_f32_16x16x32_bf16 v[36:39], v[156:159], v[216:219], 0
	v_mfma_f32_16x16x32_bf16 v[40:43], v[160:163], v[216:219], 0
	s_nop 0
	v_mfma_f32_16x16x32_bf16 v[64:67], v[152:155], v[182:185], v[64:67]
	v_mfma_f32_16x16x32_bf16 v[60:63], v[148:151], v[182:185], v[60:63]
	v_mfma_f32_16x16x32_bf16 v[52:55], v[148:151], v[204:207], v[52:55]
	v_mfma_f32_16x16x32_bf16 v[56:59], v[152:155], v[204:207], v[56:59]
	v_mfma_f32_16x16x32_bf16 v[48:51], v[152:155], v[212:215], v[48:51]
	v_mfma_f32_16x16x32_bf16 v[44:47], v[148:151], v[212:215], v[44:47]
	v_mfma_f32_16x16x32_bf16 v[36:39], v[148:151], v[224:227], v[36:39]
	v_mfma_f32_16x16x32_bf16 v[40:43], v[152:155], v[224:227], v[40:43]
	s_setprio 0
	s_setprio 1
	v_mfma_f32_16x16x32_bf16 v[30:33], v[144:147], v[178:181], 0
	v_mfma_f32_16x16x32_bf16 v[26:29], v[140:143], v[178:181], 0
	v_mfma_f32_16x16x32_bf16 v[18:21], v[140:143], v[200:203], 0
	v_mfma_f32_16x16x32_bf16 v[22:25], v[144:147], v[200:203], 0
	v_mfma_f32_16x16x32_bf16 v[14:17], v[144:147], v[208:211], 0
	v_mfma_f32_16x16x32_bf16 v[10:13], v[140:143], v[208:211], 0
	v_mfma_f32_16x16x32_bf16 v[2:5], v[140:143], v[216:219], 0
	v_mfma_f32_16x16x32_bf16 v[6:9], v[144:147], v[216:219], 0
	s_nop 0
	v_mfma_f32_16x16x32_bf16 v[30:33], v[136:139], v[182:185], v[30:33]
	v_mfma_f32_16x16x32_bf16 v[26:29], v[132:135], v[182:185], v[26:29]
	v_mfma_f32_16x16x32_bf16 v[18:21], v[132:135], v[204:207], v[18:21]
	v_mfma_f32_16x16x32_bf16 v[22:25], v[136:139], v[204:207], v[22:25]
	v_mfma_f32_16x16x32_bf16 v[14:17], v[136:139], v[212:215], v[14:17]
	v_mfma_f32_16x16x32_bf16 v[10:13], v[132:135], v[212:215], v[10:13]
	v_mfma_f32_16x16x32_bf16 v[2:5], v[132:135], v[224:227], v[2:5]
	s_barrier
	v_mfma_f32_16x16x32_bf16 v[6:9], v[136:139], v[224:227], v[6:9]
	s_setprio 0
	s_add_i32 s68, 0, 0x18000
	s_add_i32 s70, 0, 0x1c000
	v_add_u32_e32 v132, s68, v222
	v_add_u32_e32 v133, s70, v222
	ds_read_b128 v[134:137], v132
	ds_read_b128 v[138:141], v132 offset:1024
	ds_read_b128 v[142:145], v132 offset:2048
	ds_read_b128 v[146:149], v132 offset:3072
	ds_read_b128 v[150:153], v133
	ds_read_b128 v[154:157], v133 offset:1024
	ds_read_b128 v[158:161], v133 offset:2048
	ds_read_b128 v[178:181], v133 offset:3072
	s_add_u32 s40, s36, 0x40100
	s_addc_u32 s41, s37, 0
	s_mov_b32 m0, s45
	v_lshl_add_u64 v[162:163], s[40:41], 0, v[194:195]
	ds_read_b128 v[182:185], v223 offset:32768
	ds_read_b128 v[200:203], v223 offset:33792
	ds_read_b128 v[204:207], v223 offset:34816
	ds_read_b128 v[208:211], v223 offset:35840
	ds_read_b128 v[212:215], v223 offset:36864
	ds_read_b128 v[216:219], v223 offset:37888
	ds_read_b128 v[224:227], v223 offset:38912
	ds_read_b128 v[228:231], v223 offset:39936
	global_load_lds_dwordx4 v[162:163], off
	v_lshl_add_u64 v[162:163], s[40:41], 0, v[192:193]
	s_mov_b32 m0, s46
	s_nop 0
	global_load_lds_dwordx4 v[162:163], off
	s_waitcnt vmcnt(8)
	s_waitcnt lgkmcnt(0)
	s_barrier
	v_mfma_f32_16x16x32_bf16 v[128:131], v[134:137], v[182:185], v[128:131]
	s_setprio 1
	v_mfma_f32_16x16x32_bf16 v[124:127], v[142:145], v[182:185], v[124:127]
	v_mfma_f32_16x16x32_bf16 v[116:119], v[142:145], v[204:207], v[116:119]
	v_mfma_f32_16x16x32_bf16 v[120:123], v[134:137], v[204:207], v[120:123]
	v_mfma_f32_16x16x32_bf16 v[112:115], v[134:137], v[212:215], v[112:115]
	v_mfma_f32_16x16x32_bf16 v[108:111], v[142:145], v[212:215], v[108:111]
	v_mfma_f32_16x16x32_bf16 v[100:103], v[142:145], v[224:227], v[100:103]
	v_mfma_f32_16x16x32_bf16 v[104:107], v[134:137], v[224:227], v[104:107]
	v_mfma_f32_16x16x32_bf16 v[128:131], v[138:141], v[200:203], v[128:131]
	v_mfma_f32_16x16x32_bf16 v[124:127], v[146:149], v[200:203], v[124:127]
	v_mfma_f32_16x16x32_bf16 v[116:119], v[146:149], v[208:211], v[116:119]
	v_mfma_f32_16x16x32_bf16 v[120:123], v[138:141], v[208:211], v[120:123]
	v_mfma_f32_16x16x32_bf16 v[112:115], v[138:141], v[216:219], v[112:115]
	v_mfma_f32_16x16x32_bf16 v[108:111], v[146:149], v[216:219], v[108:111]
	v_mfma_f32_16x16x32_bf16 v[100:103], v[146:149], v[228:231], v[100:103]
	v_mfma_f32_16x16x32_bf16 v[104:107], v[138:141], v[228:231], v[104:107]
	s_setprio 0
	s_setprio 1
	v_mfma_f32_16x16x32_bf16 v[96:99], v[150:153], v[182:185], v[96:99]
	v_mfma_f32_16x16x32_bf16 v[92:95], v[158:161], v[182:185], v[92:95]
	v_mfma_f32_16x16x32_bf16 v[84:87], v[158:161], v[204:207], v[84:87]
	v_mfma_f32_16x16x32_bf16 v[88:91], v[150:153], v[204:207], v[88:91]
	v_mfma_f32_16x16x32_bf16 v[80:83], v[150:153], v[212:215], v[80:83]
	v_mfma_f32_16x16x32_bf16 v[76:79], v[158:161], v[212:215], v[76:79]
	v_mfma_f32_16x16x32_bf16 v[68:71], v[158:161], v[224:227], v[68:71]
	v_mfma_f32_16x16x32_bf16 v[72:75], v[150:153], v[224:227], v[72:75]
	v_mfma_f32_16x16x32_bf16 v[96:99], v[154:157], v[200:203], v[96:99]
	v_mfma_f32_16x16x32_bf16 v[92:95], v[178:181], v[200:203], v[92:95]
	v_mfma_f32_16x16x32_bf16 v[84:87], v[178:181], v[208:211], v[84:87]
	v_mfma_f32_16x16x32_bf16 v[88:91], v[154:157], v[208:211], v[88:91]
	v_mfma_f32_16x16x32_bf16 v[80:83], v[154:157], v[216:219], v[80:83]
	v_mfma_f32_16x16x32_bf16 v[76:79], v[178:181], v[216:219], v[76:79]
	v_mfma_f32_16x16x32_bf16 v[68:71], v[178:181], v[228:231], v[68:71]
	s_barrier
	v_mfma_f32_16x16x32_bf16 v[72:75], v[154:157], v[228:231], v[72:75]
	s_setprio 0
	s_add_i32 s68, s68, s42
	s_mov_b64 s[24:25], 0x180
	s_add_i32 s69, s68, 0x2000
	v_lshl_add_u64 v[162:163], v[164:165], 0, s[24:25]
	s_mov_b32 m0, s68
	s_add_u32 s40, s30, 0x40180
	ds_read_b128 v[182:185], v223 offset:49152
	ds_read_b128 v[200:203], v223 offset:50176
	ds_read_b128 v[204:207], v223 offset:51200
	ds_read_b128 v[208:211], v223 offset:52224
	ds_read_b128 v[212:215], v223 offset:53248
	ds_read_b128 v[216:219], v223 offset:54272
	ds_read_b128 v[224:227], v223 offset:55296
	ds_read_b128 v[228:231], v223 offset:56320
	global_load_lds_dwordx4 v[162:163], off
	v_lshl_add_u64 v[162:163], v[166:167], 0, s[24:25]
	s_mov_b32 m0, s69
	s_addc_u32 s41, s31, 0
	s_add_i32 s70, s70, s42
	global_load_lds_dwordx4 v[162:163], off
	v_lshl_add_u64 v[162:163], s[40:41], 0, v[34:35]
	s_mov_b32 m0, s70
	s_add_i32 s71, s70, 0x2000
	global_load_lds_dwordx4 v[162:163], off
	v_lshl_add_u64 v[162:163], s[40:41], 0, v[190:191]
	s_mov_b32 m0, s71
	s_nop 0
	global_load_lds_dwordx4 v[162:163], off
	v_lshl_add_u64 v[162:163], v[168:169], 0, s[24:25]
	s_mov_b32 m0, s51
	s_nop 0
	global_load_lds_dwordx4 v[162:163], off
	v_lshl_add_u64 v[162:163], v[170:171], 0, s[24:25]
	s_mov_b32 m0, s52
	s_nop 0
	global_load_lds_dwordx4 v[162:163], off
	s_waitcnt vmcnt(8)
	s_waitcnt lgkmcnt(0)
	s_barrier
	v_mfma_f32_16x16x32_bf16 v[64:67], v[134:137], v[182:185], v[64:67]
	s_setprio 1
	v_mfma_f32_16x16x32_bf16 v[60:63], v[142:145], v[182:185], v[60:63]
	v_mfma_f32_16x16x32_bf16 v[52:55], v[142:145], v[204:207], v[52:55]
	v_mfma_f32_16x16x32_bf16 v[56:59], v[134:137], v[204:207], v[56:59]
	v_mfma_f32_16x16x32_bf16 v[48:51], v[134:137], v[212:215], v[48:51]
	v_mfma_f32_16x16x32_bf16 v[44:47], v[142:145], v[212:215], v[44:47]
	v_mfma_f32_16x16x32_bf16 v[36:39], v[142:145], v[224:227], v[36:39]
	v_mfma_f32_16x16x32_bf16 v[40:43], v[134:137], v[224:227], v[40:43]
	v_mfma_f32_16x16x32_bf16 v[64:67], v[138:141], v[200:203], v[64:67]
	v_mfma_f32_16x16x32_bf16 v[60:63], v[146:149], v[200:203], v[60:63]
	v_mfma_f32_16x16x32_bf16 v[52:55], v[146:149], v[208:211], v[52:55]
	v_mfma_f32_16x16x32_bf16 v[56:59], v[138:141], v[208:211], v[56:59]
	v_mfma_f32_16x16x32_bf16 v[48:51], v[138:141], v[216:219], v[48:51]
	v_mfma_f32_16x16x32_bf16 v[44:47], v[146:149], v[216:219], v[44:47]
	v_mfma_f32_16x16x32_bf16 v[36:39], v[146:149], v[228:231], v[36:39]
	v_mfma_f32_16x16x32_bf16 v[40:43], v[138:141], v[228:231], v[40:43]
	s_setprio 0
	s_setprio 1
	v_mfma_f32_16x16x32_bf16 v[30:33], v[150:153], v[182:185], v[30:33]
	v_mfma_f32_16x16x32_bf16 v[26:29], v[158:161], v[182:185], v[26:29]
	v_mfma_f32_16x16x32_bf16 v[18:21], v[158:161], v[204:207], v[18:21]
	v_mfma_f32_16x16x32_bf16 v[22:25], v[150:153], v[204:207], v[22:25]
	v_mfma_f32_16x16x32_bf16 v[14:17], v[150:153], v[212:215], v[14:17]
	v_mfma_f32_16x16x32_bf16 v[10:13], v[158:161], v[212:215], v[10:13]
	v_mfma_f32_16x16x32_bf16 v[2:5], v[158:161], v[224:227], v[2:5]
	v_mfma_f32_16x16x32_bf16 v[6:9], v[150:153], v[224:227], v[6:9]
	v_mfma_f32_16x16x32_bf16 v[30:33], v[154:157], v[200:203], v[30:33]
	v_mfma_f32_16x16x32_bf16 v[26:29], v[178:181], v[200:203], v[26:29]
	v_mfma_f32_16x16x32_bf16 v[18:21], v[178:181], v[208:211], v[18:21]
	v_mfma_f32_16x16x32_bf16 v[22:25], v[154:157], v[208:211], v[22:25]
	v_mfma_f32_16x16x32_bf16 v[14:17], v[154:157], v[216:219], v[14:17]
	v_mfma_f32_16x16x32_bf16 v[10:13], v[178:181], v[216:219], v[10:13]
	v_mfma_f32_16x16x32_bf16 v[2:5], v[178:181], v[228:231], v[2:5]
	s_barrier
	v_mfma_f32_16x16x32_bf16 v[6:9], v[154:157], v[228:231], v[6:9]
	s_setprio 0
	s_add_u32 s36, s36, 0x40180
	s_addc_u32 s37, s37, 0
	s_add_u32 s72, s30, 0x200
	s_addc_u32 s73, s31, 0
	s_mov_b32 s74, 0
.LBB0_541:
	ds_read_b128 v[134:137], v172
	ds_read_b128 v[138:141], v172 offset:1024
	ds_read_b128 v[142:145], v172 offset:2048
	ds_read_b128 v[146:149], v172 offset:3072
	ds_read_b128 v[150:153], v173
	ds_read_b128 v[154:157], v173 offset:1024
	ds_read_b128 v[158:161], v173 offset:2048
	ds_read_b128 v[162:165], v173 offset:3072
	s_add_u32 s14, s36, 0xfffc0080
	s_addc_u32 s30, s37, -1
	s_cmp_eq_u32 s74, 12
	s_cselect_b32 s41, s58, s30
	s_cselect_b32 s40, s59, s14
	s_cselect_b32 s31, s60, s73
	s_cselect_b32 s30, s61, s72
	s_mov_b32 m0, s62
	v_lshl_add_u64 v[170:171], s[36:37], 0, v[196:197]
	ds_read_b128 v[166:169], v223
	ds_read_b128 v[178:181], v223 offset:1024
	ds_read_b128 v[182:185], v223 offset:2048
	ds_read_b128 v[200:203], v223 offset:3072
	ds_read_b128 v[204:207], v223 offset:4096
	ds_read_b128 v[208:211], v223 offset:5120
	ds_read_b128 v[212:215], v223 offset:6144
	ds_read_b128 v[216:219], v223 offset:7168
	global_load_lds_dwordx4 v[170:171], off
	v_lshl_add_u64 v[170:171], s[36:37], 0, v[198:199]
	s_mov_b32 m0, s63
	s_nop 0
	global_load_lds_dwordx4 v[170:171], off
	s_waitcnt vmcnt(8)
	s_waitcnt lgkmcnt(0)
	s_barrier
	v_mfma_f32_16x16x32_bf16 v[128:131], v[134:137], v[166:169], v[128:131]
	s_setprio 1
	v_mfma_f32_16x16x32_bf16 v[124:127], v[142:145], v[166:169], v[124:127]
	v_mfma_f32_16x16x32_bf16 v[116:119], v[142:145], v[182:185], v[116:119]
	v_mfma_f32_16x16x32_bf16 v[120:123], v[134:137], v[182:185], v[120:123]
	v_mfma_f32_16x16x32_bf16 v[112:115], v[134:137], v[204:207], v[112:115]
	v_mfma_f32_16x16x32_bf16 v[108:111], v[142:145], v[204:207], v[108:111]
	v_mfma_f32_16x16x32_bf16 v[100:103], v[142:145], v[212:215], v[100:103]
	v_mfma_f32_16x16x32_bf16 v[104:107], v[134:137], v[212:215], v[104:107]
	v_mfma_f32_16x16x32_bf16 v[128:131], v[138:141], v[178:181], v[128:131]
	v_mfma_f32_16x16x32_bf16 v[124:127], v[146:149], v[178:181], v[124:127]
	v_mfma_f32_16x16x32_bf16 v[116:119], v[146:149], v[200:203], v[116:119]
	v_mfma_f32_16x16x32_bf16 v[120:123], v[138:141], v[200:203], v[120:123]
	v_mfma_f32_16x16x32_bf16 v[112:115], v[138:141], v[208:211], v[112:115]
	v_mfma_f32_16x16x32_bf16 v[108:111], v[146:149], v[208:211], v[108:111]
	v_mfma_f32_16x16x32_bf16 v[100:103], v[146:149], v[216:219], v[100:103]
	v_mfma_f32_16x16x32_bf16 v[104:107], v[138:141], v[216:219], v[104:107]
	s_setprio 0
	s_setprio 1
	v_mfma_f32_16x16x32_bf16 v[96:99], v[150:153], v[166:169], v[96:99]
	v_mfma_f32_16x16x32_bf16 v[92:95], v[158:161], v[166:169], v[92:95]
	v_mfma_f32_16x16x32_bf16 v[84:87], v[158:161], v[182:185], v[84:87]
	v_mfma_f32_16x16x32_bf16 v[88:91], v[150:153], v[182:185], v[88:91]
	v_mfma_f32_16x16x32_bf16 v[80:83], v[150:153], v[204:207], v[80:83]
	v_mfma_f32_16x16x32_bf16 v[76:79], v[158:161], v[204:207], v[76:79]
	v_mfma_f32_16x16x32_bf16 v[68:71], v[158:161], v[212:215], v[68:71]
	v_mfma_f32_16x16x32_bf16 v[72:75], v[150:153], v[212:215], v[72:75]
	v_mfma_f32_16x16x32_bf16 v[96:99], v[154:157], v[178:181], v[96:99]
	v_mfma_f32_16x16x32_bf16 v[92:95], v[162:165], v[178:181], v[92:95]
	v_mfma_f32_16x16x32_bf16 v[84:87], v[162:165], v[200:203], v[84:87]
	v_mfma_f32_16x16x32_bf16 v[88:91], v[154:157], v[200:203], v[88:91]
	v_mfma_f32_16x16x32_bf16 v[80:83], v[154:157], v[208:211], v[80:83]
	v_mfma_f32_16x16x32_bf16 v[76:79], v[162:165], v[208:211], v[76:79]
	v_mfma_f32_16x16x32_bf16 v[68:71], v[162:165], v[216:219], v[68:71]
	s_barrier
	v_mfma_f32_16x16x32_bf16 v[72:75], v[154:157], v[216:219], v[72:75]
	s_setprio 0
	s_mov_b32 m0, s64
	v_lshl_add_u64 v[170:171], s[30:31], 0, v[34:35]
	s_add_u32 s76, s30, 0x40000
	ds_read_b128 v[166:169], v223 offset:16384
	ds_read_b128 v[178:181], v223 offset:17408
	ds_read_b128 v[182:185], v223 offset:18432
	ds_read_b128 v[200:203], v223 offset:19456
	ds_read_b128 v[204:207], v223 offset:20480
	ds_read_b128 v[208:211], v223 offset:21504
	ds_read_b128 v[212:215], v223 offset:22528
	ds_read_b128 v[216:219], v223 offset:23552
	global_load_lds_dwordx4 v[170:171], off
	v_lshl_add_u64 v[174:175], s[30:31], 0, v[190:191]
	s_mov_b32 m0, s65
	s_addc_u32 s77, s31, 0
	global_load_lds_dwordx4 v[174:175], off
	v_lshl_add_u64 v[224:225], s[76:77], 0, v[34:35]
	s_mov_b32 m0, s66
	v_lshl_add_u64 v[226:227], s[40:41], 0, v[192:193]
	global_load_lds_dwordx4 v[224:225], off
	v_lshl_add_u64 v[224:225], s[76:77], 0, v[190:191]
	s_mov_b32 m0, s67
	s_nop 0
	global_load_lds_dwordx4 v[224:225], off
	v_lshl_add_u64 v[224:225], s[40:41], 0, v[194:195]
	s_mov_b32 m0, s43
	s_nop 0
	global_load_lds_dwordx4 v[224:225], off
	s_mov_b32 m0, s44
	s_nop 0
	global_load_lds_dwordx4 v[226:227], off
	s_waitcnt vmcnt(8)
	s_waitcnt lgkmcnt(0)
	s_barrier
	v_mfma_f32_16x16x32_bf16 v[64:67], v[134:137], v[166:169], v[64:67]
	s_setprio 1
	v_mfma_f32_16x16x32_bf16 v[60:63], v[142:145], v[166:169], v[60:63]
	v_mfma_f32_16x16x32_bf16 v[52:55], v[142:145], v[182:185], v[52:55]
	v_mfma_f32_16x16x32_bf16 v[56:59], v[134:137], v[182:185], v[56:59]
	v_mfma_f32_16x16x32_bf16 v[48:51], v[134:137], v[204:207], v[48:51]
	v_mfma_f32_16x16x32_bf16 v[44:47], v[142:145], v[204:207], v[44:47]
	v_mfma_f32_16x16x32_bf16 v[36:39], v[142:145], v[212:215], v[36:39]
	v_mfma_f32_16x16x32_bf16 v[40:43], v[134:137], v[212:215], v[40:43]
	v_mfma_f32_16x16x32_bf16 v[64:67], v[138:141], v[178:181], v[64:67]
	v_mfma_f32_16x16x32_bf16 v[60:63], v[146:149], v[178:181], v[60:63]
	v_mfma_f32_16x16x32_bf16 v[52:55], v[146:149], v[200:203], v[52:55]
	v_mfma_f32_16x16x32_bf16 v[56:59], v[138:141], v[200:203], v[56:59]
	v_mfma_f32_16x16x32_bf16 v[48:51], v[138:141], v[208:211], v[48:51]
	v_mfma_f32_16x16x32_bf16 v[44:47], v[146:149], v[208:211], v[44:47]
	v_mfma_f32_16x16x32_bf16 v[36:39], v[146:149], v[216:219], v[36:39]
	v_mfma_f32_16x16x32_bf16 v[40:43], v[138:141], v[216:219], v[40:43]
	s_setprio 0
	s_setprio 1
	v_mfma_f32_16x16x32_bf16 v[30:33], v[150:153], v[166:169], v[30:33]
	v_mfma_f32_16x16x32_bf16 v[26:29], v[158:161], v[166:169], v[26:29]
	v_mfma_f32_16x16x32_bf16 v[18:21], v[158:161], v[182:185], v[18:21]
	v_mfma_f32_16x16x32_bf16 v[22:25], v[150:153], v[182:185], v[22:25]
	v_mfma_f32_16x16x32_bf16 v[14:17], v[150:153], v[204:207], v[14:17]
	v_mfma_f32_16x16x32_bf16 v[10:13], v[158:161], v[204:207], v[10:13]
	v_mfma_f32_16x16x32_bf16 v[2:5], v[158:161], v[212:215], v[2:5]
	v_mfma_f32_16x16x32_bf16 v[6:9], v[150:153], v[212:215], v[6:9]
	v_mfma_f32_16x16x32_bf16 v[30:33], v[154:157], v[178:181], v[30:33]
	v_mfma_f32_16x16x32_bf16 v[26:29], v[162:165], v[178:181], v[26:29]
	v_mfma_f32_16x16x32_bf16 v[18:21], v[162:165], v[200:203], v[18:21]
	v_mfma_f32_16x16x32_bf16 v[22:25], v[154:157], v[200:203], v[22:25]
	v_mfma_f32_16x16x32_bf16 v[14:17], v[154:157], v[208:211], v[14:17]
	v_mfma_f32_16x16x32_bf16 v[10:13], v[162:165], v[208:211], v[10:13]
	v_mfma_f32_16x16x32_bf16 v[2:5], v[162:165], v[216:219], v[2:5]
	s_barrier
	v_mfma_f32_16x16x32_bf16 v[6:9], v[154:157], v[216:219], v[6:9]
	s_setprio 0
	ds_read_b128 v[134:137], v132
	ds_read_b128 v[138:141], v132 offset:1024
	ds_read_b128 v[142:145], v132 offset:2048
	ds_read_b128 v[146:149], v132 offset:3072
	ds_read_b128 v[150:153], v133
	ds_read_b128 v[154:157], v133 offset:1024
	ds_read_b128 v[158:161], v133 offset:2048
	ds_read_b128 v[162:165], v133 offset:3072
	s_add_u32 s40, s40, 0x40000
	s_addc_u32 s41, s41, 0
	s_mov_b32 m0, s45
	v_lshl_add_u64 v[228:229], s[40:41], 0, v[194:195]
	ds_read_b128 v[166:169], v223 offset:32768
	ds_read_b128 v[178:181], v223 offset:33792
	ds_read_b128 v[182:185], v223 offset:34816
	ds_read_b128 v[200:203], v223 offset:35840
	ds_read_b128 v[204:207], v223 offset:36864
	ds_read_b128 v[208:211], v223 offset:37888
	ds_read_b128 v[212:215], v223 offset:38912
	ds_read_b128 v[216:219], v223 offset:39936
	global_load_lds_dwordx4 v[228:229], off
	v_lshl_add_u64 v[228:229], s[40:41], 0, v[192:193]
	s_mov_b32 m0, s46
	s_nop 0
	global_load_lds_dwordx4 v[228:229], off
	s_waitcnt vmcnt(8)
	s_waitcnt lgkmcnt(0)
	s_barrier
	v_mfma_f32_16x16x32_bf16 v[128:131], v[134:137], v[166:169], v[128:131]
	s_setprio 1
	v_mfma_f32_16x16x32_bf16 v[124:127], v[142:145], v[166:169], v[124:127]
	v_mfma_f32_16x16x32_bf16 v[116:119], v[142:145], v[182:185], v[116:119]
	v_mfma_f32_16x16x32_bf16 v[120:123], v[134:137], v[182:185], v[120:123]
	v_mfma_f32_16x16x32_bf16 v[112:115], v[134:137], v[204:207], v[112:115]
	v_mfma_f32_16x16x32_bf16 v[108:111], v[142:145], v[204:207], v[108:111]
	v_mfma_f32_16x16x32_bf16 v[100:103], v[142:145], v[212:215], v[100:103]
	v_mfma_f32_16x16x32_bf16 v[104:107], v[134:137], v[212:215], v[104:107]
	v_mfma_f32_16x16x32_bf16 v[128:131], v[138:141], v[178:181], v[128:131]
	v_mfma_f32_16x16x32_bf16 v[124:127], v[146:149], v[178:181], v[124:127]
	v_mfma_f32_16x16x32_bf16 v[116:119], v[146:149], v[200:203], v[116:119]
	v_mfma_f32_16x16x32_bf16 v[120:123], v[138:141], v[200:203], v[120:123]
	v_mfma_f32_16x16x32_bf16 v[112:115], v[138:141], v[208:211], v[112:115]
	v_mfma_f32_16x16x32_bf16 v[108:111], v[146:149], v[208:211], v[108:111]
	v_mfma_f32_16x16x32_bf16 v[100:103], v[146:149], v[216:219], v[100:103]
	v_mfma_f32_16x16x32_bf16 v[104:107], v[138:141], v[216:219], v[104:107]
	s_setprio 0
	s_setprio 1
	v_mfma_f32_16x16x32_bf16 v[96:99], v[150:153], v[166:169], v[96:99]
	v_mfma_f32_16x16x32_bf16 v[92:95], v[158:161], v[166:169], v[92:95]
	v_mfma_f32_16x16x32_bf16 v[84:87], v[158:161], v[182:185], v[84:87]
	v_mfma_f32_16x16x32_bf16 v[88:91], v[150:153], v[182:185], v[88:91]
	v_mfma_f32_16x16x32_bf16 v[80:83], v[150:153], v[204:207], v[80:83]
	v_mfma_f32_16x16x32_bf16 v[76:79], v[158:161], v[204:207], v[76:79]
	v_mfma_f32_16x16x32_bf16 v[68:71], v[158:161], v[212:215], v[68:71]
	v_mfma_f32_16x16x32_bf16 v[72:75], v[150:153], v[212:215], v[72:75]
	v_mfma_f32_16x16x32_bf16 v[96:99], v[154:157], v[178:181], v[96:99]
	v_mfma_f32_16x16x32_bf16 v[92:95], v[162:165], v[178:181], v[92:95]
	v_mfma_f32_16x16x32_bf16 v[84:87], v[162:165], v[200:203], v[84:87]
	v_mfma_f32_16x16x32_bf16 v[88:91], v[154:157], v[200:203], v[88:91]
	v_mfma_f32_16x16x32_bf16 v[80:83], v[154:157], v[208:211], v[80:83]
	v_mfma_f32_16x16x32_bf16 v[76:79], v[162:165], v[208:211], v[76:79]
	v_mfma_f32_16x16x32_bf16 v[68:71], v[162:165], v[216:219], v[68:71]
	s_barrier
	v_mfma_f32_16x16x32_bf16 v[72:75], v[154:157], v[216:219], v[72:75]
	s_setprio 0
	s_mov_b32 m0, s68
	v_lshl_add_u64 v[170:171], v[170:171], 0, s[18:19]
	s_add_u32 s30, s30, 0x40080
	ds_read_b128 v[166:169], v223 offset:49152
	ds_read_b128 v[178:181], v223 offset:50176
	ds_read_b128 v[182:185], v223 offset:51200
	ds_read_b128 v[200:203], v223 offset:52224
	ds_read_b128 v[204:207], v223 offset:53248
	ds_read_b128 v[208:211], v223 offset:54272
	ds_read_b128 v[212:215], v223 offset:55296
	ds_read_b128 v[216:219], v223 offset:56320
	global_load_lds_dwordx4 v[170:171], off
	v_lshl_add_u64 v[170:171], v[174:175], 0, s[18:19]
	s_mov_b32 m0, s69
	s_addc_u32 s31, s31, 0
	global_load_lds_dwordx4 v[170:171], off
	v_lshl_add_u64 v[170:171], s[30:31], 0, v[34:35]
	s_mov_b32 m0, s70
	s_nop 0
	global_load_lds_dwordx4 v[170:171], off
	v_lshl_add_u64 v[170:171], s[30:31], 0, v[190:191]
	s_mov_b32 m0, s71
	s_nop 0
	global_load_lds_dwordx4 v[170:171], off
	v_lshl_add_u64 v[170:171], v[224:225], 0, s[18:19]
	s_mov_b32 m0, s51
	s_nop 0
	global_load_lds_dwordx4 v[170:171], off
	v_lshl_add_u64 v[170:171], v[226:227], 0, s[18:19]
	s_mov_b32 m0, s52
	s_nop 0
	global_load_lds_dwordx4 v[170:171], off
	s_waitcnt vmcnt(8)
	s_waitcnt lgkmcnt(0)
	s_barrier
	v_mfma_f32_16x16x32_bf16 v[64:67], v[134:137], v[166:169], v[64:67]
	s_setprio 1
	v_mfma_f32_16x16x32_bf16 v[60:63], v[142:145], v[166:169], v[60:63]
	v_mfma_f32_16x16x32_bf16 v[52:55], v[142:145], v[182:185], v[52:55]
	v_mfma_f32_16x16x32_bf16 v[56:59], v[134:137], v[182:185], v[56:59]
	v_mfma_f32_16x16x32_bf16 v[48:51], v[134:137], v[204:207], v[48:51]
	v_mfma_f32_16x16x32_bf16 v[44:47], v[142:145], v[204:207], v[44:47]
	v_mfma_f32_16x16x32_bf16 v[36:39], v[142:145], v[212:215], v[36:39]
	v_mfma_f32_16x16x32_bf16 v[40:43], v[134:137], v[212:215], v[40:43]
	v_mfma_f32_16x16x32_bf16 v[64:67], v[138:141], v[178:181], v[64:67]
	v_mfma_f32_16x16x32_bf16 v[60:63], v[146:149], v[178:181], v[60:63]
	v_mfma_f32_16x16x32_bf16 v[52:55], v[146:149], v[200:203], v[52:55]
	v_mfma_f32_16x16x32_bf16 v[56:59], v[138:141], v[200:203], v[56:59]
	v_mfma_f32_16x16x32_bf16 v[48:51], v[138:141], v[208:211], v[48:51]
	v_mfma_f32_16x16x32_bf16 v[44:47], v[146:149], v[208:211], v[44:47]
	v_mfma_f32_16x16x32_bf16 v[36:39], v[146:149], v[216:219], v[36:39]
	v_mfma_f32_16x16x32_bf16 v[40:43], v[138:141], v[216:219], v[40:43]
	s_setprio 0
	s_setprio 1
	v_mfma_f32_16x16x32_bf16 v[30:33], v[150:153], v[166:169], v[30:33]
	v_mfma_f32_16x16x32_bf16 v[26:29], v[158:161], v[166:169], v[26:29]
	v_mfma_f32_16x16x32_bf16 v[18:21], v[158:161], v[182:185], v[18:21]
	v_mfma_f32_16x16x32_bf16 v[22:25], v[150:153], v[182:185], v[22:25]
	v_mfma_f32_16x16x32_bf16 v[14:17], v[150:153], v[204:207], v[14:17]
	v_mfma_f32_16x16x32_bf16 v[10:13], v[158:161], v[204:207], v[10:13]
	v_mfma_f32_16x16x32_bf16 v[2:5], v[158:161], v[212:215], v[2:5]
	v_mfma_f32_16x16x32_bf16 v[6:9], v[150:153], v[212:215], v[6:9]
	v_mfma_f32_16x16x32_bf16 v[30:33], v[154:157], v[178:181], v[30:33]
	v_mfma_f32_16x16x32_bf16 v[26:29], v[162:165], v[178:181], v[26:29]
	v_mfma_f32_16x16x32_bf16 v[18:21], v[162:165], v[200:203], v[18:21]
	v_mfma_f32_16x16x32_bf16 v[22:25], v[154:157], v[200:203], v[22:25]
	v_mfma_f32_16x16x32_bf16 v[14:17], v[154:157], v[208:211], v[14:17]
	v_mfma_f32_16x16x32_bf16 v[10:13], v[162:165], v[208:211], v[10:13]
	v_mfma_f32_16x16x32_bf16 v[2:5], v[162:165], v[216:219], v[2:5]
	s_barrier
	v_mfma_f32_16x16x32_bf16 v[6:9], v[154:157], v[216:219], v[6:9]
	s_setprio 0
	s_add_i32 s74, s74, 2
	s_add_u32 s36, s36, 0x100
	s_addc_u32 s37, s37, 0
	s_add_u32 s72, s72, 0x100
	s_addc_u32 s73, s73, 0
	s_cmp_gt_u32 s74, 13
	s_cbranch_scc0 .LBB0_541
	v_readlane_b32 s74, v255, 3
	s_and_b64 vcc, exec, s[10:11]
	v_readlane_b32 s75, v255, 4
	s_mov_b32 s58, 0x19b00000
	v_readlane_b32 s59, v255, 10
	s_mov_b32 s60, 0xff61b1e6
	s_mov_b64 s[62:63], 0x800
	s_mov_b32 s64, 0x3b000000
	s_cbranch_vccz .LBB0_544
	s_barrier

.LBB0_819:
	s_add_u32 s81, s30, 0x200
	s_addc_u32 s82, s31, 0
	s_add_i32 s55, 0, 0x14000
	s_add_i32 s52, 0, 0x10000
	v_add_u32_e32 v199, s55, v167
	v_add_u32_e32 v200, s52, v167
	ds_read_b128 v[10:13], v199
	ds_read_b128 v[14:17], v199 offset:1024
	ds_read_b128 v[2:5], v199 offset:2048
	ds_read_b128 v[6:9], v199 offset:3072
	ds_read_b128 v[22:25], v200 offset:3072
	ds_read_b128 v[18:21], v200 offset:2048
	ds_read_b128 v[30:33], v200 offset:1024
	ds_read_b128 v[26:29], v200
	s_lshl_b32 s14, s80, 10
	s_add_i32 s83, s14, 0
	s_add_i32 s83, s83, 0x20400
	v_mov_b32_e32 v191, v35
	v_mov_b32_e32 v175, v35
	s_add_i32 s84, s69, 0xc000
	v_readlane_b32 s26, v253, 28
	s_mov_b32 m0, s84
	v_readlane_b32 s27, v253, 29
	s_add_i32 s53, s69, 0xe000
	ds_read_b128 v[202:205], v169
	ds_read_b128 v[206:209], v169 offset:1024
	ds_read_b128 v[222:225], v169 offset:2048
	ds_read_b128 v[226:229], v169 offset:3072
	ds_read_b128 v[230:233], v169 offset:4096
	ds_read_b128 v[234:237], v169 offset:5120
	ds_read_b128 v[238:241], v169 offset:6144
	ds_read_b128 v[242:245], v169 offset:7168
	global_load_lds_dwordx4 v190, s[26:27]
	s_mov_b32 m0, s53
	s_nop 0
	global_load_lds_dwordx4 v174, s[26:27]
	s_waitcnt vmcnt(8)
	s_waitcnt lgkmcnt(0)
	s_barrier
	v_mfma_f32_16x16x128_f8f6f4 v[160:163], v[26:33], v[202:209], 0
	s_setprio 1
	v_mfma_f32_16x16x128_f8f6f4 v[156:159], v[18:25], v[202:209], 0
	v_mfma_f32_16x16x128_f8f6f4 v[148:151], v[18:25], v[222:229], 0
	v_mfma_f32_16x16x128_f8f6f4 v[152:155], v[26:33], v[222:229], 0
	v_mfma_f32_16x16x128_f8f6f4 v[144:147], v[26:33], v[230:237], 0
	v_mfma_f32_16x16x128_f8f6f4 v[140:143], v[18:25], v[230:237], 0
	v_mfma_f32_16x16x128_f8f6f4 v[132:135], v[18:25], v[238:245], 0
	v_mfma_f32_16x16x128_f8f6f4 v[136:139], v[26:33], v[238:245], 0
	s_setprio 0
	s_setprio 1
	v_mfma_f32_16x16x128_f8f6f4 v[128:131], v[10:17], v[202:209], 0
	v_mfma_f32_16x16x128_f8f6f4 v[124:127], v[2:9], v[202:209], 0
	v_mfma_f32_16x16x128_f8f6f4 v[116:119], v[2:9], v[222:229], 0
	v_mfma_f32_16x16x128_f8f6f4 v[120:123], v[10:17], v[222:229], 0
	v_mfma_f32_16x16x128_f8f6f4 v[112:115], v[10:17], v[230:237], 0
	v_mfma_f32_16x16x128_f8f6f4 v[108:111], v[2:9], v[230:237], 0
	v_mfma_f32_16x16x128_f8f6f4 v[100:103], v[2:9], v[238:245], 0
	s_barrier
	v_mfma_f32_16x16x128_f8f6f4 v[104:107], v[10:17], v[238:245], 0
	s_setprio 0
	s_add_i32 s52, s52, s68
	v_lshl_add_u64 v[194:195], s[30:31], 0, v[170:171]
	s_add_i32 s85, s52, 0x2000
	v_lshl_add_u64 v[178:179], v[194:195], 0, s[28:29]
	s_mov_b32 m0, s52
	v_lshl_add_u64 v[196:197], s[30:31], 0, v[172:173]
	s_add_u32 s36, s30, 0x20100
	ds_read_b128 v[202:205], v169 offset:16384
	ds_read_b128 v[206:209], v169 offset:17408
	ds_read_b128 v[222:225], v169 offset:18432
	ds_read_b128 v[226:229], v169 offset:19456
	ds_read_b128 v[230:233], v169 offset:20480
	ds_read_b128 v[234:237], v169 offset:21504
	ds_read_b128 v[238:241], v169 offset:22528
	ds_read_b128 v[242:245], v169 offset:23552
	global_load_lds_dwordx4 v[178:179], off
	v_lshl_add_u64 v[178:179], v[196:197], 0, s[28:29]
	s_mov_b32 m0, s85
	s_addc_u32 s37, s31, 0
	s_add_i32 s55, s55, s68
	global_load_lds_dwordx4 v[178:179], off
	v_lshl_add_u64 v[178:179], s[36:37], 0, v[170:171]
	s_mov_b32 m0, s55
	s_add_i32 s65, s55, 0x2000
	global_load_lds_dwordx4 v[178:179], off
	v_lshl_add_u64 v[178:179], s[36:37], 0, v[172:173]
	s_mov_b32 m0, s65
	v_readlane_b32 s26, v253, 37
	global_load_lds_dwordx4 v[178:179], off
	s_mov_b32 m0, s69
	v_readlane_b32 s27, v253, 38
	s_nop 4
	global_load_lds_dwordx4 v34, s[26:27]
	s_mov_b32 m0, s70
	s_nop 0
	global_load_lds_dwordx4 v192, s[26:27]
	s_waitcnt vmcnt(8)
	s_waitcnt lgkmcnt(0)
	s_barrier
	v_mfma_f32_16x16x128_f8f6f4 v[96:99], v[26:33], v[202:209], 0
	s_setprio 1
	v_mfma_f32_16x16x128_f8f6f4 v[92:95], v[18:25], v[202:209], 0
	v_mfma_f32_16x16x128_f8f6f4 v[84:87], v[18:25], v[222:229], 0
	v_mfma_f32_16x16x128_f8f6f4 v[88:91], v[26:33], v[222:229], 0
	v_mfma_f32_16x16x128_f8f6f4 v[80:83], v[26:33], v[230:237], 0
	v_mfma_f32_16x16x128_f8f6f4 v[76:79], v[18:25], v[230:237], 0
	v_mfma_f32_16x16x128_f8f6f4 v[68:71], v[18:25], v[238:245], 0
	v_mfma_f32_16x16x128_f8f6f4 v[72:75], v[26:33], v[238:245], 0
	s_setprio 0
	s_setprio 1
	v_mfma_f32_16x16x128_f8f6f4 v[64:67], v[10:17], v[202:209], 0
	v_mfma_f32_16x16x128_f8f6f4 v[60:63], v[2:9], v[202:209], 0
	v_mfma_f32_16x16x128_f8f6f4 v[52:55], v[2:9], v[222:229], 0
	v_mfma_f32_16x16x128_f8f6f4 v[56:59], v[10:17], v[222:229], 0
	v_mfma_f32_16x16x128_f8f6f4 v[48:51], v[10:17], v[230:237], 0
	v_mfma_f32_16x16x128_f8f6f4 v[44:47], v[2:9], v[230:237], 0
	v_mfma_f32_16x16x128_f8f6f4 v[36:39], v[2:9], v[238:245], 0
	s_barrier
	v_mfma_f32_16x16x128_f8f6f4 v[40:43], v[10:17], v[238:245], 0
	s_setprio 0
	s_add_i32 s54, 0, 0x18000
	s_add_i32 s51, 0, 0x1c000
	v_add_u32_e32 v201, s54, v167
	v_add_u32_e32 v202, s51, v167
	ds_read_b128 v[26:29], v201
	ds_read_b128 v[30:33], v201 offset:1024
	ds_read_b128 v[18:21], v201 offset:2048
	ds_read_b128 v[22:25], v201 offset:3072
	ds_read_b128 v[10:13], v202
	ds_read_b128 v[14:17], v202 offset:1024
	ds_read_b128 v[2:5], v202 offset:2048
	ds_read_b128 v[6:9], v202 offset:3072
	s_mov_b32 m0, s71
	ds_read_b128 v[204:207], v169 offset:32768
	ds_read_b128 v[208:211], v169 offset:33792
	ds_read_b128 v[222:225], v169 offset:34816
	ds_read_b128 v[226:229], v169 offset:35840
	ds_read_b128 v[230:233], v169 offset:36864
	ds_read_b128 v[234:237], v169 offset:37888
	ds_read_b128 v[238:241], v169 offset:38912
	ds_read_b128 v[242:245], v169 offset:39936
	global_load_lds_dwordx4 v189, s[26:27]
	s_mov_b32 m0, s72
	s_nop 0
	global_load_lds_dwordx4 v198, s[26:27]
	s_waitcnt vmcnt(8)
	s_waitcnt lgkmcnt(0)
	s_barrier
	v_mfma_f32_16x16x128_f8f6f4 v[160:163], v[26:33], v[204:211], v[160:163]
	s_setprio 1
	v_mfma_f32_16x16x128_f8f6f4 v[156:159], v[18:25], v[204:211], v[156:159]
	v_mfma_f32_16x16x128_f8f6f4 v[148:151], v[18:25], v[222:229], v[148:151]
	v_mfma_f32_16x16x128_f8f6f4 v[152:155], v[26:33], v[222:229], v[152:155]
	v_mfma_f32_16x16x128_f8f6f4 v[144:147], v[26:33], v[230:237], v[144:147]
	v_mfma_f32_16x16x128_f8f6f4 v[140:143], v[18:25], v[230:237], v[140:143]
	v_mfma_f32_16x16x128_f8f6f4 v[132:135], v[18:25], v[238:245], v[132:135]
	v_mfma_f32_16x16x128_f8f6f4 v[136:139], v[26:33], v[238:245], v[136:139]
	s_setprio 0
	s_setprio 1
	v_mfma_f32_16x16x128_f8f6f4 v[128:131], v[10:17], v[204:211], v[128:131]
	v_mfma_f32_16x16x128_f8f6f4 v[124:127], v[2:9], v[204:211], v[124:127]
	v_mfma_f32_16x16x128_f8f6f4 v[116:119], v[2:9], v[222:229], v[116:119]
	v_mfma_f32_16x16x128_f8f6f4 v[120:123], v[10:17], v[222:229], v[120:123]
	v_mfma_f32_16x16x128_f8f6f4 v[112:115], v[10:17], v[230:237], v[112:115]
	v_mfma_f32_16x16x128_f8f6f4 v[108:111], v[2:9], v[230:237], v[108:111]
	v_mfma_f32_16x16x128_f8f6f4 v[100:103], v[2:9], v[238:245], v[100:103]
	s_barrier
	v_mfma_f32_16x16x128_f8f6f4 v[104:107], v[10:17], v[238:245], v[104:107]
	s_setprio 0
	s_add_i32 s54, s54, s68
	s_mov_b64 s[26:27], 0x180
	s_add_i32 s50, s54, 0x2000
	v_lshl_add_u64 v[178:179], v[194:195], 0, s[26:27]
	s_mov_b32 m0, s54
	s_add_u32 s30, s30, 0x20180
	ds_read_b128 v[204:207], v169 offset:49152
	ds_read_b128 v[208:211], v169 offset:50176
	ds_read_b128 v[222:225], v169 offset:51200
	ds_read_b128 v[226:229], v169 offset:52224
	ds_read_b128 v[230:233], v169 offset:53248
	ds_read_b128 v[234:237], v169 offset:54272
	ds_read_b128 v[238:241], v169 offset:55296
	ds_read_b128 v[242:245], v169 offset:56320
	global_load_lds_dwordx4 v[178:179], off
	v_lshl_add_u64 v[178:179], v[196:197], 0, s[26:27]
	s_mov_b32 m0, s50
	s_addc_u32 s31, s31, 0
	s_add_i32 s51, s51, s68
	global_load_lds_dwordx4 v[178:179], off
	v_lshl_add_u64 v[178:179], s[30:31], 0, v[170:171]
	s_mov_b32 m0, s51
	s_add_i32 s64, s51, 0x2000
	global_load_lds_dwordx4 v[178:179], off
	v_lshl_add_u64 v[178:179], s[30:31], 0, v[172:173]
	s_mov_b32 m0, s64
	v_readlane_b32 s26, v253, 39
	global_load_lds_dwordx4 v[178:179], off
	s_mov_b32 m0, s75
	v_readlane_b32 s27, v253, 40
	s_nop 4
	global_load_lds_dwordx4 v34, s[26:27]
	s_mov_b32 m0, s76
	s_nop 0
	global_load_lds_dwordx4 v192, s[26:27]
	s_waitcnt vmcnt(8)
	s_waitcnt lgkmcnt(0)
	s_barrier
	v_mfma_f32_16x16x128_f8f6f4 v[96:99], v[26:33], v[204:211], v[96:99]
	s_setprio 1
	v_mfma_f32_16x16x128_f8f6f4 v[92:95], v[18:25], v[204:211], v[92:95]
	v_mfma_f32_16x16x128_f8f6f4 v[84:87], v[18:25], v[222:229], v[84:87]
	v_mfma_f32_16x16x128_f8f6f4 v[88:91], v[26:33], v[222:229], v[88:91]
	v_mfma_f32_16x16x128_f8f6f4 v[80:83], v[26:33], v[230:237], v[80:83]
	v_mfma_f32_16x16x128_f8f6f4 v[76:79], v[18:25], v[230:237], v[76:79]
	v_mfma_f32_16x16x128_f8f6f4 v[68:71], v[18:25], v[238:245], v[68:71]
	v_mfma_f32_16x16x128_f8f6f4 v[72:75], v[26:33], v[238:245], v[72:75]
	s_setprio 0
	s_setprio 1
	v_mfma_f32_16x16x128_f8f6f4 v[64:67], v[10:17], v[204:211], v[64:67]
	v_mfma_f32_16x16x128_f8f6f4 v[60:63], v[2:9], v[204:211], v[60:63]
	v_mfma_f32_16x16x128_f8f6f4 v[52:55], v[2:9], v[222:229], v[52:55]
	v_mfma_f32_16x16x128_f8f6f4 v[56:59], v[10:17], v[222:229], v[56:59]
	v_mfma_f32_16x16x128_f8f6f4 v[48:51], v[10:17], v[230:237], v[48:51]
	v_mfma_f32_16x16x128_f8f6f4 v[44:47], v[2:9], v[230:237], v[44:47]
	v_mfma_f32_16x16x128_f8f6f4 v[36:39], v[2:9], v[238:245], v[36:39]
	s_barrier
	v_mfma_f32_16x16x128_f8f6f4 v[40:43], v[10:17], v[238:245], v[40:43]
	s_setprio 0
	v_lshl_add_u64 v[18:19], s[26:27], 0, v[174:175]
	v_lshl_add_u64 v[20:21], s[26:27], 0, v[190:191]
	s_mov_b32 s63, 0
	s_mov_b64 s[30:31], 0
	s_branch .LBB0_821
.LBB0_820:
	ds_read_b128 v[204:207], v200
	ds_read_b128 v[208:211], v200 offset:1024
	ds_read_b128 v[222:225], v200 offset:2048
	ds_read_b128 v[226:229], v200 offset:3072
	ds_read_b128 v[10:13], v199
	ds_read_b128 v[14:17], v199 offset:1024
	ds_read_b128 v[2:5], v199 offset:2048
	ds_read_b128 v[6:9], v199 offset:3072
	s_add_u32 s14, s30, 0x200
	s_addc_u32 s86, s31, 0
	s_and_b64 s[40:41], s[36:37], exec
	s_cselect_b32 s14, 0, s14
	s_cselect_b32 s41, 0, s86
	s_add_u32 s40, s20, s14
	s_addc_u32 s41, s21, s41
	s_add_u32 s14, s81, s30
	s_addc_u32 s86, s82, s31
	s_and_b64 s[36:37], s[36:37], exec
	s_cselect_b32 s37, s23, s86
	s_cselect_b32 s36, s22, s14
	s_mov_b32 m0, s84
	v_lshl_add_u64 v[30:31], v[20:21], 0, s[30:31]
	ds_read_b128 v[22:25], v169
	ds_read_b128 v[26:29], v169 offset:1024
	ds_read_b128 v[230:233], v169 offset:2048
	ds_read_b128 v[234:237], v169 offset:3072
	ds_read_b128 v[238:241], v169 offset:4096
	ds_read_b128 v[242:245], v169 offset:5120
	ds_read_b128 v[178:181], v169 offset:6144
	ds_read_b128 v[182:185], v169 offset:7168
	global_load_lds_dwordx4 v[30:31], off
	v_lshl_add_u64 v[30:31], v[18:19], 0, s[30:31]
	s_mov_b32 m0, s53
	s_nop 0
	global_load_lds_dwordx4 v[30:31], off
	s_waitcnt vmcnt(8)
	s_waitcnt lgkmcnt(0)
	s_barrier
	v_mfma_f32_16x16x128_f8f6f4 v[160:163], v[204:211], v[22:29], v[160:163]
	s_setprio 1
	v_mfma_f32_16x16x128_f8f6f4 v[156:159], v[222:229], v[22:29], v[156:159]
	v_mfma_f32_16x16x128_f8f6f4 v[148:151], v[222:229], v[230:237], v[148:151]
	v_mfma_f32_16x16x128_f8f6f4 v[152:155], v[204:211], v[230:237], v[152:155]
	v_mfma_f32_16x16x128_f8f6f4 v[144:147], v[204:211], v[238:245], v[144:147]
	v_mfma_f32_16x16x128_f8f6f4 v[140:143], v[222:229], v[238:245], v[140:143]
	v_mfma_f32_16x16x128_f8f6f4 v[132:135], v[222:229], v[178:185], v[132:135]
	v_mfma_f32_16x16x128_f8f6f4 v[136:139], v[204:211], v[178:185], v[136:139]
	s_setprio 0
	s_setprio 1
	v_mfma_f32_16x16x128_f8f6f4 v[128:131], v[10:17], v[22:29], v[128:131]
	v_mfma_f32_16x16x128_f8f6f4 v[124:127], v[2:9], v[22:29], v[124:127]
	v_mfma_f32_16x16x128_f8f6f4 v[116:119], v[2:9], v[230:237], v[116:119]
	v_mfma_f32_16x16x128_f8f6f4 v[120:123], v[10:17], v[230:237], v[120:123]
	v_mfma_f32_16x16x128_f8f6f4 v[112:115], v[10:17], v[238:245], v[112:115]
	v_mfma_f32_16x16x128_f8f6f4 v[108:111], v[2:9], v[238:245], v[108:111]
	v_mfma_f32_16x16x128_f8f6f4 v[100:103], v[2:9], v[178:185], v[100:103]
	s_barrier
	v_mfma_f32_16x16x128_f8f6f4 v[104:107], v[10:17], v[178:185], v[104:107]
	s_setprio 0
	s_mov_b32 m0, s52
	v_lshl_add_u64 v[22:23], s[36:37], 0, v[170:171]
	s_add_u32 s86, s36, 0x20000
	ds_read_b128 v[178:181], v169 offset:16384
	ds_read_b128 v[182:185], v169 offset:17408
	ds_read_b128 v[230:233], v169 offset:18432
	ds_read_b128 v[234:237], v169 offset:19456
	ds_read_b128 v[238:241], v169 offset:20480
	ds_read_b128 v[242:245], v169 offset:21504
	ds_read_b128 v[212:215], v169 offset:22528
	ds_read_b128 v[216:219], v169 offset:23552
	global_load_lds_dwordx4 v[22:23], off
	v_lshl_add_u64 v[24:25], s[36:37], 0, v[172:173]
	s_mov_b32 m0, s85
	s_addc_u32 s87, s37, 0
	global_load_lds_dwordx4 v[24:25], off
	v_lshl_add_u64 v[26:27], s[86:87], 0, v[170:171]
	s_mov_b32 m0, s55
	v_mov_b32_e32 v193, v35
	global_load_lds_dwordx4 v[26:27], off
	v_lshl_add_u64 v[26:27], s[86:87], 0, v[172:173]
	s_mov_b32 m0, s65
	v_lshl_add_u64 v[28:29], s[40:41], 0, v[34:35]
	global_load_lds_dwordx4 v[26:27], off
	s_mov_b32 m0, s69
	v_lshl_add_u64 v[26:27], s[40:41], 0, v[192:193]
	global_load_lds_dwordx4 v34, s[40:41]
	s_mov_b32 m0, s70
	s_nop 0
	global_load_lds_dwordx4 v192, s[40:41]
	s_waitcnt vmcnt(8)
	s_waitcnt lgkmcnt(0)
	s_barrier
	v_mfma_f32_16x16x128_f8f6f4 v[96:99], v[204:211], v[178:185], v[96:99]
	s_setprio 1
	v_mfma_f32_16x16x128_f8f6f4 v[92:95], v[222:229], v[178:185], v[92:95]
	v_mfma_f32_16x16x128_f8f6f4 v[84:87], v[222:229], v[230:237], v[84:87]
	v_mfma_f32_16x16x128_f8f6f4 v[88:91], v[204:211], v[230:237], v[88:91]
	v_mfma_f32_16x16x128_f8f6f4 v[80:83], v[204:211], v[238:245], v[80:83]
	v_mfma_f32_16x16x128_f8f6f4 v[76:79], v[222:229], v[238:245], v[76:79]
	v_mfma_f32_16x16x128_f8f6f4 v[68:71], v[222:229], v[212:219], v[68:71]
	v_mfma_f32_16x16x128_f8f6f4 v[72:75], v[204:211], v[212:219], v[72:75]
	s_setprio 0
	s_setprio 1
	v_mfma_f32_16x16x128_f8f6f4 v[64:67], v[10:17], v[178:185], v[64:67]
	v_mfma_f32_16x16x128_f8f6f4 v[60:63], v[2:9], v[178:185], v[60:63]
	v_mfma_f32_16x16x128_f8f6f4 v[52:55], v[2:9], v[230:237], v[52:55]
	v_mfma_f32_16x16x128_f8f6f4 v[56:59], v[10:17], v[230:237], v[56:59]
	v_mfma_f32_16x16x128_f8f6f4 v[48:51], v[10:17], v[238:245], v[48:51]
	v_mfma_f32_16x16x128_f8f6f4 v[44:47], v[2:9], v[238:245], v[44:47]
	v_mfma_f32_16x16x128_f8f6f4 v[36:39], v[2:9], v[212:219], v[36:39]
	s_barrier
	v_mfma_f32_16x16x128_f8f6f4 v[40:43], v[10:17], v[212:219], v[40:43]
	s_setprio 0
	ds_read_b128 v[178:181], v201
	ds_read_b128 v[182:185], v201 offset:1024
	ds_read_b128 v[204:207], v201 offset:2048
	ds_read_b128 v[208:211], v201 offset:3072
	ds_read_b128 v[10:13], v202
	ds_read_b128 v[14:17], v202 offset:1024
	ds_read_b128 v[2:5], v202 offset:2048
	ds_read_b128 v[6:9], v202 offset:3072
	s_mov_b32 m0, s71
	ds_read_b128 v[212:215], v169 offset:32768
	ds_read_b128 v[216:219], v169 offset:33792
	ds_read_b128 v[222:225], v169 offset:34816
	ds_read_b128 v[226:229], v169 offset:35840
	ds_read_b128 v[230:233], v169 offset:36864
	ds_read_b128 v[234:237], v169 offset:37888
	ds_read_b128 v[238:241], v169 offset:38912
	ds_read_b128 v[242:245], v169 offset:39936
	global_load_lds_dwordx4 v189, s[40:41]
	s_mov_b32 m0, s72
	s_nop 0
	global_load_lds_dwordx4 v198, s[40:41]
	s_waitcnt vmcnt(8)
	s_waitcnt lgkmcnt(0)
	s_barrier
	v_mfma_f32_16x16x128_f8f6f4 v[160:163], v[178:185], v[212:219], v[160:163]
	s_setprio 1
	v_mfma_f32_16x16x128_f8f6f4 v[156:159], v[204:211], v[212:219], v[156:159]
	v_mfma_f32_16x16x128_f8f6f4 v[148:151], v[204:211], v[222:229], v[148:151]
	v_mfma_f32_16x16x128_f8f6f4 v[152:155], v[178:185], v[222:229], v[152:155]
	v_mfma_f32_16x16x128_f8f6f4 v[144:147], v[178:185], v[230:237], v[144:147]
	v_mfma_f32_16x16x128_f8f6f4 v[140:143], v[204:211], v[230:237], v[140:143]
	v_mfma_f32_16x16x128_f8f6f4 v[132:135], v[204:211], v[238:245], v[132:135]
	v_mfma_f32_16x16x128_f8f6f4 v[136:139], v[178:185], v[238:245], v[136:139]
	s_setprio 0
	s_setprio 1
	v_mfma_f32_16x16x128_f8f6f4 v[128:131], v[10:17], v[212:219], v[128:131]
	v_mfma_f32_16x16x128_f8f6f4 v[124:127], v[2:9], v[212:219], v[124:127]
	v_mfma_f32_16x16x128_f8f6f4 v[116:119], v[2:9], v[222:229], v[116:119]
	v_mfma_f32_16x16x128_f8f6f4 v[120:123], v[10:17], v[222:229], v[120:123]
	v_mfma_f32_16x16x128_f8f6f4 v[112:115], v[10:17], v[230:237], v[112:115]
	v_mfma_f32_16x16x128_f8f6f4 v[108:111], v[2:9], v[230:237], v[108:111]
	v_mfma_f32_16x16x128_f8f6f4 v[100:103], v[2:9], v[238:245], v[100:103]
	s_barrier
	v_mfma_f32_16x16x128_f8f6f4 v[104:107], v[10:17], v[238:245], v[104:107]
	s_setprio 0
	s_mov_b32 m0, s54
	v_lshl_add_u64 v[22:23], v[22:23], 0, s[18:19]
	s_add_u32 s36, s36, 0x20080
	ds_read_b128 v[212:215], v169 offset:49152
	ds_read_b128 v[216:219], v169 offset:50176
	ds_read_b128 v[222:225], v169 offset:51200
	ds_read_b128 v[226:229], v169 offset:52224
	ds_read_b128 v[230:233], v169 offset:53248
	ds_read_b128 v[234:237], v169 offset:54272
	ds_read_b128 v[238:241], v169 offset:55296
	ds_read_b128 v[242:245], v169 offset:56320
	global_load_lds_dwordx4 v[22:23], off
	v_lshl_add_u64 v[22:23], v[24:25], 0, s[18:19]
	s_mov_b32 m0, s50
	s_addc_u32 s37, s37, 0
	global_load_lds_dwordx4 v[22:23], off
	v_lshl_add_u64 v[22:23], s[36:37], 0, v[170:171]
	s_mov_b32 m0, s51
	s_nop 0
	global_load_lds_dwordx4 v[22:23], off
	v_lshl_add_u64 v[22:23], s[36:37], 0, v[172:173]
	s_mov_b32 m0, s64
	s_nop 0
	global_load_lds_dwordx4 v[22:23], off
	v_lshl_add_u64 v[22:23], v[28:29], 0, s[18:19]
	s_mov_b32 m0, s75
	s_nop 0
	global_load_lds_dwordx4 v[22:23], off
	v_lshl_add_u64 v[22:23], v[26:27], 0, s[18:19]
	s_mov_b32 m0, s76
	s_nop 0
	global_load_lds_dwordx4 v[22:23], off
	s_waitcnt vmcnt(8)
	s_waitcnt lgkmcnt(0)
	s_barrier
	v_mfma_f32_16x16x128_f8f6f4 v[96:99], v[178:185], v[212:219], v[96:99]
	s_setprio 1
	v_mfma_f32_16x16x128_f8f6f4 v[92:95], v[204:211], v[212:219], v[92:95]
	v_mfma_f32_16x16x128_f8f6f4 v[84:87], v[204:211], v[222:229], v[84:87]
	v_mfma_f32_16x16x128_f8f6f4 v[88:91], v[178:185], v[222:229], v[88:91]
	v_mfma_f32_16x16x128_f8f6f4 v[80:83], v[178:185], v[230:237], v[80:83]
	v_mfma_f32_16x16x128_f8f6f4 v[76:79], v[204:211], v[230:237], v[76:79]
	v_mfma_f32_16x16x128_f8f6f4 v[68:71], v[204:211], v[238:245], v[68:71]
	v_mfma_f32_16x16x128_f8f6f4 v[72:75], v[178:185], v[238:245], v[72:75]
	s_setprio 0
	s_setprio 1
	v_mfma_f32_16x16x128_f8f6f4 v[64:67], v[10:17], v[212:219], v[64:67]
	v_mfma_f32_16x16x128_f8f6f4 v[60:63], v[2:9], v[212:219], v[60:63]
	v_mfma_f32_16x16x128_f8f6f4 v[52:55], v[2:9], v[222:229], v[52:55]
	v_mfma_f32_16x16x128_f8f6f4 v[56:59], v[10:17], v[222:229], v[56:59]
	v_mfma_f32_16x16x128_f8f6f4 v[48:51], v[10:17], v[230:237], v[48:51]
	v_mfma_f32_16x16x128_f8f6f4 v[44:47], v[2:9], v[230:237], v[44:47]
	v_mfma_f32_16x16x128_f8f6f4 v[36:39], v[2:9], v[238:245], v[36:39]
	s_barrier
	v_mfma_f32_16x16x128_f8f6f4 v[40:43], v[10:17], v[238:245], v[40:43]
	s_setprio 0
	s_add_i32 s63, s63, 2
	s_add_u32 s30, s30, 0x100
	s_addc_u32 s31, s31, 0
	s_cmp_gt_u32 s63, 5
	s_cbranch_scc1 .LBB0_823

.LBB0_899:
	s_mul_i32 s14, s81, 0xe0000
	s_add_u32 s40, s44, s14
	s_addc_u32 s41, s45, 0
	s_and_b64 s[6:7], s[6:7], exec
	s_cselect_b32 s52, s41, s43
	s_cselect_b32 s53, s40, s42
	s_add_i32 s54, 0, 0x10000
	s_add_i32 s65, 0, 0x14000
	v_add_u32_e32 v34, s54, v167
	v_add_u32_e32 v206, s65, v167
	ds_read_b128 v[26:29], v34
	ds_read_b128 v[30:33], v34 offset:1024
	ds_read_b128 v[18:21], v34 offset:2048
	ds_read_b128 v[22:25], v34 offset:3072
	ds_read_b128 v[10:13], v206
	ds_read_b128 v[14:17], v206 offset:1024
	ds_read_b128 v[2:5], v206 offset:2048
	ds_read_b128 v[6:9], v206 offset:3072
	s_add_u32 s6, s42, 0x70080
	s_addc_u32 s7, s43, 0
	s_add_i32 s84, s72, 0xc000
	v_lshl_add_u64 v[216:217], s[6:7], 0, v[174:175]
	s_mov_b32 m0, s84
	s_add_i32 s85, s72, 0xe000
	ds_read_b128 v[178:181], v189
	ds_read_b128 v[182:185], v189 offset:1024
	ds_read_b128 v[198:201], v189 offset:2048
	ds_read_b128 v[202:205], v189 offset:3072
	ds_read_b128 v[208:211], v189 offset:4096
	ds_read_b128 v[212:215], v189 offset:5120
	ds_read_b128 v[222:225], v189 offset:6144
	ds_read_b128 v[226:229], v189 offset:7168
	global_load_lds_dwordx4 v[216:217], off
	v_lshl_add_u64 v[216:217], s[6:7], 0, v[170:171]
	s_mov_b32 m0, s85
	s_nop 0
	global_load_lds_dwordx4 v[216:217], off
	s_waitcnt vmcnt(8)
	s_waitcnt lgkmcnt(0)
	s_barrier
	v_mfma_f32_16x16x128_f8f6f4 v[160:163], v[26:33], v[178:185], 0
	s_setprio 1
	v_mfma_f32_16x16x128_f8f6f4 v[156:159], v[18:25], v[178:185], 0
	v_mfma_f32_16x16x128_f8f6f4 v[148:151], v[18:25], v[198:205], 0
	v_mfma_f32_16x16x128_f8f6f4 v[152:155], v[26:33], v[198:205], 0
	v_mfma_f32_16x16x128_f8f6f4 v[144:147], v[26:33], v[208:215], 0
	v_mfma_f32_16x16x128_f8f6f4 v[140:143], v[18:25], v[208:215], 0
	v_mfma_f32_16x16x128_f8f6f4 v[132:135], v[18:25], v[222:229], 0
	v_mfma_f32_16x16x128_f8f6f4 v[136:139], v[26:33], v[222:229], 0
	s_setprio 0
	s_setprio 1
	v_mfma_f32_16x16x128_f8f6f4 v[128:131], v[10:17], v[178:185], 0
	v_mfma_f32_16x16x128_f8f6f4 v[124:127], v[2:9], v[178:185], 0
	v_mfma_f32_16x16x128_f8f6f4 v[116:119], v[2:9], v[198:205], 0
	v_mfma_f32_16x16x128_f8f6f4 v[120:123], v[10:17], v[198:205], 0
	v_mfma_f32_16x16x128_f8f6f4 v[112:115], v[10:17], v[208:215], 0
	v_mfma_f32_16x16x128_f8f6f4 v[108:111], v[2:9], v[208:215], 0
	v_mfma_f32_16x16x128_f8f6f4 v[100:103], v[2:9], v[222:229], 0
	s_barrier
	v_mfma_f32_16x16x128_f8f6f4 v[104:107], v[10:17], v[222:229], 0
	s_setprio 0
	v_lshl_add_u64 v[198:199], v[196:197], 0, v[172:173]
	s_add_i32 s54, s54, s71
	v_lshl_add_u64 v[200:201], v[198:199], 0, s[28:29]
	s_mov_b32 m0, s54
	ds_read_b128 v[178:181], v189 offset:16384
	ds_read_b128 v[182:185], v189 offset:17408
	ds_read_b128 v[208:211], v189 offset:18432
	ds_read_b128 v[212:215], v189 offset:19456
	ds_read_b128 v[222:225], v189 offset:20480
	ds_read_b128 v[226:229], v189 offset:21504
	ds_read_b128 v[230:233], v189 offset:22528
	ds_read_b128 v[234:237], v189 offset:23552
	global_load_lds_dwordx4 v[200:201], off
	v_lshl_add_u64 v[200:201], v[196:197], 0, v[168:169]
	s_add_i32 s55, s54, 0x2000
	v_lshl_add_u64 v[202:203], v[200:201], 0, s[28:29]
	s_mov_b32 m0, s55
	s_mov_b64 s[6:7], 0x70100
	global_load_lds_dwordx4 v[202:203], off
	v_lshl_add_u64 v[202:203], v[196:197], 0, s[6:7]
	s_add_i32 s65, s65, s71
	v_lshl_add_u64 v[204:205], v[202:203], 0, v[172:173]
	s_mov_b32 m0, s65
	s_add_i32 s67, s65, 0x2000
	global_load_lds_dwordx4 v[204:205], off
	v_lshl_add_u64 v[202:203], v[202:203], 0, v[168:169]
	s_mov_b32 m0, s67
	s_nop 0
	global_load_lds_dwordx4 v[202:203], off
	v_lshl_add_u64 v[202:203], s[42:43], 0, v[174:175]
	v_lshl_add_u64 v[204:205], v[202:203], 0, s[28:29]
	s_mov_b32 m0, s72
	s_nop 0
	global_load_lds_dwordx4 v[204:205], off
	v_lshl_add_u64 v[204:205], s[42:43], 0, v[170:171]
	v_lshl_add_u64 v[216:217], v[204:205], 0, s[28:29]
	s_mov_b32 m0, s73
	s_nop 0
	global_load_lds_dwordx4 v[216:217], off
	s_waitcnt vmcnt(8)
	s_waitcnt lgkmcnt(0)
	s_barrier
	v_mfma_f32_16x16x128_f8f6f4 v[96:99], v[26:33], v[178:185], 0
	s_setprio 1
	v_mfma_f32_16x16x128_f8f6f4 v[92:95], v[18:25], v[178:185], 0
	v_mfma_f32_16x16x128_f8f6f4 v[84:87], v[18:25], v[208:215], 0
	v_mfma_f32_16x16x128_f8f6f4 v[88:91], v[26:33], v[208:215], 0
	v_mfma_f32_16x16x128_f8f6f4 v[80:83], v[26:33], v[222:229], 0
	v_mfma_f32_16x16x128_f8f6f4 v[76:79], v[18:25], v[222:229], 0
	v_mfma_f32_16x16x128_f8f6f4 v[68:71], v[18:25], v[230:237], 0
	v_mfma_f32_16x16x128_f8f6f4 v[72:75], v[26:33], v[230:237], 0
	s_setprio 0
	s_setprio 1
	v_mfma_f32_16x16x128_f8f6f4 v[64:67], v[10:17], v[178:185], 0
	v_mfma_f32_16x16x128_f8f6f4 v[60:63], v[2:9], v[178:185], 0
	v_mfma_f32_16x16x128_f8f6f4 v[52:55], v[2:9], v[208:215], 0
	v_mfma_f32_16x16x128_f8f6f4 v[56:59], v[10:17], v[208:215], 0
	v_mfma_f32_16x16x128_f8f6f4 v[48:51], v[10:17], v[222:229], 0
	v_mfma_f32_16x16x128_f8f6f4 v[44:47], v[2:9], v[222:229], 0
	v_mfma_f32_16x16x128_f8f6f4 v[36:39], v[2:9], v[230:237], 0
	s_barrier
	v_mfma_f32_16x16x128_f8f6f4 v[40:43], v[10:17], v[230:237], 0
	s_setprio 0
	s_add_i32 s50, 0, 0x18000
	s_add_i32 s63, 0, 0x1c000
	v_add_u32_e32 v207, s50, v167
	v_add_u32_e32 v208, s63, v167
	ds_read_b128 v[26:29], v207
	ds_read_b128 v[30:33], v207 offset:1024
	ds_read_b128 v[18:21], v207 offset:2048
	ds_read_b128 v[22:25], v207 offset:3072
	ds_read_b128 v[10:13], v208
	ds_read_b128 v[14:17], v208 offset:1024
	ds_read_b128 v[2:5], v208 offset:2048
	ds_read_b128 v[6:9], v208 offset:3072
	s_add_u32 s6, s42, 0x70100
	s_addc_u32 s7, s43, 0
	s_mov_b32 m0, s74
	v_lshl_add_u64 v[218:219], s[6:7], 0, v[174:175]
	ds_read_b128 v[178:181], v189 offset:32768
	ds_read_b128 v[182:185], v189 offset:33792
	ds_read_b128 v[210:213], v189 offset:34816
	ds_read_b128 v[214:217], v189 offset:35840
	ds_read_b128 v[222:225], v189 offset:36864
	ds_read_b128 v[226:229], v189 offset:37888
	ds_read_b128 v[230:233], v189 offset:38912
	ds_read_b128 v[234:237], v189 offset:39936
	global_load_lds_dwordx4 v[218:219], off
	v_lshl_add_u64 v[218:219], s[6:7], 0, v[170:171]
	s_mov_b32 m0, s75
	s_nop 0
	global_load_lds_dwordx4 v[218:219], off
	s_waitcnt vmcnt(8)
	s_waitcnt lgkmcnt(0)
	s_barrier
	v_mfma_f32_16x16x128_f8f6f4 v[160:163], v[26:33], v[178:185], v[160:163]
	s_setprio 1
	v_mfma_f32_16x16x128_f8f6f4 v[156:159], v[18:25], v[178:185], v[156:159]
	v_mfma_f32_16x16x128_f8f6f4 v[148:151], v[18:25], v[210:217], v[148:151]
	v_mfma_f32_16x16x128_f8f6f4 v[152:155], v[26:33], v[210:217], v[152:155]
	v_mfma_f32_16x16x128_f8f6f4 v[144:147], v[26:33], v[222:229], v[144:147]
	v_mfma_f32_16x16x128_f8f6f4 v[140:143], v[18:25], v[222:229], v[140:143]
	v_mfma_f32_16x16x128_f8f6f4 v[132:135], v[18:25], v[230:237], v[132:135]
	v_mfma_f32_16x16x128_f8f6f4 v[136:139], v[26:33], v[230:237], v[136:139]
	s_setprio 0
	s_setprio 1
	v_mfma_f32_16x16x128_f8f6f4 v[128:131], v[10:17], v[178:185], v[128:131]
	v_mfma_f32_16x16x128_f8f6f4 v[124:127], v[2:9], v[178:185], v[124:127]
	v_mfma_f32_16x16x128_f8f6f4 v[116:119], v[2:9], v[210:217], v[116:119]
	v_mfma_f32_16x16x128_f8f6f4 v[120:123], v[10:17], v[210:217], v[120:123]
	v_mfma_f32_16x16x128_f8f6f4 v[112:115], v[10:17], v[222:229], v[112:115]
	v_mfma_f32_16x16x128_f8f6f4 v[108:111], v[2:9], v[222:229], v[108:111]
	v_mfma_f32_16x16x128_f8f6f4 v[100:103], v[2:9], v[230:237], v[100:103]
	s_barrier
	v_mfma_f32_16x16x128_f8f6f4 v[104:107], v[10:17], v[230:237], v[104:107]
	s_setprio 0
	s_mov_b64 s[6:7], 0x180
	s_add_i32 s50, s50, s71
	v_lshl_add_u64 v[198:199], v[198:199], 0, s[6:7]
	s_mov_b32 m0, s50
	s_add_i32 s51, s50, 0x2000
	ds_read_b128 v[178:181], v189 offset:49152
	ds_read_b128 v[182:185], v189 offset:50176
	ds_read_b128 v[210:213], v189 offset:51200
	ds_read_b128 v[214:217], v189 offset:52224
	ds_read_b128 v[222:225], v189 offset:53248
	ds_read_b128 v[226:229], v189 offset:54272
	ds_read_b128 v[230:233], v189 offset:55296
	ds_read_b128 v[234:237], v189 offset:56320
	global_load_lds_dwordx4 v[198:199], off
	v_lshl_add_u64 v[198:199], v[200:201], 0, s[6:7]
	s_mov_b32 m0, s51
	s_add_i32 s63, s63, s71
	global_load_lds_dwordx4 v[198:199], off
	v_lshl_add_u64 v[198:199], v[196:197], 0, s[26:27]
	v_lshl_add_u64 v[200:201], v[198:199], 0, v[172:173]
	s_mov_b32 m0, s63
	s_add_i32 s64, s63, 0x2000
	global_load_lds_dwordx4 v[200:201], off
	v_lshl_add_u64 v[198:199], v[198:199], 0, v[168:169]
	s_mov_b32 m0, s64
	s_nop 0
	global_load_lds_dwordx4 v[198:199], off
	v_lshl_add_u64 v[198:199], v[202:203], 0, s[6:7]
	s_mov_b32 m0, s77
	s_nop 0
	global_load_lds_dwordx4 v[198:199], off
	v_lshl_add_u64 v[198:199], v[204:205], 0, s[6:7]
	s_mov_b32 m0, s78
	s_nop 0
	global_load_lds_dwordx4 v[198:199], off
	s_waitcnt vmcnt(8)
	s_waitcnt lgkmcnt(0)
	s_barrier
	v_mfma_f32_16x16x128_f8f6f4 v[96:99], v[26:33], v[178:185], v[96:99]
	s_setprio 1
	v_mfma_f32_16x16x128_f8f6f4 v[92:95], v[18:25], v[178:185], v[92:95]
	v_mfma_f32_16x16x128_f8f6f4 v[84:87], v[18:25], v[210:217], v[84:87]
	v_mfma_f32_16x16x128_f8f6f4 v[88:91], v[26:33], v[210:217], v[88:91]
	v_mfma_f32_16x16x128_f8f6f4 v[80:83], v[26:33], v[222:229], v[80:83]
	v_mfma_f32_16x16x128_f8f6f4 v[76:79], v[18:25], v[222:229], v[76:79]
	v_mfma_f32_16x16x128_f8f6f4 v[68:71], v[18:25], v[230:237], v[68:71]
	v_mfma_f32_16x16x128_f8f6f4 v[72:75], v[26:33], v[230:237], v[72:75]
	s_setprio 0
	s_setprio 1
	v_mfma_f32_16x16x128_f8f6f4 v[64:67], v[10:17], v[178:185], v[64:67]
	v_mfma_f32_16x16x128_f8f6f4 v[60:63], v[2:9], v[178:185], v[60:63]
	v_mfma_f32_16x16x128_f8f6f4 v[52:55], v[2:9], v[210:217], v[52:55]
	v_mfma_f32_16x16x128_f8f6f4 v[56:59], v[10:17], v[210:217], v[56:59]
	v_mfma_f32_16x16x128_f8f6f4 v[48:51], v[10:17], v[222:229], v[48:51]
	v_mfma_f32_16x16x128_f8f6f4 v[44:47], v[2:9], v[222:229], v[44:47]
	v_mfma_f32_16x16x128_f8f6f4 v[36:39], v[2:9], v[230:237], v[36:39]
	s_barrier
	v_mfma_f32_16x16x128_f8f6f4 v[40:43], v[10:17], v[230:237], v[40:43]
	s_setprio 0
	s_mov_b64 s[6:7], 0x200
	v_lshl_add_u64 v[18:19], v[196:197], 0, s[6:7]
	s_mov_b32 s86, 0
.LBB0_900:
	ds_read_b128 v[2:5], v34
	ds_read_b128 v[6:9], v34 offset:1024
	ds_read_b128 v[10:13], v34 offset:2048
	ds_read_b128 v[14:17], v34 offset:3072
	ds_read_b128 v[178:181], v206
	ds_read_b128 v[182:185], v206 offset:1024
	ds_read_b128 v[196:199], v206 offset:2048
	ds_read_b128 v[200:203], v206 offset:3072
	s_add_u32 s6, s42, 0x200
	s_addc_u32 s7, s43, 0
	s_cmp_eq_u32 s86, 24
	s_cselect_b64 vcc, -1, 0
	s_cselect_b32 s7, s52, s7
	s_cselect_b32 s6, s53, s6
	v_cndmask_b32_e32 v21, v19, v195, vcc
	v_cndmask_b32_e32 v20, v18, v194, vcc
	s_mov_b32 m0, s84
	v_lshl_add_u64 v[30:31], s[42:43], 0, v[190:191]
	ds_read_b128 v[22:25], v189
	ds_read_b128 v[26:29], v189 offset:1024
	ds_read_b128 v[210:213], v189 offset:2048
	ds_read_b128 v[214:217], v189 offset:3072
	ds_read_b128 v[222:225], v189 offset:4096
	ds_read_b128 v[226:229], v189 offset:5120
	ds_read_b128 v[230:233], v189 offset:6144
	ds_read_b128 v[234:237], v189 offset:7168
	global_load_lds_dwordx4 v[30:31], off
	v_lshl_add_u64 v[30:31], s[42:43], 0, v[192:193]
	s_mov_b32 m0, s85
	s_nop 0
	global_load_lds_dwordx4 v[30:31], off
	s_waitcnt vmcnt(8)
	s_waitcnt lgkmcnt(0)
	s_barrier
	v_mfma_f32_16x16x128_f8f6f4 v[160:163], v[2:9], v[22:29], v[160:163]
	s_setprio 1
	v_mfma_f32_16x16x128_f8f6f4 v[156:159], v[10:17], v[22:29], v[156:159]
	v_mfma_f32_16x16x128_f8f6f4 v[148:151], v[10:17], v[210:217], v[148:151]
	v_mfma_f32_16x16x128_f8f6f4 v[152:155], v[2:9], v[210:217], v[152:155]
	v_mfma_f32_16x16x128_f8f6f4 v[144:147], v[2:9], v[222:229], v[144:147]
	v_mfma_f32_16x16x128_f8f6f4 v[140:143], v[10:17], v[222:229], v[140:143]
	v_mfma_f32_16x16x128_f8f6f4 v[132:135], v[10:17], v[230:237], v[132:135]
	v_mfma_f32_16x16x128_f8f6f4 v[136:139], v[2:9], v[230:237], v[136:139]
	s_setprio 0
	s_setprio 1
	v_mfma_f32_16x16x128_f8f6f4 v[128:131], v[178:185], v[22:29], v[128:131]
	v_mfma_f32_16x16x128_f8f6f4 v[124:127], v[196:203], v[22:29], v[124:127]
	v_mfma_f32_16x16x128_f8f6f4 v[116:119], v[196:203], v[210:217], v[116:119]
	v_mfma_f32_16x16x128_f8f6f4 v[120:123], v[178:185], v[210:217], v[120:123]
	v_mfma_f32_16x16x128_f8f6f4 v[112:115], v[178:185], v[222:229], v[112:115]
	v_mfma_f32_16x16x128_f8f6f4 v[108:111], v[196:203], v[222:229], v[108:111]
	v_mfma_f32_16x16x128_f8f6f4 v[100:103], v[196:203], v[230:237], v[100:103]
	s_barrier
	v_mfma_f32_16x16x128_f8f6f4 v[104:107], v[178:185], v[230:237], v[104:107]
	s_setprio 0
	s_mov_b32 m0, s54
	v_lshl_add_u64 v[22:23], v[20:21], 0, v[172:173]
	ds_read_b128 v[210:213], v189 offset:16384
	ds_read_b128 v[214:217], v189 offset:17408
	ds_read_b128 v[222:225], v189 offset:18432
	ds_read_b128 v[226:229], v189 offset:19456
	ds_read_b128 v[230:233], v189 offset:20480
	ds_read_b128 v[234:237], v189 offset:21504
	ds_read_b128 v[238:241], v189 offset:22528
	ds_read_b128 v[242:245], v189 offset:23552
	global_load_lds_dwordx4 v[22:23], off
	v_lshl_add_u64 v[24:25], v[20:21], 0, v[168:169]
	s_mov_b32 m0, s55
	v_lshl_add_u64 v[26:27], v[20:21], 0, s[2:3]
	global_load_lds_dwordx4 v[24:25], off
	v_lshl_add_u64 v[28:29], v[26:27], 0, v[172:173]
	s_mov_b32 m0, s65
	v_lshl_add_u64 v[26:27], v[26:27], 0, v[168:169]
	global_load_lds_dwordx4 v[28:29], off
	s_mov_b32 m0, s67
	v_lshl_add_u64 v[28:29], s[6:7], 0, v[170:171]
	global_load_lds_dwordx4 v[26:27], off
	v_lshl_add_u64 v[26:27], s[6:7], 0, v[174:175]
	s_mov_b32 m0, s72
	s_nop 0
	global_load_lds_dwordx4 v[26:27], off
	s_mov_b32 m0, s73
	s_nop 0
	global_load_lds_dwordx4 v[28:29], off
	s_waitcnt vmcnt(8)
	s_waitcnt lgkmcnt(0)
	s_barrier
	v_mfma_f32_16x16x128_f8f6f4 v[96:99], v[2:9], v[210:217], v[96:99]
	s_setprio 1
	v_mfma_f32_16x16x128_f8f6f4 v[92:95], v[10:17], v[210:217], v[92:95]
	v_mfma_f32_16x16x128_f8f6f4 v[84:87], v[10:17], v[222:229], v[84:87]
	v_mfma_f32_16x16x128_f8f6f4 v[88:91], v[2:9], v[222:229], v[88:91]
	v_mfma_f32_16x16x128_f8f6f4 v[80:83], v[2:9], v[230:237], v[80:83]
	v_mfma_f32_16x16x128_f8f6f4 v[76:79], v[10:17], v[230:237], v[76:79]
	v_mfma_f32_16x16x128_f8f6f4 v[68:71], v[10:17], v[238:245], v[68:71]
	v_mfma_f32_16x16x128_f8f6f4 v[72:75], v[2:9], v[238:245], v[72:75]
	s_setprio 0
	s_setprio 1
	v_mfma_f32_16x16x128_f8f6f4 v[64:67], v[178:185], v[210:217], v[64:67]
	v_mfma_f32_16x16x128_f8f6f4 v[60:63], v[196:203], v[210:217], v[60:63]
	v_mfma_f32_16x16x128_f8f6f4 v[52:55], v[196:203], v[222:229], v[52:55]
	v_mfma_f32_16x16x128_f8f6f4 v[56:59], v[178:185], v[222:229], v[56:59]
	v_mfma_f32_16x16x128_f8f6f4 v[48:51], v[178:185], v[230:237], v[48:51]
	v_mfma_f32_16x16x128_f8f6f4 v[44:47], v[196:203], v[230:237], v[44:47]
	v_mfma_f32_16x16x128_f8f6f4 v[36:39], v[196:203], v[238:245], v[36:39]
	s_barrier
	v_mfma_f32_16x16x128_f8f6f4 v[40:43], v[178:185], v[238:245], v[40:43]
	s_setprio 0
	ds_read_b128 v[178:181], v207
	ds_read_b128 v[182:185], v207 offset:1024
	ds_read_b128 v[196:199], v207 offset:2048
	ds_read_b128 v[200:203], v207 offset:3072
	ds_read_b128 v[10:13], v208
	ds_read_b128 v[14:17], v208 offset:1024
	ds_read_b128 v[2:5], v208 offset:2048
	ds_read_b128 v[6:9], v208 offset:3072
	s_add_u32 s6, s6, 0x70000
	s_addc_u32 s7, s7, 0
	s_mov_b32 m0, s74
	v_lshl_add_u64 v[30:31], s[6:7], 0, v[174:175]
	ds_read_b128 v[210:213], v189 offset:32768
	ds_read_b128 v[214:217], v189 offset:33792
	ds_read_b128 v[222:225], v189 offset:34816
	ds_read_b128 v[226:229], v189 offset:35840
	ds_read_b128 v[230:233], v189 offset:36864
	ds_read_b128 v[234:237], v189 offset:37888
	ds_read_b128 v[238:241], v189 offset:38912
	ds_read_b128 v[242:245], v189 offset:39936
	global_load_lds_dwordx4 v[30:31], off
	v_lshl_add_u64 v[30:31], s[6:7], 0, v[170:171]
	s_mov_b32 m0, s75
	s_nop 0
	global_load_lds_dwordx4 v[30:31], off
	s_waitcnt vmcnt(8)
	s_waitcnt lgkmcnt(0)
	s_barrier
	v_mfma_f32_16x16x128_f8f6f4 v[160:163], v[178:185], v[210:217], v[160:163]
	s_setprio 1
	v_mfma_f32_16x16x128_f8f6f4 v[156:159], v[196:203], v[210:217], v[156:159]
	v_mfma_f32_16x16x128_f8f6f4 v[148:151], v[196:203], v[222:229], v[148:151]
	v_mfma_f32_16x16x128_f8f6f4 v[152:155], v[178:185], v[222:229], v[152:155]
	v_mfma_f32_16x16x128_f8f6f4 v[144:147], v[178:185], v[230:237], v[144:147]
	v_mfma_f32_16x16x128_f8f6f4 v[140:143], v[196:203], v[230:237], v[140:143]
	v_mfma_f32_16x16x128_f8f6f4 v[132:135], v[196:203], v[238:245], v[132:135]
	v_mfma_f32_16x16x128_f8f6f4 v[136:139], v[178:185], v[238:245], v[136:139]
	s_setprio 0
	s_setprio 1
	v_mfma_f32_16x16x128_f8f6f4 v[128:131], v[10:17], v[210:217], v[128:131]
	v_mfma_f32_16x16x128_f8f6f4 v[124:127], v[2:9], v[210:217], v[124:127]
	v_mfma_f32_16x16x128_f8f6f4 v[116:119], v[2:9], v[222:229], v[116:119]
	v_mfma_f32_16x16x128_f8f6f4 v[120:123], v[10:17], v[222:229], v[120:123]
	v_mfma_f32_16x16x128_f8f6f4 v[112:115], v[10:17], v[230:237], v[112:115]
	v_mfma_f32_16x16x128_f8f6f4 v[108:111], v[2:9], v[230:237], v[108:111]
	v_mfma_f32_16x16x128_f8f6f4 v[100:103], v[2:9], v[238:245], v[100:103]
	s_barrier
	v_mfma_f32_16x16x128_f8f6f4 v[104:107], v[10:17], v[238:245], v[104:107]
	s_setprio 0
	s_mov_b32 m0, s50
	v_lshl_add_u64 v[22:23], v[22:23], 0, s[18:19]
	ds_read_b128 v[210:213], v189 offset:49152
	ds_read_b128 v[214:217], v189 offset:50176
	ds_read_b128 v[222:225], v189 offset:51200
	ds_read_b128 v[226:229], v189 offset:52224
	ds_read_b128 v[230:233], v189 offset:53248
	ds_read_b128 v[234:237], v189 offset:54272
	ds_read_b128 v[238:241], v189 offset:55296
	ds_read_b128 v[242:245], v189 offset:56320
	global_load_lds_dwordx4 v[22:23], off
	v_lshl_add_u64 v[22:23], v[24:25], 0, s[18:19]
	s_mov_b32 m0, s51
	v_lshl_add_u64 v[20:21], v[20:21], 0, s[34:35]
	global_load_lds_dwordx4 v[22:23], off
	v_lshl_add_u64 v[22:23], v[20:21], 0, v[172:173]
	s_mov_b32 m0, s63
	v_lshl_add_u64 v[20:21], v[20:21], 0, v[168:169]
	global_load_lds_dwordx4 v[22:23], off
	s_mov_b32 m0, s64
	s_nop 0
	global_load_lds_dwordx4 v[20:21], off
	v_lshl_add_u64 v[20:21], v[26:27], 0, s[18:19]
	s_mov_b32 m0, s77
	s_nop 0
	global_load_lds_dwordx4 v[20:21], off
	v_lshl_add_u64 v[20:21], v[28:29], 0, s[18:19]
	s_mov_b32 m0, s78
	s_nop 0
	global_load_lds_dwordx4 v[20:21], off
	s_waitcnt vmcnt(8)
	s_waitcnt lgkmcnt(0)
	s_barrier
	v_mfma_f32_16x16x128_f8f6f4 v[96:99], v[178:185], v[210:217], v[96:99]
	s_setprio 1
	v_mfma_f32_16x16x128_f8f6f4 v[92:95], v[196:203], v[210:217], v[92:95]
	v_mfma_f32_16x16x128_f8f6f4 v[84:87], v[196:203], v[222:229], v[84:87]
	v_mfma_f32_16x16x128_f8f6f4 v[88:91], v[178:185], v[222:229], v[88:91]
	v_mfma_f32_16x16x128_f8f6f4 v[80:83], v[178:185], v[230:237], v[80:83]
	v_mfma_f32_16x16x128_f8f6f4 v[76:79], v[196:203], v[230:237], v[76:79]
	v_mfma_f32_16x16x128_f8f6f4 v[68:71], v[196:203], v[238:245], v[68:71]
	v_mfma_f32_16x16x128_f8f6f4 v[72:75], v[178:185], v[238:245], v[72:75]
	s_setprio 0
	s_setprio 1
	v_mfma_f32_16x16x128_f8f6f4 v[64:67], v[10:17], v[210:217], v[64:67]
	v_mfma_f32_16x16x128_f8f6f4 v[60:63], v[2:9], v[210:217], v[60:63]
	v_mfma_f32_16x16x128_f8f6f4 v[52:55], v[2:9], v[222:229], v[52:55]
	v_mfma_f32_16x16x128_f8f6f4 v[56:59], v[10:17], v[222:229], v[56:59]
	v_mfma_f32_16x16x128_f8f6f4 v[48:51], v[10:17], v[230:237], v[48:51]
	v_mfma_f32_16x16x128_f8f6f4 v[44:47], v[2:9], v[230:237], v[44:47]
	v_mfma_f32_16x16x128_f8f6f4 v[36:39], v[2:9], v[238:245], v[36:39]
	s_barrier
	v_mfma_f32_16x16x128_f8f6f4 v[40:43], v[10:17], v[238:245], v[40:43]
	s_setprio 0
	s_add_i32 s86, s86, 2
	s_add_u32 s42, s42, 0x100
	s_addc_u32 s43, s43, 0
	s_cmp_gt_u32 s86, 25
	v_lshl_add_u64 v[18:19], v[18:19], 0, s[28:29]
	s_cbranch_scc0 .LBB0_900
	s_and_b64 vcc, exec, s[36:37]
	s_mov_b64 s[84:85], s[24:25]
	s_cbranch_vccz .LBB0_903
	s_barrier

.LBB0_953:
	s_add_u32 s95, s30, 0x200
	s_addc_u32 s96, s31, 0
	s_add_i32 s65, 0, 0x14000
	s_add_i32 s67, 0, 0x10000
	v_add_u32_e32 v199, s65, v167
	v_add_u32_e32 v200, s67, v167
	ds_read_b128 v[10:13], v199
	ds_read_b128 v[14:17], v199 offset:1024
	ds_read_b128 v[2:5], v199 offset:2048
	ds_read_b128 v[6:9], v199 offset:3072
	ds_read_b128 v[22:25], v200 offset:3072
	ds_read_b128 v[18:21], v200 offset:2048
	ds_read_b128 v[30:33], v200 offset:1024
	ds_read_b128 v[26:29], v200
	s_lshl_b32 s14, s94, 10
	s_add_i32 s97, s14, 0
	s_add_i32 s97, s97, 0x20400
	v_mov_b32_e32 v191, v35
	v_mov_b32_e32 v175, v35
	s_add_i32 s83, s52, 0xc000
	v_readlane_b32 s26, v253, 28
	s_mov_b32 m0, s83
	v_readlane_b32 s27, v253, 29
	s_add_i32 s53, s52, 0xe000
	ds_read_b128 v[178:181], v169
	ds_read_b128 v[182:185], v169 offset:1024
	ds_read_b128 v[202:205], v169 offset:2048
	ds_read_b128 v[206:209], v169 offset:3072
	ds_read_b128 v[210:213], v169 offset:4096
	ds_read_b128 v[214:217], v169 offset:5120
	ds_read_b128 v[222:225], v169 offset:6144
	ds_read_b128 v[226:229], v169 offset:7168
	global_load_lds_dwordx4 v190, s[26:27]
	s_mov_b32 m0, s53
	s_nop 0
	global_load_lds_dwordx4 v174, s[26:27]
	s_waitcnt vmcnt(8)
	s_waitcnt lgkmcnt(0)
	s_barrier
	v_mfma_f32_16x16x128_f8f6f4 v[160:163], v[26:33], v[178:185], 0
	s_setprio 1
	v_mfma_f32_16x16x128_f8f6f4 v[156:159], v[18:25], v[178:185], 0
	v_mfma_f32_16x16x128_f8f6f4 v[148:151], v[18:25], v[202:209], 0
	v_mfma_f32_16x16x128_f8f6f4 v[152:155], v[26:33], v[202:209], 0
	v_mfma_f32_16x16x128_f8f6f4 v[144:147], v[26:33], v[210:217], 0
	v_mfma_f32_16x16x128_f8f6f4 v[140:143], v[18:25], v[210:217], 0
	v_mfma_f32_16x16x128_f8f6f4 v[132:135], v[18:25], v[222:229], 0
	v_mfma_f32_16x16x128_f8f6f4 v[136:139], v[26:33], v[222:229], 0
	s_setprio 0
	s_setprio 1
	v_mfma_f32_16x16x128_f8f6f4 v[128:131], v[10:17], v[178:185], 0
	v_mfma_f32_16x16x128_f8f6f4 v[124:127], v[2:9], v[178:185], 0
	v_mfma_f32_16x16x128_f8f6f4 v[116:119], v[2:9], v[202:209], 0
	v_mfma_f32_16x16x128_f8f6f4 v[120:123], v[10:17], v[202:209], 0
	v_mfma_f32_16x16x128_f8f6f4 v[112:115], v[10:17], v[210:217], 0
	v_mfma_f32_16x16x128_f8f6f4 v[108:111], v[2:9], v[210:217], 0
	v_mfma_f32_16x16x128_f8f6f4 v[100:103], v[2:9], v[222:229], 0
	s_barrier
	v_mfma_f32_16x16x128_f8f6f4 v[104:107], v[10:17], v[222:229], 0
	s_setprio 0
	v_lshl_add_u64 v[194:195], s[30:31], 0, v[170:171]
	s_add_i32 s67, s67, s82
	v_lshl_add_u64 v[196:197], v[194:195], 0, s[28:29]
	s_mov_b32 m0, s67
	s_add_i32 s55, s67, 0x2000
	ds_read_b128 v[178:181], v169 offset:16384
	ds_read_b128 v[182:185], v169 offset:17408
	ds_read_b128 v[202:205], v169 offset:18432
	ds_read_b128 v[206:209], v169 offset:19456
	ds_read_b128 v[210:213], v169 offset:20480
	ds_read_b128 v[214:217], v169 offset:21504
	ds_read_b128 v[222:225], v169 offset:22528
	ds_read_b128 v[226:229], v169 offset:23552
	global_load_lds_dwordx4 v[196:197], off
	v_lshl_add_u64 v[196:197], s[30:31], 0, v[172:173]
	s_add_u32 s46, s30, 0x20100
	v_lshl_add_u64 v[218:219], v[196:197], 0, s[28:29]
	s_mov_b32 m0, s55
	s_addc_u32 s47, s31, 0
	s_add_i32 s65, s65, s82
	global_load_lds_dwordx4 v[218:219], off
	v_lshl_add_u64 v[218:219], s[46:47], 0, v[170:171]
	s_mov_b32 m0, s65
	s_add_i32 s54, s65, 0x2000
	global_load_lds_dwordx4 v[218:219], off
	v_lshl_add_u64 v[218:219], s[46:47], 0, v[172:173]
	s_mov_b32 m0, s54
	v_readlane_b32 s26, v253, 37
	global_load_lds_dwordx4 v[218:219], off
	s_mov_b32 m0, s52
	v_readlane_b32 s27, v253, 38
	s_nop 4
	global_load_lds_dwordx4 v34, s[26:27]
	s_mov_b32 m0, s84
	s_nop 0
	global_load_lds_dwordx4 v192, s[26:27]
	s_waitcnt vmcnt(8)
	s_waitcnt lgkmcnt(0)
	s_barrier
	v_mfma_f32_16x16x128_f8f6f4 v[96:99], v[26:33], v[178:185], 0
	s_setprio 1
	v_mfma_f32_16x16x128_f8f6f4 v[92:95], v[18:25], v[178:185], 0
	v_mfma_f32_16x16x128_f8f6f4 v[84:87], v[18:25], v[202:209], 0
	v_mfma_f32_16x16x128_f8f6f4 v[88:91], v[26:33], v[202:209], 0
	v_mfma_f32_16x16x128_f8f6f4 v[80:83], v[26:33], v[210:217], 0
	v_mfma_f32_16x16x128_f8f6f4 v[76:79], v[18:25], v[210:217], 0
	v_mfma_f32_16x16x128_f8f6f4 v[68:71], v[18:25], v[222:229], 0
	v_mfma_f32_16x16x128_f8f6f4 v[72:75], v[26:33], v[222:229], 0
	s_setprio 0
	s_setprio 1
	v_mfma_f32_16x16x128_f8f6f4 v[64:67], v[10:17], v[178:185], 0
	v_mfma_f32_16x16x128_f8f6f4 v[60:63], v[2:9], v[178:185], 0
	v_mfma_f32_16x16x128_f8f6f4 v[52:55], v[2:9], v[202:209], 0
	v_mfma_f32_16x16x128_f8f6f4 v[56:59], v[10:17], v[202:209], 0
	v_mfma_f32_16x16x128_f8f6f4 v[48:51], v[10:17], v[210:217], 0
	v_mfma_f32_16x16x128_f8f6f4 v[44:47], v[2:9], v[210:217], 0
	v_mfma_f32_16x16x128_f8f6f4 v[36:39], v[2:9], v[222:229], 0
	s_barrier
	v_mfma_f32_16x16x128_f8f6f4 v[40:43], v[10:17], v[222:229], 0
	s_setprio 0
	s_add_i32 s50, 0, 0x18000
	s_add_i32 s64, 0, 0x1c000
	v_add_u32_e32 v201, s50, v167
	v_add_u32_e32 v202, s64, v167
	ds_read_b128 v[26:29], v201
	ds_read_b128 v[30:33], v201 offset:1024
	ds_read_b128 v[18:21], v201 offset:2048
	ds_read_b128 v[22:25], v201 offset:3072
	ds_read_b128 v[10:13], v202
	ds_read_b128 v[14:17], v202 offset:1024
	ds_read_b128 v[2:5], v202 offset:2048
	ds_read_b128 v[6:9], v202 offset:3072
	s_mov_b32 m0, s85
	ds_read_b128 v[178:181], v169 offset:32768
	ds_read_b128 v[182:185], v169 offset:33792
	ds_read_b128 v[204:207], v169 offset:34816
	ds_read_b128 v[208:211], v169 offset:35840
	ds_read_b128 v[212:215], v169 offset:36864
	ds_read_b128 v[216:219], v169 offset:37888
	ds_read_b128 v[222:225], v169 offset:38912
	ds_read_b128 v[226:229], v169 offset:39936
	global_load_lds_dwordx4 v189, s[26:27]
	s_mov_b32 m0, s86
	s_nop 0
	global_load_lds_dwordx4 v198, s[26:27]
	s_waitcnt vmcnt(8)
	s_waitcnt lgkmcnt(0)
	s_barrier
	v_mfma_f32_16x16x128_f8f6f4 v[160:163], v[26:33], v[178:185], v[160:163]
	s_setprio 1
	v_mfma_f32_16x16x128_f8f6f4 v[156:159], v[18:25], v[178:185], v[156:159]
	v_mfma_f32_16x16x128_f8f6f4 v[148:151], v[18:25], v[204:211], v[148:151]
	v_mfma_f32_16x16x128_f8f6f4 v[152:155], v[26:33], v[204:211], v[152:155]
	v_mfma_f32_16x16x128_f8f6f4 v[144:147], v[26:33], v[212:219], v[144:147]
	v_mfma_f32_16x16x128_f8f6f4 v[140:143], v[18:25], v[212:219], v[140:143]
	v_mfma_f32_16x16x128_f8f6f4 v[132:135], v[18:25], v[222:229], v[132:135]
	v_mfma_f32_16x16x128_f8f6f4 v[136:139], v[26:33], v[222:229], v[136:139]
	s_setprio 0
	s_setprio 1
	v_mfma_f32_16x16x128_f8f6f4 v[128:131], v[10:17], v[178:185], v[128:131]
	v_mfma_f32_16x16x128_f8f6f4 v[124:127], v[2:9], v[178:185], v[124:127]
	v_mfma_f32_16x16x128_f8f6f4 v[116:119], v[2:9], v[204:211], v[116:119]
	v_mfma_f32_16x16x128_f8f6f4 v[120:123], v[10:17], v[204:211], v[120:123]
	v_mfma_f32_16x16x128_f8f6f4 v[112:115], v[10:17], v[212:219], v[112:115]
	v_mfma_f32_16x16x128_f8f6f4 v[108:111], v[2:9], v[212:219], v[108:111]
	v_mfma_f32_16x16x128_f8f6f4 v[100:103], v[2:9], v[222:229], v[100:103]
	s_barrier
	v_mfma_f32_16x16x128_f8f6f4 v[104:107], v[10:17], v[222:229], v[104:107]
	s_setprio 0
	s_add_i32 s50, s50, s82
	s_mov_b64 s[26:27], 0x180
	s_add_i32 s51, s50, 0x2000
	v_lshl_add_u64 v[194:195], v[194:195], 0, s[26:27]
	s_mov_b32 m0, s50
	s_add_u32 s30, s30, 0x20180
	ds_read_b128 v[178:181], v169 offset:49152
	ds_read_b128 v[182:185], v169 offset:50176
	ds_read_b128 v[204:207], v169 offset:51200
	ds_read_b128 v[208:211], v169 offset:52224
	ds_read_b128 v[212:215], v169 offset:53248
	ds_read_b128 v[216:219], v169 offset:54272
	ds_read_b128 v[222:225], v169 offset:55296
	ds_read_b128 v[226:229], v169 offset:56320
	global_load_lds_dwordx4 v[194:195], off
	v_lshl_add_u64 v[194:195], v[196:197], 0, s[26:27]
	s_mov_b32 m0, s51
	s_addc_u32 s31, s31, 0
	s_add_i32 s64, s64, s82
	global_load_lds_dwordx4 v[194:195], off
	v_lshl_add_u64 v[194:195], s[30:31], 0, v[170:171]
	s_mov_b32 m0, s64
	s_add_i32 s63, s64, 0x2000
	global_load_lds_dwordx4 v[194:195], off
	v_lshl_add_u64 v[194:195], s[30:31], 0, v[172:173]
	s_mov_b32 m0, s63
	v_readlane_b32 s26, v253, 39
	global_load_lds_dwordx4 v[194:195], off
	s_mov_b32 m0, s90
	v_readlane_b32 s27, v253, 40
	s_nop 4
	global_load_lds_dwordx4 v34, s[26:27]
	s_mov_b32 m0, s91
	s_nop 0
	global_load_lds_dwordx4 v192, s[26:27]
	s_waitcnt vmcnt(8)
	s_waitcnt lgkmcnt(0)
	s_barrier
	v_mfma_f32_16x16x128_f8f6f4 v[96:99], v[26:33], v[178:185], v[96:99]
	s_setprio 1
	v_mfma_f32_16x16x128_f8f6f4 v[92:95], v[18:25], v[178:185], v[92:95]
	v_mfma_f32_16x16x128_f8f6f4 v[84:87], v[18:25], v[204:211], v[84:87]
	v_mfma_f32_16x16x128_f8f6f4 v[88:91], v[26:33], v[204:211], v[88:91]
	v_mfma_f32_16x16x128_f8f6f4 v[80:83], v[26:33], v[212:219], v[80:83]
	v_mfma_f32_16x16x128_f8f6f4 v[76:79], v[18:25], v[212:219], v[76:79]
	v_mfma_f32_16x16x128_f8f6f4 v[68:71], v[18:25], v[222:229], v[68:71]
	v_mfma_f32_16x16x128_f8f6f4 v[72:75], v[26:33], v[222:229], v[72:75]
	s_setprio 0
	s_setprio 1
	v_mfma_f32_16x16x128_f8f6f4 v[64:67], v[10:17], v[178:185], v[64:67]
	v_mfma_f32_16x16x128_f8f6f4 v[60:63], v[2:9], v[178:185], v[60:63]
	v_mfma_f32_16x16x128_f8f6f4 v[52:55], v[2:9], v[204:211], v[52:55]
	v_mfma_f32_16x16x128_f8f6f4 v[56:59], v[10:17], v[204:211], v[56:59]
	v_mfma_f32_16x16x128_f8f6f4 v[48:51], v[10:17], v[212:219], v[48:51]
	v_mfma_f32_16x16x128_f8f6f4 v[44:47], v[2:9], v[212:219], v[44:47]
	v_mfma_f32_16x16x128_f8f6f4 v[36:39], v[2:9], v[222:229], v[36:39]
	s_barrier
	v_mfma_f32_16x16x128_f8f6f4 v[40:43], v[10:17], v[222:229], v[40:43]
	s_setprio 0
	v_lshl_add_u64 v[18:19], s[26:27], 0, v[174:175]
	v_lshl_add_u64 v[20:21], s[26:27], 0, v[190:191]
	s_mov_b32 s75, 0
	s_mov_b64 s[30:31], 0
	s_branch .LBB0_955
.LBB0_954:
	ds_read_b128 v[178:181], v200
	ds_read_b128 v[182:185], v200 offset:1024
	ds_read_b128 v[204:207], v200 offset:2048
	ds_read_b128 v[208:211], v200 offset:3072
	ds_read_b128 v[10:13], v199
	ds_read_b128 v[14:17], v199 offset:1024
	ds_read_b128 v[2:5], v199 offset:2048
	ds_read_b128 v[6:9], v199 offset:3072
	s_add_u32 s14, s30, 0x200
	s_addc_u32 vcc_lo, s31, 0
	s_and_b64 s[48:49], s[46:47], exec
	s_cselect_b32 s14, 0, s14
	s_cselect_b32 s49, 0, vcc_lo
	s_add_u32 s48, s20, s14
	s_addc_u32 s49, s21, s49
	s_add_u32 s14, s95, s30
	s_addc_u32 vcc_lo, s96, s31
	s_and_b64 s[46:47], s[46:47], exec
	s_cselect_b32 s47, s43, vcc_lo
	s_cselect_b32 s46, s42, s14
	s_mov_b32 m0, s83
	v_lshl_add_u64 v[30:31], v[20:21], 0, s[30:31]
	ds_read_b128 v[22:25], v169
	ds_read_b128 v[26:29], v169 offset:1024
	ds_read_b128 v[212:215], v169 offset:2048
	ds_read_b128 v[216:219], v169 offset:3072
	ds_read_b128 v[222:225], v169 offset:4096
	ds_read_b128 v[226:229], v169 offset:5120
	ds_read_b128 v[230:233], v169 offset:6144
	ds_read_b128 v[234:237], v169 offset:7168
	global_load_lds_dwordx4 v[30:31], off
	v_lshl_add_u64 v[30:31], v[18:19], 0, s[30:31]
	s_mov_b32 m0, s53
	s_nop 0
	global_load_lds_dwordx4 v[30:31], off
	s_waitcnt vmcnt(8)
	s_waitcnt lgkmcnt(0)
	s_barrier
	v_mfma_f32_16x16x128_f8f6f4 v[160:163], v[178:185], v[22:29], v[160:163]
	s_setprio 1
	v_mfma_f32_16x16x128_f8f6f4 v[156:159], v[204:211], v[22:29], v[156:159]
	v_mfma_f32_16x16x128_f8f6f4 v[148:151], v[204:211], v[212:219], v[148:151]
	v_mfma_f32_16x16x128_f8f6f4 v[152:155], v[178:185], v[212:219], v[152:155]
	v_mfma_f32_16x16x128_f8f6f4 v[144:147], v[178:185], v[222:229], v[144:147]
	v_mfma_f32_16x16x128_f8f6f4 v[140:143], v[204:211], v[222:229], v[140:143]
	v_mfma_f32_16x16x128_f8f6f4 v[132:135], v[204:211], v[230:237], v[132:135]
	v_mfma_f32_16x16x128_f8f6f4 v[136:139], v[178:185], v[230:237], v[136:139]
	s_setprio 0
	s_setprio 1
	v_mfma_f32_16x16x128_f8f6f4 v[128:131], v[10:17], v[22:29], v[128:131]
	v_mfma_f32_16x16x128_f8f6f4 v[124:127], v[2:9], v[22:29], v[124:127]
	v_mfma_f32_16x16x128_f8f6f4 v[116:119], v[2:9], v[212:219], v[116:119]
	v_mfma_f32_16x16x128_f8f6f4 v[120:123], v[10:17], v[212:219], v[120:123]
	v_mfma_f32_16x16x128_f8f6f4 v[112:115], v[10:17], v[222:229], v[112:115]
	v_mfma_f32_16x16x128_f8f6f4 v[108:111], v[2:9], v[222:229], v[108:111]
	v_mfma_f32_16x16x128_f8f6f4 v[100:103], v[2:9], v[230:237], v[100:103]
	s_barrier
	v_mfma_f32_16x16x128_f8f6f4 v[104:107], v[10:17], v[230:237], v[104:107]
	s_setprio 0
	s_mov_b32 m0, s67
	v_lshl_add_u64 v[22:23], s[46:47], 0, v[170:171]
	s_add_u32 vcc_lo, s46, 0x20000
	ds_read_b128 v[212:215], v169 offset:16384
	ds_read_b128 v[216:219], v169 offset:17408
	ds_read_b128 v[222:225], v169 offset:18432
	ds_read_b128 v[226:229], v169 offset:19456
	ds_read_b128 v[230:233], v169 offset:20480
	ds_read_b128 v[234:237], v169 offset:21504
	ds_read_b128 v[238:241], v169 offset:22528
	ds_read_b128 v[242:245], v169 offset:23552
	global_load_lds_dwordx4 v[22:23], off
	v_lshl_add_u64 v[24:25], s[46:47], 0, v[172:173]
	s_mov_b32 m0, s55
	s_addc_u32 vcc_hi, s47, 0
	global_load_lds_dwordx4 v[24:25], off
	v_lshl_add_u64 v[26:27], vcc, 0, v[170:171]
	s_mov_b32 m0, s65
	v_mov_b32_e32 v193, v35
	global_load_lds_dwordx4 v[26:27], off
	v_lshl_add_u64 v[26:27], vcc, 0, v[172:173]
	s_mov_b32 m0, s54
	v_lshl_add_u64 v[28:29], s[48:49], 0, v[34:35]
	global_load_lds_dwordx4 v[26:27], off
	s_mov_b32 m0, s52
	v_lshl_add_u64 v[26:27], s[48:49], 0, v[192:193]
	global_load_lds_dwordx4 v34, s[48:49]
	s_mov_b32 m0, s84
	s_nop 0
	global_load_lds_dwordx4 v192, s[48:49]
	s_waitcnt vmcnt(8)
	s_waitcnt lgkmcnt(0)
	s_barrier
	v_mfma_f32_16x16x128_f8f6f4 v[96:99], v[178:185], v[212:219], v[96:99]
	s_setprio 1
	v_mfma_f32_16x16x128_f8f6f4 v[92:95], v[204:211], v[212:219], v[92:95]
	v_mfma_f32_16x16x128_f8f6f4 v[84:87], v[204:211], v[222:229], v[84:87]
	v_mfma_f32_16x16x128_f8f6f4 v[88:91], v[178:185], v[222:229], v[88:91]
	v_mfma_f32_16x16x128_f8f6f4 v[80:83], v[178:185], v[230:237], v[80:83]
	v_mfma_f32_16x16x128_f8f6f4 v[76:79], v[204:211], v[230:237], v[76:79]
	v_mfma_f32_16x16x128_f8f6f4 v[68:71], v[204:211], v[238:245], v[68:71]
	v_mfma_f32_16x16x128_f8f6f4 v[72:75], v[178:185], v[238:245], v[72:75]
	s_setprio 0
	s_setprio 1
	v_mfma_f32_16x16x128_f8f6f4 v[64:67], v[10:17], v[212:219], v[64:67]
	v_mfma_f32_16x16x128_f8f6f4 v[60:63], v[2:9], v[212:219], v[60:63]
	v_mfma_f32_16x16x128_f8f6f4 v[52:55], v[2:9], v[222:229], v[52:55]
	v_mfma_f32_16x16x128_f8f6f4 v[56:59], v[10:17], v[222:229], v[56:59]
	v_mfma_f32_16x16x128_f8f6f4 v[48:51], v[10:17], v[230:237], v[48:51]
	v_mfma_f32_16x16x128_f8f6f4 v[44:47], v[2:9], v[230:237], v[44:47]
	v_mfma_f32_16x16x128_f8f6f4 v[36:39], v[2:9], v[238:245], v[36:39]
	s_barrier
	v_mfma_f32_16x16x128_f8f6f4 v[40:43], v[10:17], v[238:245], v[40:43]
	s_setprio 0
	ds_read_b128 v[178:181], v201
	ds_read_b128 v[182:185], v201 offset:1024
	ds_read_b128 v[204:207], v201 offset:2048
	ds_read_b128 v[208:211], v201 offset:3072
	ds_read_b128 v[10:13], v202
	ds_read_b128 v[14:17], v202 offset:1024
	ds_read_b128 v[2:5], v202 offset:2048
	ds_read_b128 v[6:9], v202 offset:3072
	s_mov_b32 m0, s85
	ds_read_b128 v[212:215], v169 offset:32768
	ds_read_b128 v[216:219], v169 offset:33792
	ds_read_b128 v[222:225], v169 offset:34816
	ds_read_b128 v[226:229], v169 offset:35840
	ds_read_b128 v[230:233], v169 offset:36864
	ds_read_b128 v[234:237], v169 offset:37888
	ds_read_b128 v[238:241], v169 offset:38912
	ds_read_b128 v[242:245], v169 offset:39936
	global_load_lds_dwordx4 v189, s[48:49]
	s_mov_b32 m0, s86
	s_nop 0
	global_load_lds_dwordx4 v198, s[48:49]
	s_waitcnt vmcnt(8)
	s_waitcnt lgkmcnt(0)
	s_barrier
	v_mfma_f32_16x16x128_f8f6f4 v[160:163], v[178:185], v[212:219], v[160:163]
	s_setprio 1
	v_mfma_f32_16x16x128_f8f6f4 v[156:159], v[204:211], v[212:219], v[156:159]
	v_mfma_f32_16x16x128_f8f6f4 v[148:151], v[204:211], v[222:229], v[148:151]
	v_mfma_f32_16x16x128_f8f6f4 v[152:155], v[178:185], v[222:229], v[152:155]
	v_mfma_f32_16x16x128_f8f6f4 v[144:147], v[178:185], v[230:237], v[144:147]
	v_mfma_f32_16x16x128_f8f6f4 v[140:143], v[204:211], v[230:237], v[140:143]
	v_mfma_f32_16x16x128_f8f6f4 v[132:135], v[204:211], v[238:245], v[132:135]
	v_mfma_f32_16x16x128_f8f6f4 v[136:139], v[178:185], v[238:245], v[136:139]
	s_setprio 0
	s_setprio 1
	v_mfma_f32_16x16x128_f8f6f4 v[128:131], v[10:17], v[212:219], v[128:131]
	v_mfma_f32_16x16x128_f8f6f4 v[124:127], v[2:9], v[212:219], v[124:127]
	v_mfma_f32_16x16x128_f8f6f4 v[116:119], v[2:9], v[222:229], v[116:119]
	v_mfma_f32_16x16x128_f8f6f4 v[120:123], v[10:17], v[222:229], v[120:123]
	v_mfma_f32_16x16x128_f8f6f4 v[112:115], v[10:17], v[230:237], v[112:115]
	v_mfma_f32_16x16x128_f8f6f4 v[108:111], v[2:9], v[230:237], v[108:111]
	v_mfma_f32_16x16x128_f8f6f4 v[100:103], v[2:9], v[238:245], v[100:103]
	s_barrier
	v_mfma_f32_16x16x128_f8f6f4 v[104:107], v[10:17], v[238:245], v[104:107]
	s_setprio 0
	s_mov_b32 m0, s50
	v_lshl_add_u64 v[22:23], v[22:23], 0, s[18:19]
	s_add_u32 s46, s46, 0x20080
	ds_read_b128 v[212:215], v169 offset:49152
	ds_read_b128 v[216:219], v169 offset:50176
	ds_read_b128 v[222:225], v169 offset:51200
	ds_read_b128 v[226:229], v169 offset:52224
	ds_read_b128 v[230:233], v169 offset:53248
	ds_read_b128 v[234:237], v169 offset:54272
	ds_read_b128 v[238:241], v169 offset:55296
	ds_read_b128 v[242:245], v169 offset:56320
	global_load_lds_dwordx4 v[22:23], off
	v_lshl_add_u64 v[22:23], v[24:25], 0, s[18:19]
	s_mov_b32 m0, s51
	s_addc_u32 s47, s47, 0
	global_load_lds_dwordx4 v[22:23], off
	v_lshl_add_u64 v[22:23], s[46:47], 0, v[170:171]
	s_mov_b32 m0, s64
	s_nop 0
	global_load_lds_dwordx4 v[22:23], off
	v_lshl_add_u64 v[22:23], s[46:47], 0, v[172:173]
	s_mov_b32 m0, s63
	s_nop 0
	global_load_lds_dwordx4 v[22:23], off
	v_lshl_add_u64 v[22:23], v[28:29], 0, s[18:19]
	s_mov_b32 m0, s90
	s_nop 0
	global_load_lds_dwordx4 v[22:23], off
	v_lshl_add_u64 v[22:23], v[26:27], 0, s[18:19]
	s_mov_b32 m0, s91
	s_nop 0
	global_load_lds_dwordx4 v[22:23], off
	s_waitcnt vmcnt(8)
	s_waitcnt lgkmcnt(0)
	s_barrier
	v_mfma_f32_16x16x128_f8f6f4 v[96:99], v[178:185], v[212:219], v[96:99]
	s_setprio 1
	v_mfma_f32_16x16x128_f8f6f4 v[92:95], v[204:211], v[212:219], v[92:95]
	v_mfma_f32_16x16x128_f8f6f4 v[84:87], v[204:211], v[222:229], v[84:87]
	v_mfma_f32_16x16x128_f8f6f4 v[88:91], v[178:185], v[222:229], v[88:91]
	v_mfma_f32_16x16x128_f8f6f4 v[80:83], v[178:185], v[230:237], v[80:83]
	v_mfma_f32_16x16x128_f8f6f4 v[76:79], v[204:211], v[230:237], v[76:79]
	v_mfma_f32_16x16x128_f8f6f4 v[68:71], v[204:211], v[238:245], v[68:71]
	v_mfma_f32_16x16x128_f8f6f4 v[72:75], v[178:185], v[238:245], v[72:75]
	s_setprio 0
	s_setprio 1
	v_mfma_f32_16x16x128_f8f6f4 v[64:67], v[10:17], v[212:219], v[64:67]
	v_mfma_f32_16x16x128_f8f6f4 v[60:63], v[2:9], v[212:219], v[60:63]
	v_mfma_f32_16x16x128_f8f6f4 v[52:55], v[2:9], v[222:229], v[52:55]
	v_mfma_f32_16x16x128_f8f6f4 v[56:59], v[10:17], v[222:229], v[56:59]
	v_mfma_f32_16x16x128_f8f6f4 v[48:51], v[10:17], v[230:237], v[48:51]
	v_mfma_f32_16x16x128_f8f6f4 v[44:47], v[2:9], v[230:237], v[44:47]
	v_mfma_f32_16x16x128_f8f6f4 v[36:39], v[2:9], v[238:245], v[36:39]
	s_barrier
	v_mfma_f32_16x16x128_f8f6f4 v[40:43], v[10:17], v[238:245], v[40:43]
	s_setprio 0
	s_add_i32 s75, s75, 2
	s_add_u32 s30, s30, 0x100
	s_addc_u32 s31, s31, 0
	s_cmp_gt_u32 s75, 5
	s_cbranch_scc1 .LBB0_957

.LBB0_1086:
	s_lshl_b32 s10, s51, 18
	s_add_u32 s10, s20, s10
	s_addc_u32 s11, s21, 0
	s_and_b64 s[16:17], s[4:5], exec
	s_cselect_b32 s54, s11, s31
	s_cselect_b32 s55, s10, s30
	s_lshl_b32 s14, s50, 18
	s_add_u32 s16, s15, s14
	s_addc_u32 s17, s26, 0
	s_and_b64 s[36:37], s[4:5], exec
	s_cselect_b32 s56, s17, s23
	s_cselect_b32 s57, s16, s22
	s_add_i32 s60, 0, 0x10000
	s_add_i32 s62, 0, 0x14000
	v_add_u32_e32 v198, s60, v196
	v_add_u32_e32 v199, s62, v196
	ds_read_b128 v[26:29], v198
	ds_read_b128 v[30:33], v198 offset:1024
	ds_read_b128 v[18:21], v198 offset:2048
	ds_read_b128 v[22:25], v198 offset:3072
	ds_read_b128 v[10:13], v199
	ds_read_b128 v[14:17], v199 offset:1024
	ds_read_b128 v[2:5], v199 offset:2048
	ds_read_b128 v[6:9], v199 offset:3072
	s_add_u32 s36, s30, 0x20080
	s_addc_u32 s37, s31, 0
	s_add_i32 s58, s41, 0xc000
	v_lshl_add_u64 v[174:175], s[36:37], 0, v[168:169]
	s_mov_b32 m0, s58
	s_add_i32 s59, s41, 0xe000
	ds_read_b128 v[200:203], v197
	ds_read_b128 v[204:207], v197 offset:1024
	ds_read_b128 v[222:225], v197 offset:2048
	ds_read_b128 v[226:229], v197 offset:3072
	ds_read_b128 v[230:233], v197 offset:4096
	ds_read_b128 v[234:237], v197 offset:5120
	ds_read_b128 v[238:241], v197 offset:6144
	ds_read_b128 v[242:245], v197 offset:7168
	global_load_lds_dwordx4 v[174:175], off
	v_lshl_add_u64 v[174:175], s[36:37], 0, v[166:167]
	s_mov_b32 m0, s59
	s_nop 0
	global_load_lds_dwordx4 v[174:175], off
	s_waitcnt vmcnt(8)
	s_waitcnt lgkmcnt(0)
	s_barrier
	v_mfma_f32_16x16x128_f8f6f4 v[160:163], v[26:33], v[200:207], 0
	s_setprio 1
	v_mfma_f32_16x16x128_f8f6f4 v[156:159], v[18:25], v[200:207], 0
	v_mfma_f32_16x16x128_f8f6f4 v[148:151], v[18:25], v[222:229], 0
	v_mfma_f32_16x16x128_f8f6f4 v[152:155], v[26:33], v[222:229], 0
	v_mfma_f32_16x16x128_f8f6f4 v[144:147], v[26:33], v[230:237], 0
	v_mfma_f32_16x16x128_f8f6f4 v[140:143], v[18:25], v[230:237], 0
	v_mfma_f32_16x16x128_f8f6f4 v[132:135], v[18:25], v[238:245], 0
	v_mfma_f32_16x16x128_f8f6f4 v[136:139], v[26:33], v[238:245], 0
	s_setprio 0
	s_setprio 1
	v_mfma_f32_16x16x128_f8f6f4 v[128:131], v[10:17], v[200:207], 0
	v_mfma_f32_16x16x128_f8f6f4 v[124:127], v[2:9], v[200:207], 0
	v_mfma_f32_16x16x128_f8f6f4 v[116:119], v[2:9], v[222:229], 0
	v_mfma_f32_16x16x128_f8f6f4 v[120:123], v[10:17], v[222:229], 0
	v_mfma_f32_16x16x128_f8f6f4 v[112:115], v[10:17], v[230:237], 0
	v_mfma_f32_16x16x128_f8f6f4 v[108:111], v[2:9], v[230:237], 0
	v_mfma_f32_16x16x128_f8f6f4 v[100:103], v[2:9], v[238:245], 0
	s_barrier
	v_mfma_f32_16x16x128_f8f6f4 v[104:107], v[10:17], v[238:245], 0
	s_setprio 0
	s_add_i32 s60, s60, s40
	v_lshl_add_u64 v[174:175], s[22:23], 0, v[34:35]
	s_add_i32 s61, s60, 0x2000
	v_lshl_add_u64 v[178:179], v[174:175], 0, s[28:29]
	s_mov_b32 m0, s60
	v_lshl_add_u64 v[190:191], s[22:23], 0, v[164:165]
	s_add_u32 s36, s22, 0x20100
	ds_read_b128 v[200:203], v197 offset:16384
	ds_read_b128 v[204:207], v197 offset:17408
	ds_read_b128 v[222:225], v197 offset:18432
	ds_read_b128 v[226:229], v197 offset:19456
	ds_read_b128 v[230:233], v197 offset:20480
	ds_read_b128 v[234:237], v197 offset:21504
	ds_read_b128 v[238:241], v197 offset:22528
	ds_read_b128 v[242:245], v197 offset:23552
	global_load_lds_dwordx4 v[178:179], off
	v_lshl_add_u64 v[178:179], v[190:191], 0, s[28:29]
	s_mov_b32 m0, s61
	s_addc_u32 s37, s23, 0
	s_add_i32 s62, s62, s40
	global_load_lds_dwordx4 v[178:179], off
	v_lshl_add_u64 v[178:179], s[36:37], 0, v[34:35]
	s_mov_b32 m0, s62
	s_add_i32 s63, s62, 0x2000
	global_load_lds_dwordx4 v[178:179], off
	v_lshl_add_u64 v[178:179], s[36:37], 0, v[164:165]
	s_mov_b32 m0, s63
	v_lshl_add_u64 v[192:193], s[30:31], 0, v[168:169]
	global_load_lds_dwordx4 v[178:179], off
	v_lshl_add_u64 v[178:179], v[192:193], 0, s[28:29]
	s_mov_b32 m0, s41
	v_lshl_add_u64 v[194:195], s[30:31], 0, v[166:167]
	global_load_lds_dwordx4 v[178:179], off
	v_lshl_add_u64 v[178:179], v[194:195], 0, s[28:29]
	s_mov_b32 m0, s42
	s_nop 0
	global_load_lds_dwordx4 v[178:179], off
	s_waitcnt vmcnt(8)
	s_waitcnt lgkmcnt(0)
	s_barrier
	v_mfma_f32_16x16x128_f8f6f4 v[96:99], v[26:33], v[200:207], 0
	s_setprio 1
	v_mfma_f32_16x16x128_f8f6f4 v[92:95], v[18:25], v[200:207], 0
	v_mfma_f32_16x16x128_f8f6f4 v[84:87], v[18:25], v[222:229], 0
	v_mfma_f32_16x16x128_f8f6f4 v[88:91], v[26:33], v[222:229], 0
	v_mfma_f32_16x16x128_f8f6f4 v[80:83], v[26:33], v[230:237], 0
	v_mfma_f32_16x16x128_f8f6f4 v[76:79], v[18:25], v[230:237], 0
	v_mfma_f32_16x16x128_f8f6f4 v[68:71], v[18:25], v[238:245], 0
	v_mfma_f32_16x16x128_f8f6f4 v[72:75], v[26:33], v[238:245], 0
	s_setprio 0
	s_setprio 1
	v_mfma_f32_16x16x128_f8f6f4 v[64:67], v[10:17], v[200:207], 0
	v_mfma_f32_16x16x128_f8f6f4 v[60:63], v[2:9], v[200:207], 0
	v_mfma_f32_16x16x128_f8f6f4 v[52:55], v[2:9], v[222:229], 0
	v_mfma_f32_16x16x128_f8f6f4 v[56:59], v[10:17], v[222:229], 0
	v_mfma_f32_16x16x128_f8f6f4 v[48:51], v[10:17], v[230:237], 0
	v_mfma_f32_16x16x128_f8f6f4 v[44:47], v[2:9], v[230:237], 0
	v_mfma_f32_16x16x128_f8f6f4 v[36:39], v[2:9], v[238:245], 0
	s_barrier
	v_mfma_f32_16x16x128_f8f6f4 v[40:43], v[10:17], v[238:245], 0
	s_setprio 0
	s_add_i32 s64, 0, 0x18000
	s_add_i32 s66, 0, 0x1c000
	v_add_u32_e32 v200, s64, v196
	v_add_u32_e32 v201, s66, v196
	ds_read_b128 v[26:29], v200
	ds_read_b128 v[30:33], v200 offset:1024
	ds_read_b128 v[18:21], v200 offset:2048
	ds_read_b128 v[22:25], v200 offset:3072
	ds_read_b128 v[10:13], v201
	ds_read_b128 v[14:17], v201 offset:1024
	ds_read_b128 v[2:5], v201 offset:2048
	ds_read_b128 v[6:9], v201 offset:3072
	s_add_u32 s36, s30, 0x20100
	s_addc_u32 s37, s31, 0
	s_mov_b32 m0, s43
	v_lshl_add_u64 v[178:179], s[36:37], 0, v[168:169]
	ds_read_b128 v[202:205], v197 offset:32768
	ds_read_b128 v[206:209], v197 offset:33792
	ds_read_b128 v[222:225], v197 offset:34816
	ds_read_b128 v[226:229], v197 offset:35840
	ds_read_b128 v[230:233], v197 offset:36864
	ds_read_b128 v[234:237], v197 offset:37888
	ds_read_b128 v[238:241], v197 offset:38912
	ds_read_b128 v[242:245], v197 offset:39936
	global_load_lds_dwordx4 v[178:179], off
	v_lshl_add_u64 v[178:179], s[36:37], 0, v[166:167]
	s_mov_b32 m0, s44
	s_nop 0
	global_load_lds_dwordx4 v[178:179], off
	s_waitcnt vmcnt(8)
	s_waitcnt lgkmcnt(0)
	s_barrier
	v_mfma_f32_16x16x128_f8f6f4 v[160:163], v[26:33], v[202:209], v[160:163]
	s_setprio 1
	v_mfma_f32_16x16x128_f8f6f4 v[156:159], v[18:25], v[202:209], v[156:159]
	v_mfma_f32_16x16x128_f8f6f4 v[148:151], v[18:25], v[222:229], v[148:151]
	v_mfma_f32_16x16x128_f8f6f4 v[152:155], v[26:33], v[222:229], v[152:155]
	v_mfma_f32_16x16x128_f8f6f4 v[144:147], v[26:33], v[230:237], v[144:147]
	v_mfma_f32_16x16x128_f8f6f4 v[140:143], v[18:25], v[230:237], v[140:143]
	v_mfma_f32_16x16x128_f8f6f4 v[132:135], v[18:25], v[238:245], v[132:135]
	v_mfma_f32_16x16x128_f8f6f4 v[136:139], v[26:33], v[238:245], v[136:139]
	s_setprio 0
	s_setprio 1
	v_mfma_f32_16x16x128_f8f6f4 v[128:131], v[10:17], v[202:209], v[128:131]
	v_mfma_f32_16x16x128_f8f6f4 v[124:127], v[2:9], v[202:209], v[124:127]
	v_mfma_f32_16x16x128_f8f6f4 v[116:119], v[2:9], v[222:229], v[116:119]
	v_mfma_f32_16x16x128_f8f6f4 v[120:123], v[10:17], v[222:229], v[120:123]
	v_mfma_f32_16x16x128_f8f6f4 v[112:115], v[10:17], v[230:237], v[112:115]
	v_mfma_f32_16x16x128_f8f6f4 v[108:111], v[2:9], v[230:237], v[108:111]
	v_mfma_f32_16x16x128_f8f6f4 v[100:103], v[2:9], v[238:245], v[100:103]
	s_barrier
	v_mfma_f32_16x16x128_f8f6f4 v[104:107], v[10:17], v[238:245], v[104:107]
	s_setprio 0
	s_add_i32 s64, s64, s40
	s_mov_b64 s[24:25], 0x180
	s_add_i32 s65, s64, 0x2000
	v_lshl_add_u64 v[174:175], v[174:175], 0, s[24:25]
	s_mov_b32 m0, s64
	s_add_u32 s36, s22, 0x20180
	ds_read_b128 v[202:205], v197 offset:49152
	ds_read_b128 v[206:209], v197 offset:50176
	ds_read_b128 v[222:225], v197 offset:51200
	ds_read_b128 v[226:229], v197 offset:52224
	ds_read_b128 v[230:233], v197 offset:53248
	ds_read_b128 v[234:237], v197 offset:54272
	ds_read_b128 v[238:241], v197 offset:55296
	ds_read_b128 v[242:245], v197 offset:56320
	global_load_lds_dwordx4 v[174:175], off
	v_lshl_add_u64 v[174:175], v[190:191], 0, s[24:25]
	s_mov_b32 m0, s65
	s_addc_u32 s37, s23, 0
	s_add_i32 s66, s66, s40
	global_load_lds_dwordx4 v[174:175], off
	v_lshl_add_u64 v[174:175], s[36:37], 0, v[34:35]
	s_mov_b32 m0, s66
	s_add_i32 s67, s66, 0x2000
	global_load_lds_dwordx4 v[174:175], off
	v_lshl_add_u64 v[174:175], s[36:37], 0, v[164:165]
	s_mov_b32 m0, s67
	s_nop 0
	global_load_lds_dwordx4 v[174:175], off
	v_lshl_add_u64 v[174:175], v[192:193], 0, s[24:25]
	s_mov_b32 m0, s47
	s_nop 0
	global_load_lds_dwordx4 v[174:175], off
	v_lshl_add_u64 v[174:175], v[194:195], 0, s[24:25]
	s_mov_b32 m0, s48
	s_nop 0
	global_load_lds_dwordx4 v[174:175], off
	s_waitcnt vmcnt(8)
	s_waitcnt lgkmcnt(0)
	s_barrier
	v_mfma_f32_16x16x128_f8f6f4 v[96:99], v[26:33], v[202:209], v[96:99]
	s_setprio 1
	v_mfma_f32_16x16x128_f8f6f4 v[92:95], v[18:25], v[202:209], v[92:95]
	v_mfma_f32_16x16x128_f8f6f4 v[84:87], v[18:25], v[222:229], v[84:87]
	v_mfma_f32_16x16x128_f8f6f4 v[88:91], v[26:33], v[222:229], v[88:91]
	v_mfma_f32_16x16x128_f8f6f4 v[80:83], v[26:33], v[230:237], v[80:83]
	v_mfma_f32_16x16x128_f8f6f4 v[76:79], v[18:25], v[230:237], v[76:79]
	v_mfma_f32_16x16x128_f8f6f4 v[68:71], v[18:25], v[238:245], v[68:71]
	v_mfma_f32_16x16x128_f8f6f4 v[72:75], v[26:33], v[238:245], v[72:75]
	s_setprio 0
	s_setprio 1
	v_mfma_f32_16x16x128_f8f6f4 v[64:67], v[10:17], v[202:209], v[64:67]
	v_mfma_f32_16x16x128_f8f6f4 v[60:63], v[2:9], v[202:209], v[60:63]
	v_mfma_f32_16x16x128_f8f6f4 v[52:55], v[2:9], v[222:229], v[52:55]
	v_mfma_f32_16x16x128_f8f6f4 v[56:59], v[10:17], v[222:229], v[56:59]
	v_mfma_f32_16x16x128_f8f6f4 v[48:51], v[10:17], v[230:237], v[48:51]
	v_mfma_f32_16x16x128_f8f6f4 v[44:47], v[2:9], v[230:237], v[44:47]
	v_mfma_f32_16x16x128_f8f6f4 v[36:39], v[2:9], v[238:245], v[36:39]
	s_barrier
	v_mfma_f32_16x16x128_f8f6f4 v[40:43], v[10:17], v[238:245], v[40:43]
	s_setprio 0
	s_add_u32 s30, s30, 0x20180
	s_addc_u32 s31, s31, 0
	s_add_u32 s68, s22, 0x200
	s_addc_u32 s69, s23, 0
	s_mov_b32 s70, 0
.LBB0_1087:
	ds_read_b128 v[2:5], v198
	ds_read_b128 v[6:9], v198 offset:1024
	ds_read_b128 v[10:13], v198 offset:2048
	ds_read_b128 v[14:17], v198 offset:3072
	ds_read_b128 v[18:21], v199
	ds_read_b128 v[22:25], v199 offset:1024
	ds_read_b128 v[26:29], v199 offset:2048
	ds_read_b128 v[30:33], v199 offset:3072
	s_add_u32 s14, s30, 0xfffe0080
	s_addc_u32 s22, s31, -1
	s_cmp_eq_u32 s70, 4
	s_cselect_b32 s37, s54, s22
	s_cselect_b32 s36, s55, s14
	s_cselect_b32 s23, s56, s69
	s_cselect_b32 s22, s57, s68
	s_mov_b32 m0, s58
	v_lshl_add_u64 v[174:175], s[30:31], 0, v[170:171]
	ds_read_b128 v[202:205], v197
	ds_read_b128 v[206:209], v197 offset:1024
	ds_read_b128 v[222:225], v197 offset:2048
	ds_read_b128 v[226:229], v197 offset:3072
	ds_read_b128 v[230:233], v197 offset:4096
	ds_read_b128 v[234:237], v197 offset:5120
	ds_read_b128 v[238:241], v197 offset:6144
	ds_read_b128 v[242:245], v197 offset:7168
	global_load_lds_dwordx4 v[174:175], off
	v_lshl_add_u64 v[174:175], s[30:31], 0, v[172:173]
	s_mov_b32 m0, s59
	s_nop 0
	global_load_lds_dwordx4 v[174:175], off
	s_waitcnt vmcnt(8)
	s_waitcnt lgkmcnt(0)
	s_barrier
	v_mfma_f32_16x16x128_f8f6f4 v[160:163], v[2:9], v[202:209], v[160:163]
	s_setprio 1
	v_mfma_f32_16x16x128_f8f6f4 v[156:159], v[10:17], v[202:209], v[156:159]
	v_mfma_f32_16x16x128_f8f6f4 v[148:151], v[10:17], v[222:229], v[148:151]
	v_mfma_f32_16x16x128_f8f6f4 v[152:155], v[2:9], v[222:229], v[152:155]
	v_mfma_f32_16x16x128_f8f6f4 v[144:147], v[2:9], v[230:237], v[144:147]
	v_mfma_f32_16x16x128_f8f6f4 v[140:143], v[10:17], v[230:237], v[140:143]
	v_mfma_f32_16x16x128_f8f6f4 v[132:135], v[10:17], v[238:245], v[132:135]
	v_mfma_f32_16x16x128_f8f6f4 v[136:139], v[2:9], v[238:245], v[136:139]
	s_setprio 0
	s_setprio 1
	v_mfma_f32_16x16x128_f8f6f4 v[128:131], v[18:25], v[202:209], v[128:131]
	v_mfma_f32_16x16x128_f8f6f4 v[124:127], v[26:33], v[202:209], v[124:127]
	v_mfma_f32_16x16x128_f8f6f4 v[116:119], v[26:33], v[222:229], v[116:119]
	v_mfma_f32_16x16x128_f8f6f4 v[120:123], v[18:25], v[222:229], v[120:123]
	v_mfma_f32_16x16x128_f8f6f4 v[112:115], v[18:25], v[230:237], v[112:115]
	v_mfma_f32_16x16x128_f8f6f4 v[108:111], v[26:33], v[230:237], v[108:111]
	v_mfma_f32_16x16x128_f8f6f4 v[100:103], v[26:33], v[238:245], v[100:103]
	s_barrier
	v_mfma_f32_16x16x128_f8f6f4 v[104:107], v[18:25], v[238:245], v[104:107]
	s_setprio 0
	s_mov_b32 m0, s60
	v_lshl_add_u64 v[174:175], s[22:23], 0, v[34:35]
	s_add_u32 s72, s22, 0x20000
	ds_read_b128 v[202:205], v197 offset:16384
	ds_read_b128 v[206:209], v197 offset:17408
	ds_read_b128 v[222:225], v197 offset:18432
	ds_read_b128 v[226:229], v197 offset:19456
	ds_read_b128 v[230:233], v197 offset:20480
	ds_read_b128 v[234:237], v197 offset:21504
	ds_read_b128 v[238:241], v197 offset:22528
	ds_read_b128 v[242:245], v197 offset:23552
	global_load_lds_dwordx4 v[174:175], off
	v_lshl_add_u64 v[190:191], s[22:23], 0, v[164:165]
	s_mov_b32 m0, s61
	s_addc_u32 s73, s23, 0
	global_load_lds_dwordx4 v[190:191], off
	v_lshl_add_u64 v[178:179], s[72:73], 0, v[34:35]
	s_mov_b32 m0, s62
	v_lshl_add_u64 v[192:193], s[36:37], 0, v[168:169]
	global_load_lds_dwordx4 v[178:179], off
	v_lshl_add_u64 v[178:179], s[72:73], 0, v[164:165]
	s_mov_b32 m0, s63
	v_lshl_add_u64 v[194:195], s[36:37], 0, v[166:167]
	global_load_lds_dwordx4 v[178:179], off
	s_mov_b32 m0, s41
	s_nop 0
	global_load_lds_dwordx4 v[192:193], off
	s_mov_b32 m0, s42
	s_nop 0
	global_load_lds_dwordx4 v[194:195], off
	s_waitcnt vmcnt(8)
	s_waitcnt lgkmcnt(0)
	s_barrier
	v_mfma_f32_16x16x128_f8f6f4 v[96:99], v[2:9], v[202:209], v[96:99]
	s_setprio 1
	v_mfma_f32_16x16x128_f8f6f4 v[92:95], v[10:17], v[202:209], v[92:95]
	v_mfma_f32_16x16x128_f8f6f4 v[84:87], v[10:17], v[222:229], v[84:87]
	v_mfma_f32_16x16x128_f8f6f4 v[88:91], v[2:9], v[222:229], v[88:91]
	v_mfma_f32_16x16x128_f8f6f4 v[80:83], v[2:9], v[230:237], v[80:83]
	v_mfma_f32_16x16x128_f8f6f4 v[76:79], v[10:17], v[230:237], v[76:79]
	v_mfma_f32_16x16x128_f8f6f4 v[68:71], v[10:17], v[238:245], v[68:71]
	v_mfma_f32_16x16x128_f8f6f4 v[72:75], v[2:9], v[238:245], v[72:75]
	s_setprio 0
	s_setprio 1
	v_mfma_f32_16x16x128_f8f6f4 v[64:67], v[18:25], v[202:209], v[64:67]
	v_mfma_f32_16x16x128_f8f6f4 v[60:63], v[26:33], v[202:209], v[60:63]
	v_mfma_f32_16x16x128_f8f6f4 v[52:55], v[26:33], v[222:229], v[52:55]
	v_mfma_f32_16x16x128_f8f6f4 v[56:59], v[18:25], v[222:229], v[56:59]
	v_mfma_f32_16x16x128_f8f6f4 v[48:51], v[18:25], v[230:237], v[48:51]
	v_mfma_f32_16x16x128_f8f6f4 v[44:47], v[26:33], v[230:237], v[44:47]
	v_mfma_f32_16x16x128_f8f6f4 v[36:39], v[26:33], v[238:245], v[36:39]
	s_barrier
	v_mfma_f32_16x16x128_f8f6f4 v[40:43], v[18:25], v[238:245], v[40:43]
	s_setprio 0
	ds_read_b128 v[26:29], v200
	ds_read_b128 v[30:33], v200 offset:1024
	ds_read_b128 v[18:21], v200 offset:2048
	ds_read_b128 v[22:25], v200 offset:3072
	ds_read_b128 v[10:13], v201
	ds_read_b128 v[14:17], v201 offset:1024
	ds_read_b128 v[2:5], v201 offset:2048
	ds_read_b128 v[6:9], v201 offset:3072
	s_add_u32 s36, s36, 0x20000
	s_addc_u32 s37, s37, 0
	s_mov_b32 m0, s43
	v_lshl_add_u64 v[178:179], s[36:37], 0, v[168:169]
	ds_read_b128 v[202:205], v197 offset:32768
	ds_read_b128 v[206:209], v197 offset:33792
	ds_read_b128 v[222:225], v197 offset:34816
	ds_read_b128 v[226:229], v197 offset:35840
	ds_read_b128 v[230:233], v197 offset:36864
	ds_read_b128 v[234:237], v197 offset:37888
	ds_read_b128 v[238:241], v197 offset:38912
	ds_read_b128 v[242:245], v197 offset:39936
	global_load_lds_dwordx4 v[178:179], off
	v_lshl_add_u64 v[178:179], s[36:37], 0, v[166:167]
	s_mov_b32 m0, s44
	s_nop 0
	global_load_lds_dwordx4 v[178:179], off
	s_waitcnt vmcnt(8)
	s_waitcnt lgkmcnt(0)
	s_barrier
	v_mfma_f32_16x16x128_f8f6f4 v[160:163], v[26:33], v[202:209], v[160:163]
	s_setprio 1
	v_mfma_f32_16x16x128_f8f6f4 v[156:159], v[18:25], v[202:209], v[156:159]
	v_mfma_f32_16x16x128_f8f6f4 v[148:151], v[18:25], v[222:229], v[148:151]
	v_mfma_f32_16x16x128_f8f6f4 v[152:155], v[26:33], v[222:229], v[152:155]
	v_mfma_f32_16x16x128_f8f6f4 v[144:147], v[26:33], v[230:237], v[144:147]
	v_mfma_f32_16x16x128_f8f6f4 v[140:143], v[18:25], v[230:237], v[140:143]
	v_mfma_f32_16x16x128_f8f6f4 v[132:135], v[18:25], v[238:245], v[132:135]
	v_mfma_f32_16x16x128_f8f6f4 v[136:139], v[26:33], v[238:245], v[136:139]
	s_setprio 0
	s_setprio 1
	v_mfma_f32_16x16x128_f8f6f4 v[128:131], v[10:17], v[202:209], v[128:131]
	v_mfma_f32_16x16x128_f8f6f4 v[124:127], v[2:9], v[202:209], v[124:127]
	v_mfma_f32_16x16x128_f8f6f4 v[116:119], v[2:9], v[222:229], v[116:119]
	v_mfma_f32_16x16x128_f8f6f4 v[120:123], v[10:17], v[222:229], v[120:123]
	v_mfma_f32_16x16x128_f8f6f4 v[112:115], v[10:17], v[230:237], v[112:115]
	v_mfma_f32_16x16x128_f8f6f4 v[108:111], v[2:9], v[230:237], v[108:111]
	v_mfma_f32_16x16x128_f8f6f4 v[100:103], v[2:9], v[238:245], v[100:103]
	s_barrier
	v_mfma_f32_16x16x128_f8f6f4 v[104:107], v[10:17], v[238:245], v[104:107]
	s_setprio 0
	s_mov_b32 m0, s64
	v_lshl_add_u64 v[174:175], v[174:175], 0, s[18:19]
	s_add_u32 s22, s22, 0x20080
	ds_read_b128 v[202:205], v197 offset:49152
	ds_read_b128 v[206:209], v197 offset:50176
	ds_read_b128 v[222:225], v197 offset:51200
	ds_read_b128 v[226:229], v197 offset:52224
	ds_read_b128 v[230:233], v197 offset:53248
	ds_read_b128 v[234:237], v197 offset:54272
	ds_read_b128 v[238:241], v197 offset:55296
	ds_read_b128 v[242:245], v197 offset:56320
	global_load_lds_dwordx4 v[174:175], off
	v_lshl_add_u64 v[174:175], v[190:191], 0, s[18:19]
	s_mov_b32 m0, s65
	s_addc_u32 s23, s23, 0
	global_load_lds_dwordx4 v[174:175], off
	v_lshl_add_u64 v[174:175], s[22:23], 0, v[34:35]
	s_mov_b32 m0, s66
	s_nop 0
	global_load_lds_dwordx4 v[174:175], off
	v_lshl_add_u64 v[174:175], s[22:23], 0, v[164:165]
	s_mov_b32 m0, s67
	s_nop 0
	global_load_lds_dwordx4 v[174:175], off
	v_lshl_add_u64 v[174:175], v[192:193], 0, s[18:19]
	s_mov_b32 m0, s47
	s_nop 0
	global_load_lds_dwordx4 v[174:175], off
	v_lshl_add_u64 v[174:175], v[194:195], 0, s[18:19]
	s_mov_b32 m0, s48
	s_nop 0
	global_load_lds_dwordx4 v[174:175], off
	s_waitcnt vmcnt(8)
	s_waitcnt lgkmcnt(0)
	s_barrier
	v_mfma_f32_16x16x128_f8f6f4 v[96:99], v[26:33], v[202:209], v[96:99]
	s_setprio 1
	v_mfma_f32_16x16x128_f8f6f4 v[92:95], v[18:25], v[202:209], v[92:95]
	v_mfma_f32_16x16x128_f8f6f4 v[84:87], v[18:25], v[222:229], v[84:87]
	v_mfma_f32_16x16x128_f8f6f4 v[88:91], v[26:33], v[222:229], v[88:91]
	v_mfma_f32_16x16x128_f8f6f4 v[80:83], v[26:33], v[230:237], v[80:83]
	v_mfma_f32_16x16x128_f8f6f4 v[76:79], v[18:25], v[230:237], v[76:79]
	v_mfma_f32_16x16x128_f8f6f4 v[68:71], v[18:25], v[238:245], v[68:71]
	v_mfma_f32_16x16x128_f8f6f4 v[72:75], v[26:33], v[238:245], v[72:75]
	s_setprio 0
	s_setprio 1
	v_mfma_f32_16x16x128_f8f6f4 v[64:67], v[10:17], v[202:209], v[64:67]
	v_mfma_f32_16x16x128_f8f6f4 v[60:63], v[2:9], v[202:209], v[60:63]
	v_mfma_f32_16x16x128_f8f6f4 v[52:55], v[2:9], v[222:229], v[52:55]
	v_mfma_f32_16x16x128_f8f6f4 v[56:59], v[10:17], v[222:229], v[56:59]
	v_mfma_f32_16x16x128_f8f6f4 v[48:51], v[10:17], v[230:237], v[48:51]
	v_mfma_f32_16x16x128_f8f6f4 v[44:47], v[2:9], v[230:237], v[44:47]
	v_mfma_f32_16x16x128_f8f6f4 v[36:39], v[2:9], v[238:245], v[36:39]
	s_barrier
	v_mfma_f32_16x16x128_f8f6f4 v[40:43], v[10:17], v[238:245], v[40:43]
	s_setprio 0
	s_add_i32 s70, s70, 2
	s_add_u32 s30, s30, 0x100
	s_addc_u32 s31, s31, 0
	s_add_u32 s68, s68, 0x100
	s_addc_u32 s69, s69, 0
	s_cmp_gt_u32 s70, 5
	s_cbranch_scc0 .LBB0_1087

.LBB0_1160:
	s_add_u32 s22, s30, 0x100
	s_addc_u32 s23, s31, 0
	s_add_i32 s65, 0, 0x10000
	s_cmp_eq_u32 s64, 18
	s_cselect_b32 s41, s58, s23
	s_cselect_b32 s40, s59, s22
	s_cselect_b32 s37, s60, s63
	s_cselect_b32 s36, s61, s62
	s_add_i32 s66, 0, 0x14000
	v_add_u32_e32 v2, s65, v222
	v_add_u32_e32 v6, s66, v222
	ds_read_b128 v[26:29], v2
	ds_read_b128 v[30:33], v2 offset:1024
	ds_read_b128 v[18:21], v2 offset:2048
	ds_read_b128 v[22:25], v2 offset:3072
	ds_read_b128 v[10:13], v6
	ds_read_b128 v[14:17], v6 offset:1024
	ds_read_b128 v[2:5], v6 offset:2048
	ds_read_b128 v[6:9], v6 offset:3072
	v_lshl_add_u64 v[174:175], s[30:31], 0, v[170:171]
	s_add_i32 m0, s43, 0xc000
	ds_read_b128 v[190:193], v223
	ds_read_b128 v[194:197], v223 offset:1024
	ds_read_b128 v[198:201], v223 offset:2048
	ds_read_b128 v[202:205], v223 offset:3072
	ds_read_b128 v[224:227], v223 offset:4096
	ds_read_b128 v[228:231], v223 offset:5120
	ds_read_b128 v[232:235], v223 offset:6144
	ds_read_b128 v[236:239], v223 offset:7168
	global_load_lds_dwordx4 v[174:175], off
	v_lshl_add_u64 v[174:175], s[30:31], 0, v[172:173]
	s_add_i32 m0, s43, 0xe000
	s_nop 0
	global_load_lds_dwordx4 v[174:175], off
	s_waitcnt vmcnt(8)
	s_waitcnt lgkmcnt(0)
	s_barrier
	v_mfma_f32_16x16x128_f8f6f4 v[160:163], v[26:33], v[190:197], v[160:163]
	s_setprio 1
	v_mfma_f32_16x16x128_f8f6f4 v[156:159], v[18:25], v[190:197], v[156:159]
	v_mfma_f32_16x16x128_f8f6f4 v[140:143], v[18:25], v[198:205], v[140:143]
	v_mfma_f32_16x16x128_f8f6f4 v[144:147], v[26:33], v[198:205], v[144:147]
	v_mfma_f32_16x16x128_f8f6f4 v[132:135], v[26:33], v[224:231], v[132:135]
	v_mfma_f32_16x16x128_f8f6f4 v[124:127], v[18:25], v[224:231], v[124:127]
	v_mfma_f32_16x16x128_f8f6f4 v[108:111], v[18:25], v[232:239], v[108:111]
	v_mfma_f32_16x16x128_f8f6f4 v[116:119], v[26:33], v[232:239], v[116:119]
	s_setprio 0
	s_setprio 1
	v_mfma_f32_16x16x128_f8f6f4 v[152:155], v[10:17], v[190:197], v[152:155]
	v_mfma_f32_16x16x128_f8f6f4 v[148:151], v[2:9], v[190:197], v[148:151]
	v_mfma_f32_16x16x128_f8f6f4 v[128:131], v[2:9], v[198:205], v[128:131]
	v_mfma_f32_16x16x128_f8f6f4 v[136:139], v[10:17], v[198:205], v[136:139]
	v_mfma_f32_16x16x128_f8f6f4 v[120:123], v[10:17], v[224:231], v[120:123]
	v_mfma_f32_16x16x128_f8f6f4 v[112:115], v[2:9], v[224:231], v[112:115]
	v_mfma_f32_16x16x128_f8f6f4 v[100:103], v[2:9], v[232:239], v[100:103]
	s_barrier
	v_mfma_f32_16x16x128_f8f6f4 v[104:107], v[10:17], v[232:239], v[104:107]
	s_setprio 0
	s_add_i32 s14, s65, s42
	v_lshl_add_u64 v[174:175], s[36:37], 0, v[34:35]
	s_mov_b32 m0, s14
	ds_read_b128 v[196:199], v223 offset:16384
	ds_read_b128 v[200:203], v223 offset:17408
	ds_read_b128 v[204:207], v223 offset:18432
	ds_read_b128 v[208:211], v223 offset:19456
	ds_read_b128 v[224:227], v223 offset:20480
	ds_read_b128 v[228:231], v223 offset:21504
	ds_read_b128 v[232:235], v223 offset:22528
	ds_read_b128 v[236:239], v223 offset:23552
	global_load_lds_dwordx4 v[174:175], off
	s_add_i32 m0, s14, 0x2000
	s_add_u32 s30, s36, 0x58000
	v_lshl_add_u64 v[190:191], s[36:37], 0, v[164:165]
	s_addc_u32 s31, s37, 0
	s_add_i32 s14, s66, s42
	global_load_lds_dwordx4 v[190:191], off
	v_lshl_add_u64 v[178:179], s[30:31], 0, v[34:35]
	s_mov_b32 m0, s14
	v_lshl_add_u64 v[192:193], s[40:41], 0, v[168:169]
	global_load_lds_dwordx4 v[178:179], off
	v_lshl_add_u64 v[178:179], s[30:31], 0, v[164:165]
	s_add_i32 m0, s14, 0x2000
	v_lshl_add_u64 v[194:195], s[40:41], 0, v[166:167]
	global_load_lds_dwordx4 v[178:179], off
	s_mov_b32 m0, s43
	s_nop 0
	global_load_lds_dwordx4 v[192:193], off
	s_mov_b32 m0, s44
	s_nop 0
	global_load_lds_dwordx4 v[194:195], off
	s_waitcnt vmcnt(8)
	s_waitcnt lgkmcnt(0)
	s_barrier
	v_mfma_f32_16x16x128_f8f6f4 v[96:99], v[26:33], v[196:203], v[96:99]
	s_setprio 1
	v_mfma_f32_16x16x128_f8f6f4 v[92:95], v[18:25], v[196:203], v[92:95]
	v_mfma_f32_16x16x128_f8f6f4 v[76:79], v[18:25], v[204:211], v[76:79]
	v_mfma_f32_16x16x128_f8f6f4 v[84:87], v[26:33], v[204:211], v[84:87]
	v_mfma_f32_16x16x128_f8f6f4 v[68:71], v[26:33], v[224:231], v[68:71]
	v_mfma_f32_16x16x128_f8f6f4 v[60:63], v[18:25], v[224:231], v[60:63]
	v_mfma_f32_16x16x128_f8f6f4 v[44:47], v[18:25], v[232:239], v[44:47]
	v_mfma_f32_16x16x128_f8f6f4 v[52:55], v[26:33], v[232:239], v[52:55]
	s_setprio 0
	s_setprio 1
	v_mfma_f32_16x16x128_f8f6f4 v[88:91], v[10:17], v[196:203], v[88:91]
	v_mfma_f32_16x16x128_f8f6f4 v[80:83], v[2:9], v[196:203], v[80:83]
	v_mfma_f32_16x16x128_f8f6f4 v[64:67], v[2:9], v[204:211], v[64:67]
	v_mfma_f32_16x16x128_f8f6f4 v[72:75], v[10:17], v[204:211], v[72:75]
	v_mfma_f32_16x16x128_f8f6f4 v[56:59], v[10:17], v[224:231], v[56:59]
	v_mfma_f32_16x16x128_f8f6f4 v[48:51], v[2:9], v[224:231], v[48:51]
	v_mfma_f32_16x16x128_f8f6f4 v[36:39], v[2:9], v[232:239], v[36:39]
	s_barrier
	v_mfma_f32_16x16x128_f8f6f4 v[40:43], v[10:17], v[232:239], v[40:43]
	s_setprio 0
	s_add_i32 s14, 0, 0x18000
	s_add_i32 s65, 0, 0x1c000
	v_add_u32_e32 v14, s14, v222
	v_add_u32_e32 v30, s65, v222
	ds_read_b128 v[2:5], v14
	ds_read_b128 v[6:9], v14 offset:1024
	ds_read_b128 v[10:13], v14 offset:2048
	ds_read_b128 v[14:17], v14 offset:3072
	ds_read_b128 v[18:21], v30
	ds_read_b128 v[22:25], v30 offset:1024
	ds_read_b128 v[26:29], v30 offset:2048
	ds_read_b128 v[30:33], v30 offset:3072
	s_add_u32 s30, s40, 0x58000
	s_addc_u32 s31, s41, 0
	s_mov_b32 m0, s45
	v_lshl_add_u64 v[178:179], s[30:31], 0, v[168:169]
	ds_read_b128 v[196:199], v223 offset:32768
	ds_read_b128 v[200:203], v223 offset:33792
	ds_read_b128 v[204:207], v223 offset:34816
	ds_read_b128 v[208:211], v223 offset:35840
	ds_read_b128 v[224:227], v223 offset:36864
	ds_read_b128 v[228:231], v223 offset:37888
	ds_read_b128 v[232:235], v223 offset:38912
	ds_read_b128 v[236:239], v223 offset:39936
	global_load_lds_dwordx4 v[178:179], off
	v_lshl_add_u64 v[178:179], s[30:31], 0, v[166:167]
	s_mov_b32 m0, s46
	s_nop 0
	global_load_lds_dwordx4 v[178:179], off
	s_waitcnt vmcnt(8)
	s_waitcnt lgkmcnt(0)
	s_barrier
	v_mfma_f32_16x16x128_f8f6f4 v[160:163], v[2:9], v[196:203], v[160:163]
	s_setprio 1
	v_mfma_f32_16x16x128_f8f6f4 v[156:159], v[10:17], v[196:203], v[156:159]
	v_mfma_f32_16x16x128_f8f6f4 v[140:143], v[10:17], v[204:211], v[140:143]
	v_mfma_f32_16x16x128_f8f6f4 v[144:147], v[2:9], v[204:211], v[144:147]
	v_mfma_f32_16x16x128_f8f6f4 v[132:135], v[2:9], v[224:231], v[132:135]
	v_mfma_f32_16x16x128_f8f6f4 v[124:127], v[10:17], v[224:231], v[124:127]
	v_mfma_f32_16x16x128_f8f6f4 v[108:111], v[10:17], v[232:239], v[108:111]
	v_mfma_f32_16x16x128_f8f6f4 v[116:119], v[2:9], v[232:239], v[116:119]
	s_setprio 0
	s_setprio 1
	v_mfma_f32_16x16x128_f8f6f4 v[152:155], v[18:25], v[196:203], v[152:155]
	v_mfma_f32_16x16x128_f8f6f4 v[148:151], v[26:33], v[196:203], v[148:151]
	v_mfma_f32_16x16x128_f8f6f4 v[128:131], v[26:33], v[204:211], v[128:131]
	v_mfma_f32_16x16x128_f8f6f4 v[136:139], v[18:25], v[204:211], v[136:139]
	v_mfma_f32_16x16x128_f8f6f4 v[120:123], v[18:25], v[224:231], v[120:123]
	v_mfma_f32_16x16x128_f8f6f4 v[112:115], v[26:33], v[224:231], v[112:115]
	v_mfma_f32_16x16x128_f8f6f4 v[100:103], v[26:33], v[232:239], v[100:103]
	s_barrier
	v_mfma_f32_16x16x128_f8f6f4 v[104:107], v[18:25], v[232:239], v[104:107]
	s_setprio 0
	s_add_i32 s14, s14, s42
	v_lshl_add_u64 v[174:175], v[174:175], 0, s[18:19]
	s_mov_b32 m0, s14
	ds_read_b128 v[196:199], v223 offset:49152
	ds_read_b128 v[200:203], v223 offset:50176
	ds_read_b128 v[204:207], v223 offset:51200
	ds_read_b128 v[208:211], v223 offset:52224
	ds_read_b128 v[224:227], v223 offset:53248
	ds_read_b128 v[228:231], v223 offset:54272
	ds_read_b128 v[232:235], v223 offset:55296
	ds_read_b128 v[236:239], v223 offset:56320
	global_load_lds_dwordx4 v[174:175], off
	s_add_i32 m0, s14, 0x2000
	s_add_u32 s30, s36, 0x58080
	v_lshl_add_u64 v[174:175], v[190:191], 0, s[18:19]
	s_addc_u32 s31, s37, 0
	s_add_i32 s14, s65, s42
	global_load_lds_dwordx4 v[174:175], off
	v_lshl_add_u64 v[174:175], s[30:31], 0, v[34:35]
	s_mov_b32 m0, s14
	s_nop 0
	global_load_lds_dwordx4 v[174:175], off
	v_lshl_add_u64 v[174:175], s[30:31], 0, v[164:165]
	s_add_i32 m0, s14, 0x2000
	s_nop 0
	global_load_lds_dwordx4 v[174:175], off
	v_lshl_add_u64 v[174:175], v[192:193], 0, s[18:19]
	s_mov_b32 m0, s51
	s_nop 0
	global_load_lds_dwordx4 v[174:175], off
	v_lshl_add_u64 v[174:175], v[194:195], 0, s[18:19]
	s_mov_b32 m0, s52
	s_nop 0
	global_load_lds_dwordx4 v[174:175], off
	s_waitcnt vmcnt(8)
	s_waitcnt lgkmcnt(0)
	s_barrier
	v_mfma_f32_16x16x128_f8f6f4 v[96:99], v[2:9], v[196:203], v[96:99]
	s_setprio 1
	v_mfma_f32_16x16x128_f8f6f4 v[92:95], v[10:17], v[196:203], v[92:95]
	v_mfma_f32_16x16x128_f8f6f4 v[76:79], v[10:17], v[204:211], v[76:79]
	v_mfma_f32_16x16x128_f8f6f4 v[84:87], v[2:9], v[204:211], v[84:87]
	v_mfma_f32_16x16x128_f8f6f4 v[68:71], v[2:9], v[224:231], v[68:71]
	v_mfma_f32_16x16x128_f8f6f4 v[60:63], v[10:17], v[224:231], v[60:63]
	v_mfma_f32_16x16x128_f8f6f4 v[44:47], v[10:17], v[232:239], v[44:47]
	v_mfma_f32_16x16x128_f8f6f4 v[52:55], v[2:9], v[232:239], v[52:55]
	s_setprio 0
	s_setprio 1
	v_mfma_f32_16x16x128_f8f6f4 v[88:91], v[18:25], v[196:203], v[88:91]
	v_mfma_f32_16x16x128_f8f6f4 v[80:83], v[26:33], v[196:203], v[80:83]
	v_mfma_f32_16x16x128_f8f6f4 v[64:67], v[26:33], v[204:211], v[64:67]
	v_mfma_f32_16x16x128_f8f6f4 v[72:75], v[18:25], v[204:211], v[72:75]
	v_mfma_f32_16x16x128_f8f6f4 v[56:59], v[18:25], v[224:231], v[56:59]
	v_mfma_f32_16x16x128_f8f6f4 v[48:51], v[26:33], v[224:231], v[48:51]
	v_mfma_f32_16x16x128_f8f6f4 v[36:39], v[26:33], v[232:239], v[36:39]
	s_barrier
	v_mfma_f32_16x16x128_f8f6f4 v[40:43], v[18:25], v[232:239], v[40:43]
	s_setprio 0
	s_add_i32 s64, s64, 2
	s_add_u32 s62, s62, 0x100
	s_addc_u32 s63, s63, 0
	s_cmp_gt_u32 s64, 19
	s_mov_b64 s[30:31], s[22:23]
	s_cbranch_scc0 .LBB0_1160
	s_and_b64 vcc, exec, s[8:9]
	s_mov_b32 s58, 0x19b00000
	v_readlane_b32 s59, v255, 10
	s_mov_b32 s60, 0xff61b1e6
	s_mov_b64 s[62:63], 0x800
	s_cbranch_vccz .LBB0_1163
	s_barrier
